# GEMM K-loop load segments: LDS-DMA issued before the fragment ds_reads (52 segments), on top of v056
# speedup vs baseline: 1.0021x; 1.0009x over previous
.LBB0_417:
	s_add_u32 s28, s6, 0xfffc0080
	s_addc_u32 s29, s7, -1
	s_add_i32 s43, 0, 0x10000
	s_cmp_eq_u32 s42, 12
	s_cselect_b32 s31, s5, s29
	s_cselect_b32 s30, s8, s28
	s_cselect_b32 s29, s9, s33
	s_cselect_b32 s28, s21, s23
	s_add_i32 s63, 0, 0x14000
	s_add_i32 m0, s45, 0xc000
	s_nop 0
	global_load_lds_dwordx4 v166, s[6:7]
	s_add_i32 m0, s45, 0xe000
	s_nop 0
	global_load_lds_dwordx4 v164, s[6:7]
	ds_read_b128 v[130:133], v165
	ds_read_b128 v[134:137], v165 offset:1024
	ds_read_b128 v[138:141], v165 offset:2048
	ds_read_b128 v[142:145], v165 offset:3072
	ds_read_b128 v[146:149], v165 offset:16384
	ds_read_b128 v[150:153], v165 offset:17408
	ds_read_b128 v[154:157], v165 offset:18432
	ds_read_b128 v[168:171], v165 offset:19456
	ds_read_b128 v[172:175], v188
	ds_read_b128 v[176:179], v188 offset:1024
	ds_read_b128 v[180:183], v188 offset:2048
	ds_read_b128 v[190:193], v188 offset:3072
	ds_read_b128 v[194:197], v188 offset:4096
	ds_read_b128 v[198:201], v188 offset:5120
	ds_read_b128 v[202:205], v188 offset:6144
	ds_read_b128 v[206:209], v188 offset:7168
	s_waitcnt vmcnt(8) lgkmcnt(0)
	s_barrier
	v_mfma_f32_16x16x32_bf16 v[126:129], v[130:133], v[172:175], v[126:129]
	v_mfma_f32_16x16x32_bf16 v[122:125], v[138:141], v[172:175], v[122:125]
	v_mfma_f32_16x16x32_bf16 v[114:117], v[130:133], v[180:183], v[114:117]
	v_mfma_f32_16x16x32_bf16 v[106:109], v[138:141], v[180:183], v[106:109]
	v_mfma_f32_16x16x32_bf16 v[98:101], v[130:133], v[194:197], v[98:101]
	v_mfma_f32_16x16x32_bf16 v[90:93], v[138:141], v[194:197], v[90:93]
	v_mfma_f32_16x16x32_bf16 v[82:85], v[130:133], v[202:205], v[82:85]
	v_mfma_f32_16x16x32_bf16 v[74:77], v[138:141], v[202:205], v[74:77]
	v_mfma_f32_16x16x32_bf16 v[126:129], v[134:137], v[176:179], v[126:129]
	v_mfma_f32_16x16x32_bf16 v[122:125], v[142:145], v[176:179], v[122:125]
	v_mfma_f32_16x16x32_bf16 v[114:117], v[134:137], v[190:193], v[114:117]
	v_mfma_f32_16x16x32_bf16 v[106:109], v[142:145], v[190:193], v[106:109]
	v_mfma_f32_16x16x32_bf16 v[98:101], v[134:137], v[198:201], v[98:101]
	v_mfma_f32_16x16x32_bf16 v[90:93], v[142:145], v[198:201], v[90:93]
	v_mfma_f32_16x16x32_bf16 v[82:85], v[134:137], v[206:209], v[82:85]
	v_mfma_f32_16x16x32_bf16 v[74:77], v[142:145], v[206:209], v[74:77]
	v_mfma_f32_16x16x32_bf16 v[118:121], v[146:149], v[172:175], v[118:121]
	v_mfma_f32_16x16x32_bf16 v[110:113], v[154:157], v[172:175], v[110:113]
	v_mfma_f32_16x16x32_bf16 v[102:105], v[146:149], v[180:183], v[102:105]
	v_mfma_f32_16x16x32_bf16 v[94:97], v[154:157], v[180:183], v[94:97]
	v_mfma_f32_16x16x32_bf16 v[86:89], v[146:149], v[194:197], v[86:89]
	v_mfma_f32_16x16x32_bf16 v[78:81], v[154:157], v[194:197], v[78:81]
	v_mfma_f32_16x16x32_bf16 v[70:73], v[146:149], v[202:205], v[70:73]
	v_mfma_f32_16x16x32_bf16 v[66:69], v[154:157], v[202:205], v[66:69]
	v_mfma_f32_16x16x32_bf16 v[118:121], v[150:153], v[176:179], v[118:121]
	v_mfma_f32_16x16x32_bf16 v[110:113], v[168:171], v[176:179], v[110:113]
	v_mfma_f32_16x16x32_bf16 v[102:105], v[150:153], v[190:193], v[102:105]
	v_mfma_f32_16x16x32_bf16 v[94:97], v[168:171], v[190:193], v[94:97]
	v_mfma_f32_16x16x32_bf16 v[86:89], v[150:153], v[198:201], v[86:89]
	v_mfma_f32_16x16x32_bf16 v[78:81], v[168:171], v[198:201], v[78:81]
	v_mfma_f32_16x16x32_bf16 v[70:73], v[150:153], v[206:209], v[70:73]
	v_mfma_f32_16x16x32_bf16 v[66:69], v[168:171], v[206:209], v[66:69]
	s_barrier
	s_add_i32 s43, s43, s44
	v_lshl_add_u64 v[216:217], s[28:29], 0, v[0:1]
	s_mov_b32 m0, s43
	s_nop 0
	global_load_lds_dwordx4 v0, s[28:29]
	s_add_i32 m0, s43, 0x2000
	s_add_u32 s58, s28, 0x40000
	v_lshl_add_u64 v[218:219], s[28:29], 0, v[158:159]
	s_addc_u32 s59, s29, 0
	s_add_i32 s43, s63, s44
	global_load_lds_dwordx4 v158, s[28:29]
	s_mov_b32 m0, s43
	v_lshl_add_u64 v[222:223], s[30:31], 0, v[160:161]
	global_load_lds_dwordx4 v0, s[58:59]
	s_add_i32 m0, s43, 0x2000
	s_nop 0
	global_load_lds_dwordx4 v158, s[58:59]
	s_mov_b32 m0, s45
	v_lshl_add_u64 v[220:221], s[30:31], 0, v[162:163]
	global_load_lds_dwordx4 v162, s[30:31]
	s_mov_b32 m0, s46
	s_nop 0
	global_load_lds_dwordx4 v160, s[30:31]
	ds_read_b128 v[172:175], v188 offset:16384
	ds_read_b128 v[176:179], v188 offset:17408
	ds_read_b128 v[180:183], v188 offset:18432
	ds_read_b128 v[190:193], v188 offset:19456
	ds_read_b128 v[194:197], v188 offset:20480
	ds_read_b128 v[198:201], v188 offset:21504
	ds_read_b128 v[202:205], v188 offset:22528
	ds_read_b128 v[206:209], v188 offset:23552
	s_waitcnt vmcnt(8) lgkmcnt(0)
	s_barrier
	v_mfma_f32_16x16x32_bf16 v[62:65], v[130:133], v[172:175], v[62:65]
	v_mfma_f32_16x16x32_bf16 v[58:61], v[138:141], v[172:175], v[58:61]
	v_mfma_f32_16x16x32_bf16 v[50:53], v[130:133], v[180:183], v[50:53]
	v_mfma_f32_16x16x32_bf16 v[42:45], v[138:141], v[180:183], v[42:45]
	v_mfma_f32_16x16x32_bf16 v[34:37], v[130:133], v[194:197], v[34:37]
	v_mfma_f32_16x16x32_bf16 v[26:29], v[138:141], v[194:197], v[26:29]
	v_mfma_f32_16x16x32_bf16 v[18:21], v[130:133], v[202:205], v[18:21]
	v_mfma_f32_16x16x32_bf16 v[10:13], v[138:141], v[202:205], v[10:13]
	v_mfma_f32_16x16x32_bf16 v[62:65], v[134:137], v[176:179], v[62:65]
	v_mfma_f32_16x16x32_bf16 v[58:61], v[142:145], v[176:179], v[58:61]
	v_mfma_f32_16x16x32_bf16 v[50:53], v[134:137], v[190:193], v[50:53]
	v_mfma_f32_16x16x32_bf16 v[42:45], v[142:145], v[190:193], v[42:45]
	v_mfma_f32_16x16x32_bf16 v[34:37], v[134:137], v[198:201], v[34:37]
	v_mfma_f32_16x16x32_bf16 v[26:29], v[142:145], v[198:201], v[26:29]
	v_mfma_f32_16x16x32_bf16 v[18:21], v[134:137], v[206:209], v[18:21]
	v_mfma_f32_16x16x32_bf16 v[10:13], v[142:145], v[206:209], v[10:13]
	v_mfma_f32_16x16x32_bf16 v[54:57], v[146:149], v[172:175], v[54:57]
	v_mfma_f32_16x16x32_bf16 v[46:49], v[154:157], v[172:175], v[46:49]
	v_mfma_f32_16x16x32_bf16 v[38:41], v[146:149], v[180:183], v[38:41]
	v_mfma_f32_16x16x32_bf16 v[30:33], v[154:157], v[180:183], v[30:33]
	v_mfma_f32_16x16x32_bf16 v[22:25], v[146:149], v[194:197], v[22:25]
	v_mfma_f32_16x16x32_bf16 v[14:17], v[154:157], v[194:197], v[14:17]
	v_mfma_f32_16x16x32_bf16 v[6:9], v[146:149], v[202:205], v[6:9]
	v_mfma_f32_16x16x32_bf16 v[2:5], v[154:157], v[202:205], v[2:5]
	v_mfma_f32_16x16x32_bf16 v[54:57], v[150:153], v[176:179], v[54:57]
	v_mfma_f32_16x16x32_bf16 v[46:49], v[168:171], v[176:179], v[46:49]
	v_mfma_f32_16x16x32_bf16 v[38:41], v[150:153], v[190:193], v[38:41]
	v_mfma_f32_16x16x32_bf16 v[30:33], v[168:171], v[190:193], v[30:33]
	v_mfma_f32_16x16x32_bf16 v[22:25], v[150:153], v[198:201], v[22:25]
	v_mfma_f32_16x16x32_bf16 v[14:17], v[168:171], v[198:201], v[14:17]
	v_mfma_f32_16x16x32_bf16 v[6:9], v[150:153], v[206:209], v[6:9]
	v_mfma_f32_16x16x32_bf16 v[2:5], v[168:171], v[206:209], v[2:5]
	s_barrier
	s_add_i32 s43, 0, 0x18000
	s_add_i32 s58, 0, 0x1c000
	s_add_u32 s30, s30, 0x40000
	s_addc_u32 s31, s31, 0
	s_mov_b32 m0, s47
	s_nop 0
	global_load_lds_dwordx4 v162, s[30:31]
	s_mov_b32 m0, s48
	s_nop 0
	global_load_lds_dwordx4 v160, s[30:31]
	ds_read_b128 v[130:133], v165 offset:32768
	ds_read_b128 v[134:137], v165 offset:33792
	ds_read_b128 v[138:141], v165 offset:34816
	ds_read_b128 v[142:145], v165 offset:35840
	ds_read_b128 v[146:149], v165 offset:49152
	ds_read_b128 v[150:153], v165 offset:50176
	ds_read_b128 v[154:157], v165 offset:51200
	ds_read_b128 v[168:171], v165 offset:52224
	ds_read_b128 v[172:175], v188 offset:32768
	ds_read_b128 v[176:179], v188 offset:33792
	ds_read_b128 v[180:183], v188 offset:34816
	ds_read_b128 v[190:193], v188 offset:35840
	ds_read_b128 v[194:197], v188 offset:36864
	ds_read_b128 v[198:201], v188 offset:37888
	ds_read_b128 v[202:205], v188 offset:38912
	ds_read_b128 v[206:209], v188 offset:39936
	s_waitcnt vmcnt(8) lgkmcnt(0)
	s_barrier
	v_mfma_f32_16x16x32_bf16 v[126:129], v[130:133], v[172:175], v[126:129]
	v_mfma_f32_16x16x32_bf16 v[122:125], v[138:141], v[172:175], v[122:125]
	v_mfma_f32_16x16x32_bf16 v[114:117], v[130:133], v[180:183], v[114:117]
	v_mfma_f32_16x16x32_bf16 v[106:109], v[138:141], v[180:183], v[106:109]
	v_mfma_f32_16x16x32_bf16 v[98:101], v[130:133], v[194:197], v[98:101]
	v_mfma_f32_16x16x32_bf16 v[90:93], v[138:141], v[194:197], v[90:93]
	v_mfma_f32_16x16x32_bf16 v[82:85], v[130:133], v[202:205], v[82:85]
	v_mfma_f32_16x16x32_bf16 v[74:77], v[138:141], v[202:205], v[74:77]
	v_mfma_f32_16x16x32_bf16 v[126:129], v[134:137], v[176:179], v[126:129]
	v_mfma_f32_16x16x32_bf16 v[122:125], v[142:145], v[176:179], v[122:125]
	v_mfma_f32_16x16x32_bf16 v[114:117], v[134:137], v[190:193], v[114:117]
	v_mfma_f32_16x16x32_bf16 v[106:109], v[142:145], v[190:193], v[106:109]
	v_mfma_f32_16x16x32_bf16 v[98:101], v[134:137], v[198:201], v[98:101]
	v_mfma_f32_16x16x32_bf16 v[90:93], v[142:145], v[198:201], v[90:93]
	v_mfma_f32_16x16x32_bf16 v[82:85], v[134:137], v[206:209], v[82:85]
	v_mfma_f32_16x16x32_bf16 v[74:77], v[142:145], v[206:209], v[74:77]
	v_mfma_f32_16x16x32_bf16 v[118:121], v[146:149], v[172:175], v[118:121]
	v_mfma_f32_16x16x32_bf16 v[110:113], v[154:157], v[172:175], v[110:113]
	v_mfma_f32_16x16x32_bf16 v[102:105], v[146:149], v[180:183], v[102:105]
	v_mfma_f32_16x16x32_bf16 v[94:97], v[154:157], v[180:183], v[94:97]
	v_mfma_f32_16x16x32_bf16 v[86:89], v[146:149], v[194:197], v[86:89]
	v_mfma_f32_16x16x32_bf16 v[78:81], v[154:157], v[194:197], v[78:81]
	v_mfma_f32_16x16x32_bf16 v[70:73], v[146:149], v[202:205], v[70:73]
	v_mfma_f32_16x16x32_bf16 v[66:69], v[154:157], v[202:205], v[66:69]
	v_mfma_f32_16x16x32_bf16 v[118:121], v[150:153], v[176:179], v[118:121]
	v_mfma_f32_16x16x32_bf16 v[110:113], v[168:171], v[176:179], v[110:113]
	v_mfma_f32_16x16x32_bf16 v[102:105], v[150:153], v[190:193], v[102:105]
	v_mfma_f32_16x16x32_bf16 v[94:97], v[168:171], v[190:193], v[94:97]
	v_mfma_f32_16x16x32_bf16 v[86:89], v[150:153], v[198:201], v[86:89]
	v_mfma_f32_16x16x32_bf16 v[78:81], v[168:171], v[198:201], v[78:81]
	v_mfma_f32_16x16x32_bf16 v[70:73], v[150:153], v[206:209], v[70:73]
	v_mfma_f32_16x16x32_bf16 v[66:69], v[168:171], v[206:209], v[66:69]
	s_barrier
	s_add_i32 s30, s43, s44
	v_lshl_add_u64 v[216:217], v[216:217], 0, s[56:57]
	s_mov_b32 m0, s30
	s_nop 0
	global_load_lds_dwordx4 v[216:217], off
	s_add_i32 m0, s30, 0x2000
	s_add_u32 s28, s28, 0x40080
	v_lshl_add_u64 v[216:217], v[218:219], 0, s[56:57]
	s_addc_u32 s29, s29, 0
	s_add_i32 s30, s58, s44
	global_load_lds_dwordx4 v[216:217], off
	s_mov_b32 m0, s30
	s_nop 0
	global_load_lds_dwordx4 v0, s[28:29]
	s_add_i32 m0, s30, 0x2000
	s_nop 0
	global_load_lds_dwordx4 v158, s[28:29]
	s_mov_b32 m0, s49
	v_lshl_add_u64 v[216:217], v[220:221], 0, s[56:57]
	global_load_lds_dwordx4 v[216:217], off
	s_mov_b32 m0, s52
	v_lshl_add_u64 v[216:217], v[222:223], 0, s[56:57]
	global_load_lds_dwordx4 v[216:217], off
	ds_read_b128 v[172:175], v188 offset:49152
	ds_read_b128 v[176:179], v188 offset:50176
	ds_read_b128 v[180:183], v188 offset:51200
	ds_read_b128 v[190:193], v188 offset:52224
	ds_read_b128 v[194:197], v188 offset:53248
	ds_read_b128 v[198:201], v188 offset:54272
	ds_read_b128 v[202:205], v188 offset:55296
	ds_read_b128 v[206:209], v188 offset:56320
	s_waitcnt vmcnt(8) lgkmcnt(0)
	s_barrier
	v_mfma_f32_16x16x32_bf16 v[62:65], v[130:133], v[172:175], v[62:65]
	v_mfma_f32_16x16x32_bf16 v[58:61], v[138:141], v[172:175], v[58:61]
	v_mfma_f32_16x16x32_bf16 v[50:53], v[130:133], v[180:183], v[50:53]
	v_mfma_f32_16x16x32_bf16 v[42:45], v[138:141], v[180:183], v[42:45]
	v_mfma_f32_16x16x32_bf16 v[34:37], v[130:133], v[194:197], v[34:37]
	v_mfma_f32_16x16x32_bf16 v[26:29], v[138:141], v[194:197], v[26:29]
	v_mfma_f32_16x16x32_bf16 v[18:21], v[130:133], v[202:205], v[18:21]
	v_mfma_f32_16x16x32_bf16 v[10:13], v[138:141], v[202:205], v[10:13]
	v_mfma_f32_16x16x32_bf16 v[62:65], v[134:137], v[176:179], v[62:65]
	v_mfma_f32_16x16x32_bf16 v[58:61], v[142:145], v[176:179], v[58:61]
	v_mfma_f32_16x16x32_bf16 v[50:53], v[134:137], v[190:193], v[50:53]
	v_mfma_f32_16x16x32_bf16 v[42:45], v[142:145], v[190:193], v[42:45]
	v_mfma_f32_16x16x32_bf16 v[34:37], v[134:137], v[198:201], v[34:37]
	v_mfma_f32_16x16x32_bf16 v[26:29], v[142:145], v[198:201], v[26:29]
	v_mfma_f32_16x16x32_bf16 v[18:21], v[134:137], v[206:209], v[18:21]
	v_mfma_f32_16x16x32_bf16 v[10:13], v[142:145], v[206:209], v[10:13]
	v_mfma_f32_16x16x32_bf16 v[54:57], v[146:149], v[172:175], v[54:57]
	v_mfma_f32_16x16x32_bf16 v[46:49], v[154:157], v[172:175], v[46:49]
	v_mfma_f32_16x16x32_bf16 v[38:41], v[146:149], v[180:183], v[38:41]
	v_mfma_f32_16x16x32_bf16 v[30:33], v[154:157], v[180:183], v[30:33]
	v_mfma_f32_16x16x32_bf16 v[22:25], v[146:149], v[194:197], v[22:25]
	v_mfma_f32_16x16x32_bf16 v[14:17], v[154:157], v[194:197], v[14:17]
	v_mfma_f32_16x16x32_bf16 v[6:9], v[146:149], v[202:205], v[6:9]
	v_mfma_f32_16x16x32_bf16 v[2:5], v[154:157], v[202:205], v[2:5]
	v_mfma_f32_16x16x32_bf16 v[54:57], v[150:153], v[176:179], v[54:57]
	v_mfma_f32_16x16x32_bf16 v[46:49], v[168:171], v[176:179], v[46:49]
	v_mfma_f32_16x16x32_bf16 v[38:41], v[150:153], v[190:193], v[38:41]
	v_mfma_f32_16x16x32_bf16 v[30:33], v[168:171], v[190:193], v[30:33]
	v_mfma_f32_16x16x32_bf16 v[22:25], v[150:153], v[198:201], v[22:25]
	v_mfma_f32_16x16x32_bf16 v[14:17], v[168:171], v[198:201], v[14:17]
	v_mfma_f32_16x16x32_bf16 v[6:9], v[150:153], v[206:209], v[6:9]
	v_mfma_f32_16x16x32_bf16 v[2:5], v[168:171], v[206:209], v[2:5]
	s_barrier
	s_add_i32 s42, s42, 2
	s_add_u32 s23, s23, 0x100
	s_addc_u32 s33, s33, 0
	s_add_u32 s6, s6, 0x100
	s_addc_u32 s7, s7, 0
	s_cmp_gt_u32 s42, 13
	s_cbranch_scc0 .LBB0_417
	s_and_b64 vcc, exec, s[18:19]
	s_cbranch_vccz .LBB0_420
	s_barrier

.LBB0_587:
	s_add_u32 s18, s34, s62
	s_addc_u32 s19, s35, s63
	s_add_u32 s18, s18, 0x100
	s_addc_u32 s19, s19, 0
	s_add_u32 s70, s8, s62
	s_addc_u32 s71, s9, s63
	s_add_i32 s26, 0, 0x10000
	s_cmpk_eq_i32 s62, 0x700
	s_cselect_b32 s77, s47, s19
	s_cselect_b32 s76, s59, s18
	s_cselect_b32 s71, s37, s71
	s_cselect_b32 s70, vcc_lo, s70
	s_add_i32 s27, 0, 0x14000
	v_lshl_add_u64 v[208:209], v[142:143], 0, s[62:63]
	s_add_i32 m0, s4, 0xc000
	s_nop 0
	global_load_lds_dwordx4 v[208:209], off
	s_add_i32 m0, s4, 0xe000
	v_lshl_add_u64 v[208:209], v[140:141], 0, s[62:63]
	global_load_lds_dwordx4 v[208:209], off
	ds_read_b128 v[146:149], v241
	ds_read_b128 v[150:153], v241 offset:1024
	ds_read_b128 v[154:157], v241 offset:2048
	ds_read_b128 v[158:161], v241 offset:3072
	ds_read_b128 v[162:165], v241 offset:16384
	ds_read_b128 v[168:171], v241 offset:17408
	ds_read_b128 v[172:175], v241 offset:18432
	ds_read_b128 v[176:179], v241 offset:19456
	ds_read_b128 v[180:183], v145
	ds_read_b128 v[184:187], v145 offset:1024
	ds_read_b128 v[188:191], v145 offset:2048
	ds_read_b128 v[192:195], v145 offset:3072
	ds_read_b128 v[196:199], v145 offset:4096
	ds_read_b128 v[200:203], v145 offset:5120
	ds_read_b128 v[204:207], v145 offset:6144
	ds_read_b128 v[216:219], v145 offset:7168
	s_waitcnt vmcnt(8) lgkmcnt(0)
	s_barrier
	v_mfma_f32_16x16x32_bf16 v[134:137], v[146:149], v[180:183], v[134:137]
	v_mfma_f32_16x16x32_bf16 v[130:133], v[154:157], v[180:183], v[130:133]
	v_mfma_f32_16x16x32_bf16 v[110:113], v[146:149], v[188:191], v[110:113]
	v_mfma_f32_16x16x32_bf16 v[106:109], v[154:157], v[188:191], v[106:109]
	v_mfma_f32_16x16x32_bf16 v[94:97], v[146:149], v[196:199], v[94:97]
	v_mfma_f32_16x16x32_bf16 v[90:93], v[154:157], v[196:199], v[90:93]
	v_mfma_f32_16x16x32_bf16 v[78:81], v[146:149], v[204:207], v[78:81]
	v_mfma_f32_16x16x32_bf16 v[74:77], v[154:157], v[204:207], v[74:77]
	v_mfma_f32_16x16x32_bf16 v[134:137], v[150:153], v[184:187], v[134:137]
	v_mfma_f32_16x16x32_bf16 v[130:133], v[158:161], v[184:187], v[130:133]
	v_mfma_f32_16x16x32_bf16 v[110:113], v[150:153], v[192:195], v[110:113]
	v_mfma_f32_16x16x32_bf16 v[106:109], v[158:161], v[192:195], v[106:109]
	v_mfma_f32_16x16x32_bf16 v[94:97], v[150:153], v[200:203], v[94:97]
	v_mfma_f32_16x16x32_bf16 v[90:93], v[158:161], v[200:203], v[90:93]
	v_mfma_f32_16x16x32_bf16 v[78:81], v[150:153], v[216:219], v[78:81]
	v_mfma_f32_16x16x32_bf16 v[74:77], v[158:161], v[216:219], v[74:77]
	v_mfma_f32_16x16x32_bf16 v[122:125], v[162:165], v[180:183], v[122:125]
	v_mfma_f32_16x16x32_bf16 v[114:117], v[172:175], v[180:183], v[114:117]
	v_mfma_f32_16x16x32_bf16 v[102:105], v[162:165], v[188:191], v[102:105]
	v_mfma_f32_16x16x32_bf16 v[98:101], v[172:175], v[188:191], v[98:101]
	v_mfma_f32_16x16x32_bf16 v[86:89], v[162:165], v[196:199], v[86:89]
	v_mfma_f32_16x16x32_bf16 v[82:85], v[172:175], v[196:199], v[82:85]
	v_mfma_f32_16x16x32_bf16 v[70:73], v[162:165], v[204:207], v[70:73]
	v_mfma_f32_16x16x32_bf16 v[66:69], v[172:175], v[204:207], v[66:69]
	v_mfma_f32_16x16x32_bf16 v[122:125], v[168:171], v[184:187], v[122:125]
	v_mfma_f32_16x16x32_bf16 v[114:117], v[176:179], v[184:187], v[114:117]
	v_mfma_f32_16x16x32_bf16 v[102:105], v[168:171], v[192:195], v[102:105]
	v_mfma_f32_16x16x32_bf16 v[98:101], v[176:179], v[192:195], v[98:101]
	v_mfma_f32_16x16x32_bf16 v[86:89], v[168:171], v[200:203], v[86:89]
	v_mfma_f32_16x16x32_bf16 v[82:85], v[176:179], v[200:203], v[82:85]
	v_mfma_f32_16x16x32_bf16 v[70:73], v[168:171], v[216:219], v[70:73]
	v_mfma_f32_16x16x32_bf16 v[66:69], v[176:179], v[216:219], v[66:69]
	s_barrier
	s_add_i32 s18, s26, s84
	v_lshl_add_u64 v[208:209], s[70:71], 0, v[0:1]
	s_mov_b32 m0, s18
	s_nop 0
	global_load_lds_dwordx4 v0, s[70:71]
	s_add_i32 m0, s18, 0x2000
	s_add_u32 s18, s70, 0x40000
	v_lshl_add_u64 v[220:221], s[70:71], 0, v[118:119]
	s_addc_u32 s19, s71, 0
	s_add_i32 s26, s27, s84
	global_load_lds_dwordx4 v118, s[70:71]
	s_mov_b32 m0, s26
	v_lshl_add_u64 v[224:225], s[76:77], 0, v[120:121]
	global_load_lds_dwordx4 v0, s[18:19]
	s_add_i32 m0, s26, 0x2000
	s_nop 0
	global_load_lds_dwordx4 v118, s[18:19]
	s_mov_b32 m0, s4
	v_lshl_add_u64 v[222:223], s[76:77], 0, v[126:127]
	global_load_lds_dwordx4 v126, s[76:77]
	s_mov_b32 m0, s5
	s_nop 0
	global_load_lds_dwordx4 v120, s[76:77]
	ds_read_b128 v[180:183], v145 offset:16384
	ds_read_b128 v[184:187], v145 offset:17408
	ds_read_b128 v[188:191], v145 offset:18432
	ds_read_b128 v[192:195], v145 offset:19456
	ds_read_b128 v[196:199], v145 offset:20480
	ds_read_b128 v[200:203], v145 offset:21504
	ds_read_b128 v[204:207], v145 offset:22528
	ds_read_b128 v[216:219], v145 offset:23552
	s_waitcnt vmcnt(8) lgkmcnt(0)
	s_barrier
	v_mfma_f32_16x16x32_bf16 v[62:65], v[146:149], v[180:183], v[62:65]
	v_mfma_f32_16x16x32_bf16 v[58:61], v[154:157], v[180:183], v[58:61]
	v_mfma_f32_16x16x32_bf16 v[46:49], v[146:149], v[188:191], v[46:49]
	v_mfma_f32_16x16x32_bf16 v[42:45], v[154:157], v[188:191], v[42:45]
	v_mfma_f32_16x16x32_bf16 v[30:33], v[146:149], v[196:199], v[30:33]
	v_mfma_f32_16x16x32_bf16 v[26:29], v[154:157], v[196:199], v[26:29]
	v_mfma_f32_16x16x32_bf16 v[14:17], v[146:149], v[204:207], v[14:17]
	v_mfma_f32_16x16x32_bf16 v[10:13], v[154:157], v[204:207], v[10:13]
	v_mfma_f32_16x16x32_bf16 v[62:65], v[150:153], v[184:187], v[62:65]
	v_mfma_f32_16x16x32_bf16 v[58:61], v[158:161], v[184:187], v[58:61]
	v_mfma_f32_16x16x32_bf16 v[46:49], v[150:153], v[192:195], v[46:49]
	v_mfma_f32_16x16x32_bf16 v[42:45], v[158:161], v[192:195], v[42:45]
	v_mfma_f32_16x16x32_bf16 v[30:33], v[150:153], v[200:203], v[30:33]
	v_mfma_f32_16x16x32_bf16 v[26:29], v[158:161], v[200:203], v[26:29]
	v_mfma_f32_16x16x32_bf16 v[14:17], v[150:153], v[216:219], v[14:17]
	v_mfma_f32_16x16x32_bf16 v[10:13], v[158:161], v[216:219], v[10:13]
	v_mfma_f32_16x16x32_bf16 v[54:57], v[162:165], v[180:183], v[54:57]
	v_mfma_f32_16x16x32_bf16 v[50:53], v[172:175], v[180:183], v[50:53]
	v_mfma_f32_16x16x32_bf16 v[38:41], v[162:165], v[188:191], v[38:41]
	v_mfma_f32_16x16x32_bf16 v[34:37], v[172:175], v[188:191], v[34:37]
	v_mfma_f32_16x16x32_bf16 v[22:25], v[162:165], v[196:199], v[22:25]
	v_mfma_f32_16x16x32_bf16 v[18:21], v[172:175], v[196:199], v[18:21]
	v_mfma_f32_16x16x32_bf16 v[6:9], v[162:165], v[204:207], v[6:9]
	v_mfma_f32_16x16x32_bf16 v[2:5], v[172:175], v[204:207], v[2:5]
	v_mfma_f32_16x16x32_bf16 v[54:57], v[168:171], v[184:187], v[54:57]
	v_mfma_f32_16x16x32_bf16 v[50:53], v[176:179], v[184:187], v[50:53]
	v_mfma_f32_16x16x32_bf16 v[38:41], v[168:171], v[192:195], v[38:41]
	v_mfma_f32_16x16x32_bf16 v[34:37], v[176:179], v[192:195], v[34:37]
	v_mfma_f32_16x16x32_bf16 v[22:25], v[168:171], v[200:203], v[22:25]
	v_mfma_f32_16x16x32_bf16 v[18:21], v[176:179], v[200:203], v[18:21]
	v_mfma_f32_16x16x32_bf16 v[6:9], v[168:171], v[216:219], v[6:9]
	v_mfma_f32_16x16x32_bf16 v[2:5], v[176:179], v[216:219], v[2:5]
	s_barrier
	s_add_i32 s26, 0, 0x18000
	s_add_i32 s27, 0, 0x1c000
	s_add_u32 s18, s76, 0x40000
	s_addc_u32 s19, s77, 0
	s_mov_b32 m0, s33
	s_nop 0
	global_load_lds_dwordx4 v126, s[18:19]
	s_mov_b32 m0, s92
	v_lshl_add_u64 v[242:243], s[18:19], 0, v[120:121]
	global_load_lds_dwordx4 v120, s[18:19]
	ds_read_b128 v[146:149], v241 offset:32768
	ds_read_b128 v[150:153], v241 offset:33792
	ds_read_b128 v[154:157], v241 offset:34816
	ds_read_b128 v[158:161], v241 offset:35840
	ds_read_b128 v[162:165], v241 offset:49152
	ds_read_b128 v[168:171], v241 offset:50176
	ds_read_b128 v[172:175], v241 offset:51200
	ds_read_b128 v[176:179], v241 offset:52224
	ds_read_b128 v[180:183], v145 offset:32768
	ds_read_b128 v[184:187], v145 offset:33792
	ds_read_b128 v[188:191], v145 offset:34816
	ds_read_b128 v[192:195], v145 offset:35840
	ds_read_b128 v[196:199], v145 offset:36864
	ds_read_b128 v[200:203], v145 offset:37888
	ds_read_b128 v[204:207], v145 offset:38912
	ds_read_b128 v[216:219], v145 offset:39936
	s_waitcnt vmcnt(8) lgkmcnt(0)
	s_barrier
	v_mfma_f32_16x16x32_bf16 v[134:137], v[146:149], v[180:183], v[134:137]
	v_mfma_f32_16x16x32_bf16 v[130:133], v[154:157], v[180:183], v[130:133]
	v_mfma_f32_16x16x32_bf16 v[110:113], v[146:149], v[188:191], v[110:113]
	v_mfma_f32_16x16x32_bf16 v[106:109], v[154:157], v[188:191], v[106:109]
	v_mfma_f32_16x16x32_bf16 v[94:97], v[146:149], v[196:199], v[94:97]
	v_mfma_f32_16x16x32_bf16 v[90:93], v[154:157], v[196:199], v[90:93]
	v_mfma_f32_16x16x32_bf16 v[78:81], v[146:149], v[204:207], v[78:81]
	v_mfma_f32_16x16x32_bf16 v[74:77], v[154:157], v[204:207], v[74:77]
	v_mfma_f32_16x16x32_bf16 v[134:137], v[150:153], v[184:187], v[134:137]
	v_mfma_f32_16x16x32_bf16 v[130:133], v[158:161], v[184:187], v[130:133]
	v_mfma_f32_16x16x32_bf16 v[110:113], v[150:153], v[192:195], v[110:113]
	v_mfma_f32_16x16x32_bf16 v[106:109], v[158:161], v[192:195], v[106:109]
	v_mfma_f32_16x16x32_bf16 v[94:97], v[150:153], v[200:203], v[94:97]
	v_mfma_f32_16x16x32_bf16 v[90:93], v[158:161], v[200:203], v[90:93]
	v_mfma_f32_16x16x32_bf16 v[78:81], v[150:153], v[216:219], v[78:81]
	v_mfma_f32_16x16x32_bf16 v[74:77], v[158:161], v[216:219], v[74:77]
	v_mfma_f32_16x16x32_bf16 v[122:125], v[162:165], v[180:183], v[122:125]
	v_mfma_f32_16x16x32_bf16 v[114:117], v[172:175], v[180:183], v[114:117]
	v_mfma_f32_16x16x32_bf16 v[102:105], v[162:165], v[188:191], v[102:105]
	v_mfma_f32_16x16x32_bf16 v[98:101], v[172:175], v[188:191], v[98:101]
	v_mfma_f32_16x16x32_bf16 v[86:89], v[162:165], v[196:199], v[86:89]
	v_mfma_f32_16x16x32_bf16 v[82:85], v[172:175], v[196:199], v[82:85]
	v_mfma_f32_16x16x32_bf16 v[70:73], v[162:165], v[204:207], v[70:73]
	v_mfma_f32_16x16x32_bf16 v[66:69], v[172:175], v[204:207], v[66:69]
	v_mfma_f32_16x16x32_bf16 v[122:125], v[168:171], v[184:187], v[122:125]
	v_mfma_f32_16x16x32_bf16 v[114:117], v[176:179], v[184:187], v[114:117]
	v_mfma_f32_16x16x32_bf16 v[102:105], v[168:171], v[192:195], v[102:105]
	v_mfma_f32_16x16x32_bf16 v[98:101], v[176:179], v[192:195], v[98:101]
	v_mfma_f32_16x16x32_bf16 v[86:89], v[168:171], v[200:203], v[86:89]
	v_mfma_f32_16x16x32_bf16 v[82:85], v[176:179], v[200:203], v[82:85]
	v_mfma_f32_16x16x32_bf16 v[70:73], v[168:171], v[216:219], v[70:73]
	v_mfma_f32_16x16x32_bf16 v[66:69], v[176:179], v[216:219], v[66:69]
	s_barrier
	s_add_i32 s18, s26, s84
	v_lshl_add_u64 v[208:209], v[208:209], 0, s[56:57]
	s_mov_b32 m0, s18
	s_nop 0
	global_load_lds_dwordx4 v[208:209], off
	s_add_i32 m0, s18, 0x2000
	s_add_u32 s18, s70, 0x40080
	v_lshl_add_u64 v[208:209], v[220:221], 0, s[56:57]
	s_addc_u32 s19, s71, 0
	s_add_i32 s26, s27, s84
	global_load_lds_dwordx4 v[208:209], off
	s_mov_b32 m0, s26
	s_nop 0
	global_load_lds_dwordx4 v0, s[18:19]
	s_add_i32 m0, s26, 0x2000
	s_nop 0
	global_load_lds_dwordx4 v118, s[18:19]
	s_mov_b32 m0, s90
	v_lshl_add_u64 v[208:209], v[222:223], 0, s[56:57]
	global_load_lds_dwordx4 v[208:209], off
	s_mov_b32 m0, s96
	v_lshl_add_u64 v[208:209], v[224:225], 0, s[56:57]
	global_load_lds_dwordx4 v[208:209], off
	ds_read_b128 v[180:183], v145 offset:49152
	ds_read_b128 v[184:187], v145 offset:50176
	ds_read_b128 v[188:191], v145 offset:51200
	ds_read_b128 v[192:195], v145 offset:52224
	ds_read_b128 v[196:199], v145 offset:53248
	ds_read_b128 v[200:203], v145 offset:54272
	ds_read_b128 v[204:207], v145 offset:55296
	ds_read_b128 v[216:219], v145 offset:56320
	s_waitcnt vmcnt(8) lgkmcnt(0)
	s_barrier
	v_mfma_f32_16x16x32_bf16 v[62:65], v[146:149], v[180:183], v[62:65]
	v_mfma_f32_16x16x32_bf16 v[58:61], v[154:157], v[180:183], v[58:61]
	v_mfma_f32_16x16x32_bf16 v[46:49], v[146:149], v[188:191], v[46:49]
	v_mfma_f32_16x16x32_bf16 v[42:45], v[154:157], v[188:191], v[42:45]
	v_mfma_f32_16x16x32_bf16 v[30:33], v[146:149], v[196:199], v[30:33]
	v_mfma_f32_16x16x32_bf16 v[26:29], v[154:157], v[196:199], v[26:29]
	v_mfma_f32_16x16x32_bf16 v[14:17], v[146:149], v[204:207], v[14:17]
	v_mfma_f32_16x16x32_bf16 v[10:13], v[154:157], v[204:207], v[10:13]
	v_mfma_f32_16x16x32_bf16 v[62:65], v[150:153], v[184:187], v[62:65]
	v_mfma_f32_16x16x32_bf16 v[58:61], v[158:161], v[184:187], v[58:61]
	v_mfma_f32_16x16x32_bf16 v[46:49], v[150:153], v[192:195], v[46:49]
	v_mfma_f32_16x16x32_bf16 v[42:45], v[158:161], v[192:195], v[42:45]
	v_mfma_f32_16x16x32_bf16 v[30:33], v[150:153], v[200:203], v[30:33]
	v_mfma_f32_16x16x32_bf16 v[26:29], v[158:161], v[200:203], v[26:29]
	v_mfma_f32_16x16x32_bf16 v[14:17], v[150:153], v[216:219], v[14:17]
	v_mfma_f32_16x16x32_bf16 v[10:13], v[158:161], v[216:219], v[10:13]
	v_mfma_f32_16x16x32_bf16 v[54:57], v[162:165], v[180:183], v[54:57]
	v_mfma_f32_16x16x32_bf16 v[50:53], v[172:175], v[180:183], v[50:53]
	v_mfma_f32_16x16x32_bf16 v[38:41], v[162:165], v[188:191], v[38:41]
	v_mfma_f32_16x16x32_bf16 v[34:37], v[172:175], v[188:191], v[34:37]
	v_mfma_f32_16x16x32_bf16 v[22:25], v[162:165], v[196:199], v[22:25]
	v_mfma_f32_16x16x32_bf16 v[18:21], v[172:175], v[196:199], v[18:21]
	v_mfma_f32_16x16x32_bf16 v[6:9], v[162:165], v[204:207], v[6:9]
	v_mfma_f32_16x16x32_bf16 v[2:5], v[172:175], v[204:207], v[2:5]
	v_mfma_f32_16x16x32_bf16 v[54:57], v[168:171], v[184:187], v[54:57]
	v_mfma_f32_16x16x32_bf16 v[50:53], v[176:179], v[184:187], v[50:53]
	v_mfma_f32_16x16x32_bf16 v[38:41], v[168:171], v[192:195], v[38:41]
	v_mfma_f32_16x16x32_bf16 v[34:37], v[176:179], v[192:195], v[34:37]
	v_mfma_f32_16x16x32_bf16 v[22:25], v[168:171], v[200:203], v[22:25]
	v_mfma_f32_16x16x32_bf16 v[18:21], v[176:179], v[200:203], v[18:21]
	v_mfma_f32_16x16x32_bf16 v[6:9], v[168:171], v[216:219], v[6:9]
	v_mfma_f32_16x16x32_bf16 v[2:5], v[176:179], v[216:219], v[2:5]
	s_barrier
	s_add_i32 vcc_hi, vcc_hi, 2
	s_add_u32 s62, s62, 0x100
	s_addc_u32 s63, s63, 0
	s_cmp_gt_u32 vcc_hi, 13
	s_cbranch_scc0 .LBB0_587
	s_add_u32 s62, s8, 0xffffff00
	s_addc_u32 s63, s9, -1
	s_andn2_b64 vcc, exec, s[44:45]
	s_cbranch_vccnz .LBB0_590
	v_mov_b32_e32 v2, 0
	s_mov_b32 s20, s36
	s_mov_b32 s83, s46
	s_mov_b64 s[34:35], s[52:53]
	s_mov_b32 s68, s58
	v_mov_b32_e32 v3, v2
	v_mov_b32_e32 v4, v2
	v_mov_b32_e32 v5, v2
	v_mov_b32_e32 v6, v2
	v_mov_b32_e32 v7, v2
	v_mov_b32_e32 v8, v2
	v_mov_b32_e32 v9, v2
	v_mov_b32_e32 v18, v2
	v_mov_b32_e32 v19, v2
	v_mov_b32_e32 v20, v2
	v_mov_b32_e32 v21, v2
	v_mov_b32_e32 v22, v2
	v_mov_b32_e32 v23, v2
	v_mov_b32_e32 v24, v2
	v_mov_b32_e32 v25, v2
	v_mov_b32_e32 v34, v2
	v_mov_b32_e32 v35, v2
	v_mov_b32_e32 v36, v2
	v_mov_b32_e32 v37, v2
	v_mov_b32_e32 v38, v2
	v_mov_b32_e32 v39, v2
	v_mov_b32_e32 v40, v2
	v_mov_b32_e32 v41, v2
	v_mov_b32_e32 v50, v2
	v_mov_b32_e32 v51, v2
	v_mov_b32_e32 v52, v2
	v_mov_b32_e32 v53, v2
	v_mov_b32_e32 v54, v2
	v_mov_b32_e32 v55, v2
	v_mov_b32_e32 v56, v2
	v_mov_b32_e32 v57, v2
	v_mov_b32_e32 v10, v2
	v_mov_b32_e32 v11, v2
	v_mov_b32_e32 v12, v2
	v_mov_b32_e32 v13, v2
	v_mov_b32_e32 v14, v2
	v_mov_b32_e32 v15, v2
	v_mov_b32_e32 v16, v2
	v_mov_b32_e32 v17, v2
	v_mov_b32_e32 v26, v2
	v_mov_b32_e32 v27, v2
	v_mov_b32_e32 v28, v2
	v_mov_b32_e32 v29, v2
	v_mov_b32_e32 v30, v2
	v_mov_b32_e32 v31, v2
	v_mov_b32_e32 v32, v2
	v_mov_b32_e32 v33, v2
	v_mov_b32_e32 v42, v2
	v_mov_b32_e32 v43, v2
	v_mov_b32_e32 v44, v2
	v_mov_b32_e32 v45, v2
	v_mov_b32_e32 v46, v2
	v_mov_b32_e32 v47, v2
	v_mov_b32_e32 v48, v2
	v_mov_b32_e32 v49, v2
	v_mov_b32_e32 v58, v2
	v_mov_b32_e32 v59, v2
	v_mov_b32_e32 v60, v2
	v_mov_b32_e32 v61, v2
	v_mov_b32_e32 v62, v2
	v_mov_b32_e32 v63, v2
	v_mov_b32_e32 v64, v2
	v_mov_b32_e32 v65, v2
	v_mov_b32_e32 v66, v2
	v_mov_b32_e32 v67, v2
	v_mov_b32_e32 v68, v2
	v_mov_b32_e32 v69, v2
	v_mov_b32_e32 v70, v2
	v_mov_b32_e32 v71, v2
	v_mov_b32_e32 v72, v2
	v_mov_b32_e32 v73, v2
	v_mov_b32_e32 v82, v2
	v_mov_b32_e32 v83, v2
	v_mov_b32_e32 v84, v2
	v_mov_b32_e32 v85, v2
	v_mov_b32_e32 v86, v2
	v_mov_b32_e32 v87, v2
	v_mov_b32_e32 v88, v2
	v_mov_b32_e32 v89, v2
	v_mov_b32_e32 v98, v2
	v_mov_b32_e32 v99, v2
	v_mov_b32_e32 v100, v2
	v_mov_b32_e32 v101, v2
	v_mov_b32_e32 v102, v2
	v_mov_b32_e32 v103, v2
	v_mov_b32_e32 v104, v2
	v_mov_b32_e32 v105, v2
	v_mov_b32_e32 v114, v2
	v_mov_b32_e32 v115, v2
	v_mov_b32_e32 v116, v2
	v_mov_b32_e32 v117, v2
	v_mov_b32_e32 v122, v2
	v_mov_b32_e32 v123, v2
	v_mov_b32_e32 v124, v2
	v_mov_b32_e32 v125, v2
	v_mov_b32_e32 v74, v2
	v_mov_b32_e32 v75, v2
	v_mov_b32_e32 v76, v2
	v_mov_b32_e32 v77, v2
	v_mov_b32_e32 v78, v2
	v_mov_b32_e32 v79, v2
	v_mov_b32_e32 v80, v2
	v_mov_b32_e32 v81, v2
	v_mov_b32_e32 v90, v2
	v_mov_b32_e32 v91, v2
	v_mov_b32_e32 v92, v2
	v_mov_b32_e32 v93, v2
	v_mov_b32_e32 v94, v2
	v_mov_b32_e32 v95, v2
	v_mov_b32_e32 v96, v2
	v_mov_b32_e32 v97, v2
	v_mov_b32_e32 v106, v2
	v_mov_b32_e32 v107, v2
	v_mov_b32_e32 v108, v2
	v_mov_b32_e32 v109, v2
	v_mov_b32_e32 v110, v2
	v_mov_b32_e32 v111, v2
	v_mov_b32_e32 v112, v2
	v_mov_b32_e32 v113, v2
	v_mov_b32_e32 v130, v2
	v_mov_b32_e32 v131, v2
	v_mov_b32_e32 v132, v2
	v_mov_b32_e32 v133, v2
	v_mov_b32_e32 v134, v2
	v_mov_b32_e32 v135, v2
	v_mov_b32_e32 v136, v2
	v_mov_b32_e32 v137, v2
	s_andn2_b64 vcc, exec, s[42:43]
	s_cbranch_vccnz .LBB0_591
	s_branch .LBB0_592

.LBB0_684:
	s_add_u32 s52, s30, s48
	s_addc_u32 s53, s31, s49
	s_add_u32 s52, s52, 0x100
	s_addc_u32 s53, s53, 0
	s_add_u32 s95, s8, s48
	s_addc_u32 s96, s9, s49
	s_add_i32 vcc_lo, 0, 0x10000
	s_cmpk_eq_i32 s48, 0x700
	s_cselect_b32 s63, s37, s53
	s_cselect_b32 s62, s59, s52
	s_cselect_b32 s53, s35, s96
	s_cselect_b32 s52, s93, s95
	s_add_i32 s95, 0, 0x14000
	v_add_u32_e32 v158, vcc_lo, v144
	v_add_u32_e32 v167, s95, v144
	v_lshl_add_u64 v[208:209], v[142:143], 0, s[48:49]
	s_add_i32 m0, s4, 0xc000
	s_nop 0
	global_load_lds_dwordx4 v[208:209], off
	s_add_i32 m0, s4, 0xe000
	v_lshl_add_u64 v[208:209], v[140:141], 0, s[48:49]
	global_load_lds_dwordx4 v[208:209], off
	ds_read_b128 v[146:149], v158
	ds_read_b128 v[150:153], v158 offset:1024
	ds_read_b128 v[154:157], v158 offset:2048
	ds_read_b128 v[158:161], v158 offset:3072
	ds_read_b128 v[162:165], v167
	ds_read_b128 v[168:171], v167 offset:1024
	ds_read_b128 v[172:175], v167 offset:2048
	ds_read_b128 v[176:179], v167 offset:3072
	ds_read_b128 v[180:183], v145
	ds_read_b128 v[184:187], v145 offset:1024
	ds_read_b128 v[188:191], v145 offset:2048
	ds_read_b128 v[192:195], v145 offset:3072
	ds_read_b128 v[196:199], v145 offset:4096
	ds_read_b128 v[200:203], v145 offset:5120
	ds_read_b128 v[204:207], v145 offset:6144
	ds_read_b128 v[216:219], v145 offset:7168
	s_waitcnt vmcnt(8) lgkmcnt(0)
	s_barrier
	v_mfma_f32_16x16x32_bf16 v[134:137], v[146:149], v[180:183], v[134:137]
	v_mfma_f32_16x16x32_bf16 v[130:133], v[154:157], v[180:183], v[130:133]
	v_mfma_f32_16x16x32_bf16 v[110:113], v[146:149], v[188:191], v[110:113]
	v_mfma_f32_16x16x32_bf16 v[106:109], v[154:157], v[188:191], v[106:109]
	v_mfma_f32_16x16x32_bf16 v[94:97], v[146:149], v[196:199], v[94:97]
	v_mfma_f32_16x16x32_bf16 v[90:93], v[154:157], v[196:199], v[90:93]
	v_mfma_f32_16x16x32_bf16 v[78:81], v[146:149], v[204:207], v[78:81]
	v_mfma_f32_16x16x32_bf16 v[74:77], v[154:157], v[204:207], v[74:77]
	v_mfma_f32_16x16x32_bf16 v[134:137], v[150:153], v[184:187], v[134:137]
	v_mfma_f32_16x16x32_bf16 v[130:133], v[158:161], v[184:187], v[130:133]
	v_mfma_f32_16x16x32_bf16 v[110:113], v[150:153], v[192:195], v[110:113]
	v_mfma_f32_16x16x32_bf16 v[106:109], v[158:161], v[192:195], v[106:109]
	v_mfma_f32_16x16x32_bf16 v[94:97], v[150:153], v[200:203], v[94:97]
	v_mfma_f32_16x16x32_bf16 v[90:93], v[158:161], v[200:203], v[90:93]
	v_mfma_f32_16x16x32_bf16 v[78:81], v[150:153], v[216:219], v[78:81]
	v_mfma_f32_16x16x32_bf16 v[74:77], v[158:161], v[216:219], v[74:77]
	v_mfma_f32_16x16x32_bf16 v[122:125], v[162:165], v[180:183], v[122:125]
	v_mfma_f32_16x16x32_bf16 v[114:117], v[172:175], v[180:183], v[114:117]
	v_mfma_f32_16x16x32_bf16 v[102:105], v[162:165], v[188:191], v[102:105]
	v_mfma_f32_16x16x32_bf16 v[98:101], v[172:175], v[188:191], v[98:101]
	v_mfma_f32_16x16x32_bf16 v[86:89], v[162:165], v[196:199], v[86:89]
	v_mfma_f32_16x16x32_bf16 v[82:85], v[172:175], v[196:199], v[82:85]
	v_mfma_f32_16x16x32_bf16 v[70:73], v[162:165], v[204:207], v[70:73]
	v_mfma_f32_16x16x32_bf16 v[66:69], v[172:175], v[204:207], v[66:69]
	v_mfma_f32_16x16x32_bf16 v[122:125], v[168:171], v[184:187], v[122:125]
	v_mfma_f32_16x16x32_bf16 v[114:117], v[176:179], v[184:187], v[114:117]
	v_mfma_f32_16x16x32_bf16 v[102:105], v[168:171], v[192:195], v[102:105]
	v_mfma_f32_16x16x32_bf16 v[98:101], v[176:179], v[192:195], v[98:101]
	v_mfma_f32_16x16x32_bf16 v[86:89], v[168:171], v[200:203], v[86:89]
	v_mfma_f32_16x16x32_bf16 v[82:85], v[176:179], v[200:203], v[82:85]
	v_mfma_f32_16x16x32_bf16 v[70:73], v[168:171], v[216:219], v[70:73]
	v_mfma_f32_16x16x32_bf16 v[66:69], v[176:179], v[216:219], v[66:69]
	s_barrier
	s_add_i32 s96, vcc_lo, s77
	v_lshl_add_u64 v[208:209], s[52:53], 0, v[0:1]
	s_mov_b32 m0, s96
	s_nop 0
	global_load_lds_dwordx4 v0, s[52:53]
	s_add_i32 m0, s96, 0x2000
	s_add_u32 vcc_lo, s52, 0x40000
	v_lshl_add_u64 v[220:221], s[52:53], 0, v[118:119]
	s_addc_u32 vcc_hi, s53, 0
	s_add_i32 s95, s95, s77
	global_load_lds_dwordx4 v118, s[52:53]
	v_lshl_add_u64 v[222:223], vcc, 0, v[0:1]
	s_mov_b32 m0, s95
	v_lshl_add_u64 v[224:225], s[62:63], 0, v[120:121]
	global_load_lds_dwordx4 v[222:223], off
	s_add_i32 m0, s95, 0x2000
	v_lshl_add_u64 v[222:223], vcc, 0, v[118:119]
	global_load_lds_dwordx4 v[222:223], off
	s_mov_b32 m0, s4
	v_lshl_add_u64 v[222:223], s[62:63], 0, v[126:127]
	global_load_lds_dwordx4 v126, s[62:63]
	s_mov_b32 m0, s5
	s_nop 0
	global_load_lds_dwordx4 v120, s[62:63]
	ds_read_b128 v[180:183], v145 offset:16384
	ds_read_b128 v[184:187], v145 offset:17408
	ds_read_b128 v[188:191], v145 offset:18432
	ds_read_b128 v[192:195], v145 offset:19456
	ds_read_b128 v[196:199], v145 offset:20480
	ds_read_b128 v[200:203], v145 offset:21504
	ds_read_b128 v[204:207], v145 offset:22528
	ds_read_b128 v[216:219], v145 offset:23552
	s_waitcnt vmcnt(8) lgkmcnt(0)
	s_barrier
	v_mfma_f32_16x16x32_bf16 v[62:65], v[146:149], v[180:183], v[62:65]
	v_mfma_f32_16x16x32_bf16 v[58:61], v[154:157], v[180:183], v[58:61]
	v_mfma_f32_16x16x32_bf16 v[46:49], v[146:149], v[188:191], v[46:49]
	v_mfma_f32_16x16x32_bf16 v[42:45], v[154:157], v[188:191], v[42:45]
	v_mfma_f32_16x16x32_bf16 v[30:33], v[146:149], v[196:199], v[30:33]
	v_mfma_f32_16x16x32_bf16 v[26:29], v[154:157], v[196:199], v[26:29]
	v_mfma_f32_16x16x32_bf16 v[14:17], v[146:149], v[204:207], v[14:17]
	v_mfma_f32_16x16x32_bf16 v[10:13], v[154:157], v[204:207], v[10:13]
	v_mfma_f32_16x16x32_bf16 v[62:65], v[150:153], v[184:187], v[62:65]
	v_mfma_f32_16x16x32_bf16 v[58:61], v[158:161], v[184:187], v[58:61]
	v_mfma_f32_16x16x32_bf16 v[46:49], v[150:153], v[192:195], v[46:49]
	v_mfma_f32_16x16x32_bf16 v[42:45], v[158:161], v[192:195], v[42:45]
	v_mfma_f32_16x16x32_bf16 v[30:33], v[150:153], v[200:203], v[30:33]
	v_mfma_f32_16x16x32_bf16 v[26:29], v[158:161], v[200:203], v[26:29]
	v_mfma_f32_16x16x32_bf16 v[14:17], v[150:153], v[216:219], v[14:17]
	v_mfma_f32_16x16x32_bf16 v[10:13], v[158:161], v[216:219], v[10:13]
	v_mfma_f32_16x16x32_bf16 v[54:57], v[162:165], v[180:183], v[54:57]
	v_mfma_f32_16x16x32_bf16 v[50:53], v[172:175], v[180:183], v[50:53]
	v_mfma_f32_16x16x32_bf16 v[38:41], v[162:165], v[188:191], v[38:41]
	v_mfma_f32_16x16x32_bf16 v[34:37], v[172:175], v[188:191], v[34:37]
	v_mfma_f32_16x16x32_bf16 v[22:25], v[162:165], v[196:199], v[22:25]
	v_mfma_f32_16x16x32_bf16 v[18:21], v[172:175], v[196:199], v[18:21]
	v_mfma_f32_16x16x32_bf16 v[6:9], v[162:165], v[204:207], v[6:9]
	v_mfma_f32_16x16x32_bf16 v[2:5], v[172:175], v[204:207], v[2:5]
	v_mfma_f32_16x16x32_bf16 v[54:57], v[168:171], v[184:187], v[54:57]
	v_mfma_f32_16x16x32_bf16 v[50:53], v[176:179], v[184:187], v[50:53]
	v_mfma_f32_16x16x32_bf16 v[38:41], v[168:171], v[192:195], v[38:41]
	v_mfma_f32_16x16x32_bf16 v[34:37], v[176:179], v[192:195], v[34:37]
	v_mfma_f32_16x16x32_bf16 v[22:25], v[168:171], v[200:203], v[22:25]
	v_mfma_f32_16x16x32_bf16 v[18:21], v[176:179], v[200:203], v[18:21]
	v_mfma_f32_16x16x32_bf16 v[6:9], v[168:171], v[216:219], v[6:9]
	v_mfma_f32_16x16x32_bf16 v[2:5], v[176:179], v[216:219], v[2:5]
	s_barrier
	s_add_i32 s95, 0, 0x18000
	s_add_i32 s96, 0, 0x1c000
	v_add_u32_e32 v158, s95, v144
	v_add_u32_e32 v167, s96, v144
	s_add_u32 s62, s62, 0x40000
	s_addc_u32 s63, s63, 0
	s_mov_b32 m0, s33
	s_nop 0
	global_load_lds_dwordx4 v126, s[62:63]
	s_mov_b32 m0, s84
	v_lshl_add_u64 v[242:243], s[62:63], 0, v[120:121]
	global_load_lds_dwordx4 v120, s[62:63]
	ds_read_b128 v[146:149], v158
	ds_read_b128 v[150:153], v158 offset:1024
	ds_read_b128 v[154:157], v158 offset:2048
	ds_read_b128 v[158:161], v158 offset:3072
	ds_read_b128 v[162:165], v167
	ds_read_b128 v[168:171], v167 offset:1024
	ds_read_b128 v[172:175], v167 offset:2048
	ds_read_b128 v[176:179], v167 offset:3072
	ds_read_b128 v[180:183], v145 offset:32768
	ds_read_b128 v[184:187], v145 offset:33792
	ds_read_b128 v[188:191], v145 offset:34816
	ds_read_b128 v[192:195], v145 offset:35840
	ds_read_b128 v[196:199], v145 offset:36864
	ds_read_b128 v[200:203], v145 offset:37888
	ds_read_b128 v[204:207], v145 offset:38912
	ds_read_b128 v[216:219], v145 offset:39936
	s_waitcnt vmcnt(8) lgkmcnt(0)
	s_barrier
	v_mfma_f32_16x16x32_bf16 v[134:137], v[146:149], v[180:183], v[134:137]
	v_mfma_f32_16x16x32_bf16 v[130:133], v[154:157], v[180:183], v[130:133]
	v_mfma_f32_16x16x32_bf16 v[110:113], v[146:149], v[188:191], v[110:113]
	v_mfma_f32_16x16x32_bf16 v[106:109], v[154:157], v[188:191], v[106:109]
	v_mfma_f32_16x16x32_bf16 v[94:97], v[146:149], v[196:199], v[94:97]
	v_mfma_f32_16x16x32_bf16 v[90:93], v[154:157], v[196:199], v[90:93]
	v_mfma_f32_16x16x32_bf16 v[78:81], v[146:149], v[204:207], v[78:81]
	v_mfma_f32_16x16x32_bf16 v[74:77], v[154:157], v[204:207], v[74:77]
	v_mfma_f32_16x16x32_bf16 v[134:137], v[150:153], v[184:187], v[134:137]
	v_mfma_f32_16x16x32_bf16 v[130:133], v[158:161], v[184:187], v[130:133]
	v_mfma_f32_16x16x32_bf16 v[110:113], v[150:153], v[192:195], v[110:113]
	v_mfma_f32_16x16x32_bf16 v[106:109], v[158:161], v[192:195], v[106:109]
	v_mfma_f32_16x16x32_bf16 v[94:97], v[150:153], v[200:203], v[94:97]
	v_mfma_f32_16x16x32_bf16 v[90:93], v[158:161], v[200:203], v[90:93]
	v_mfma_f32_16x16x32_bf16 v[78:81], v[150:153], v[216:219], v[78:81]
	v_mfma_f32_16x16x32_bf16 v[74:77], v[158:161], v[216:219], v[74:77]
	v_mfma_f32_16x16x32_bf16 v[122:125], v[162:165], v[180:183], v[122:125]
	v_mfma_f32_16x16x32_bf16 v[114:117], v[172:175], v[180:183], v[114:117]
	v_mfma_f32_16x16x32_bf16 v[102:105], v[162:165], v[188:191], v[102:105]
	v_mfma_f32_16x16x32_bf16 v[98:101], v[172:175], v[188:191], v[98:101]
	v_mfma_f32_16x16x32_bf16 v[86:89], v[162:165], v[196:199], v[86:89]
	v_mfma_f32_16x16x32_bf16 v[82:85], v[172:175], v[196:199], v[82:85]
	v_mfma_f32_16x16x32_bf16 v[70:73], v[162:165], v[204:207], v[70:73]
	v_mfma_f32_16x16x32_bf16 v[66:69], v[172:175], v[204:207], v[66:69]
	v_mfma_f32_16x16x32_bf16 v[122:125], v[168:171], v[184:187], v[122:125]
	v_mfma_f32_16x16x32_bf16 v[114:117], v[176:179], v[184:187], v[114:117]
	v_mfma_f32_16x16x32_bf16 v[102:105], v[168:171], v[192:195], v[102:105]
	v_mfma_f32_16x16x32_bf16 v[98:101], v[176:179], v[192:195], v[98:101]
	v_mfma_f32_16x16x32_bf16 v[86:89], v[168:171], v[200:203], v[86:89]
	v_mfma_f32_16x16x32_bf16 v[82:85], v[176:179], v[200:203], v[82:85]
	v_mfma_f32_16x16x32_bf16 v[70:73], v[168:171], v[216:219], v[70:73]
	v_mfma_f32_16x16x32_bf16 v[66:69], v[176:179], v[216:219], v[66:69]
	s_barrier
	s_add_i32 s62, s95, s77
	v_lshl_add_u64 v[208:209], v[208:209], 0, s[56:57]
	s_mov_b32 m0, s62
	s_nop 0
	global_load_lds_dwordx4 v[208:209], off
	s_add_i32 m0, s62, 0x2000
	s_add_u32 s52, s52, 0x40080
	v_lshl_add_u64 v[208:209], v[220:221], 0, s[56:57]
	s_addc_u32 s53, s53, 0
	s_add_i32 s62, s96, s77
	global_load_lds_dwordx4 v[208:209], off
	s_mov_b32 m0, s62
	s_nop 0
	global_load_lds_dwordx4 v0, s[52:53]
	s_add_i32 m0, s62, 0x2000
	s_nop 0
	global_load_lds_dwordx4 v118, s[52:53]
	s_mov_b32 m0, s85
	v_lshl_add_u64 v[208:209], v[222:223], 0, s[56:57]
	global_load_lds_dwordx4 v[208:209], off
	s_mov_b32 m0, s90
	v_lshl_add_u64 v[208:209], v[224:225], 0, s[56:57]
	global_load_lds_dwordx4 v[208:209], off
	ds_read_b128 v[180:183], v145 offset:49152
	ds_read_b128 v[184:187], v145 offset:50176
	ds_read_b128 v[188:191], v145 offset:51200
	ds_read_b128 v[192:195], v145 offset:52224
	ds_read_b128 v[196:199], v145 offset:53248
	ds_read_b128 v[200:203], v145 offset:54272
	ds_read_b128 v[204:207], v145 offset:55296
	ds_read_b128 v[216:219], v145 offset:56320
	s_waitcnt vmcnt(8) lgkmcnt(0)
	s_barrier
	v_mfma_f32_16x16x32_bf16 v[62:65], v[146:149], v[180:183], v[62:65]
	v_mfma_f32_16x16x32_bf16 v[58:61], v[154:157], v[180:183], v[58:61]
	v_mfma_f32_16x16x32_bf16 v[46:49], v[146:149], v[188:191], v[46:49]
	v_mfma_f32_16x16x32_bf16 v[42:45], v[154:157], v[188:191], v[42:45]
	v_mfma_f32_16x16x32_bf16 v[30:33], v[146:149], v[196:199], v[30:33]
	v_mfma_f32_16x16x32_bf16 v[26:29], v[154:157], v[196:199], v[26:29]
	v_mfma_f32_16x16x32_bf16 v[14:17], v[146:149], v[204:207], v[14:17]
	v_mfma_f32_16x16x32_bf16 v[10:13], v[154:157], v[204:207], v[10:13]
	v_mfma_f32_16x16x32_bf16 v[62:65], v[150:153], v[184:187], v[62:65]
	v_mfma_f32_16x16x32_bf16 v[58:61], v[158:161], v[184:187], v[58:61]
	v_mfma_f32_16x16x32_bf16 v[46:49], v[150:153], v[192:195], v[46:49]
	v_mfma_f32_16x16x32_bf16 v[42:45], v[158:161], v[192:195], v[42:45]
	v_mfma_f32_16x16x32_bf16 v[30:33], v[150:153], v[200:203], v[30:33]
	v_mfma_f32_16x16x32_bf16 v[26:29], v[158:161], v[200:203], v[26:29]
	v_mfma_f32_16x16x32_bf16 v[14:17], v[150:153], v[216:219], v[14:17]
	v_mfma_f32_16x16x32_bf16 v[10:13], v[158:161], v[216:219], v[10:13]
	v_mfma_f32_16x16x32_bf16 v[54:57], v[162:165], v[180:183], v[54:57]
	v_mfma_f32_16x16x32_bf16 v[50:53], v[172:175], v[180:183], v[50:53]
	v_mfma_f32_16x16x32_bf16 v[38:41], v[162:165], v[188:191], v[38:41]
	v_mfma_f32_16x16x32_bf16 v[34:37], v[172:175], v[188:191], v[34:37]
	v_mfma_f32_16x16x32_bf16 v[22:25], v[162:165], v[196:199], v[22:25]
	v_mfma_f32_16x16x32_bf16 v[18:21], v[172:175], v[196:199], v[18:21]
	v_mfma_f32_16x16x32_bf16 v[6:9], v[162:165], v[204:207], v[6:9]
	v_mfma_f32_16x16x32_bf16 v[2:5], v[172:175], v[204:207], v[2:5]
	v_mfma_f32_16x16x32_bf16 v[54:57], v[168:171], v[184:187], v[54:57]
	v_mfma_f32_16x16x32_bf16 v[50:53], v[176:179], v[184:187], v[50:53]
	v_mfma_f32_16x16x32_bf16 v[38:41], v[168:171], v[192:195], v[38:41]
	v_mfma_f32_16x16x32_bf16 v[34:37], v[176:179], v[192:195], v[34:37]
	v_mfma_f32_16x16x32_bf16 v[22:25], v[168:171], v[200:203], v[22:25]
	v_mfma_f32_16x16x32_bf16 v[18:21], v[176:179], v[200:203], v[18:21]
	v_mfma_f32_16x16x32_bf16 v[6:9], v[168:171], v[216:219], v[6:9]
	v_mfma_f32_16x16x32_bf16 v[2:5], v[176:179], v[216:219], v[2:5]
	s_barrier
	s_add_i32 s94, s94, 2
	s_add_u32 s48, s48, 0x100
	s_addc_u32 s49, s49, 0
	s_cmp_gt_u32 s94, 13
	s_cbranch_scc0 .LBB0_684
	s_add_u32 s48, s8, 0xffffff00
	s_addc_u32 s49, s9, -1
	s_andn2_b64 vcc, exec, s[42:43]
	s_cbranch_vccnz .LBB0_687
	v_mov_b32_e32 v2, 0
	s_mov_b32 s18, s34
	s_mov_b32 s92, s36
	s_mov_b64 s[30:31], s[46:47]
	s_mov_b32 s68, s58
	v_mov_b32_e32 v3, v2
	v_mov_b32_e32 v4, v2
	v_mov_b32_e32 v5, v2
	v_mov_b32_e32 v6, v2
	v_mov_b32_e32 v7, v2
	v_mov_b32_e32 v8, v2
	v_mov_b32_e32 v9, v2
	v_mov_b32_e32 v18, v2
	v_mov_b32_e32 v19, v2
	v_mov_b32_e32 v20, v2
	v_mov_b32_e32 v21, v2
	v_mov_b32_e32 v22, v2
	v_mov_b32_e32 v23, v2
	v_mov_b32_e32 v24, v2
	v_mov_b32_e32 v25, v2
	v_mov_b32_e32 v34, v2
	v_mov_b32_e32 v35, v2
	v_mov_b32_e32 v36, v2
	v_mov_b32_e32 v37, v2
	v_mov_b32_e32 v38, v2
	v_mov_b32_e32 v39, v2
	v_mov_b32_e32 v40, v2
	v_mov_b32_e32 v41, v2
	v_mov_b32_e32 v50, v2
	v_mov_b32_e32 v51, v2
	v_mov_b32_e32 v52, v2
	v_mov_b32_e32 v53, v2
	v_mov_b32_e32 v54, v2
	v_mov_b32_e32 v55, v2
	v_mov_b32_e32 v56, v2
	v_mov_b32_e32 v57, v2
	v_mov_b32_e32 v10, v2
	v_mov_b32_e32 v11, v2
	v_mov_b32_e32 v12, v2
	v_mov_b32_e32 v13, v2
	v_mov_b32_e32 v14, v2
	v_mov_b32_e32 v15, v2
	v_mov_b32_e32 v16, v2
	v_mov_b32_e32 v17, v2
	v_mov_b32_e32 v26, v2
	v_mov_b32_e32 v27, v2
	v_mov_b32_e32 v28, v2
	v_mov_b32_e32 v29, v2
	v_mov_b32_e32 v30, v2
	v_mov_b32_e32 v31, v2
	v_mov_b32_e32 v32, v2
	v_mov_b32_e32 v33, v2
	v_mov_b32_e32 v42, v2
	v_mov_b32_e32 v43, v2
	v_mov_b32_e32 v44, v2
	v_mov_b32_e32 v45, v2
	v_mov_b32_e32 v46, v2
	v_mov_b32_e32 v47, v2
	v_mov_b32_e32 v48, v2
	v_mov_b32_e32 v49, v2
	v_mov_b32_e32 v58, v2
	v_mov_b32_e32 v59, v2
	v_mov_b32_e32 v60, v2
	v_mov_b32_e32 v61, v2
	v_mov_b32_e32 v62, v2
	v_mov_b32_e32 v63, v2
	v_mov_b32_e32 v64, v2
	v_mov_b32_e32 v65, v2
	v_mov_b32_e32 v66, v2
	v_mov_b32_e32 v67, v2
	v_mov_b32_e32 v68, v2
	v_mov_b32_e32 v69, v2
	v_mov_b32_e32 v70, v2
	v_mov_b32_e32 v71, v2
	v_mov_b32_e32 v72, v2
	v_mov_b32_e32 v73, v2
	v_mov_b32_e32 v82, v2
	v_mov_b32_e32 v83, v2
	v_mov_b32_e32 v84, v2
	v_mov_b32_e32 v85, v2
	v_mov_b32_e32 v86, v2
	v_mov_b32_e32 v87, v2
	v_mov_b32_e32 v88, v2
	v_mov_b32_e32 v89, v2
	v_mov_b32_e32 v98, v2
	v_mov_b32_e32 v99, v2
	v_mov_b32_e32 v100, v2
	v_mov_b32_e32 v101, v2
	v_mov_b32_e32 v102, v2
	v_mov_b32_e32 v103, v2
	v_mov_b32_e32 v104, v2
	v_mov_b32_e32 v105, v2
	v_mov_b32_e32 v114, v2
	v_mov_b32_e32 v115, v2
	v_mov_b32_e32 v116, v2
	v_mov_b32_e32 v117, v2
	v_mov_b32_e32 v122, v2
	v_mov_b32_e32 v123, v2
	v_mov_b32_e32 v124, v2
	v_mov_b32_e32 v125, v2
	v_mov_b32_e32 v74, v2
	v_mov_b32_e32 v75, v2
	v_mov_b32_e32 v76, v2
	v_mov_b32_e32 v77, v2
	v_mov_b32_e32 v78, v2
	v_mov_b32_e32 v79, v2
	v_mov_b32_e32 v80, v2
	v_mov_b32_e32 v81, v2
	v_mov_b32_e32 v90, v2
	v_mov_b32_e32 v91, v2
	v_mov_b32_e32 v92, v2
	v_mov_b32_e32 v93, v2
	v_mov_b32_e32 v94, v2
	v_mov_b32_e32 v95, v2
	v_mov_b32_e32 v96, v2
	v_mov_b32_e32 v97, v2
	v_mov_b32_e32 v106, v2
	v_mov_b32_e32 v107, v2
	v_mov_b32_e32 v108, v2
	v_mov_b32_e32 v109, v2
	v_mov_b32_e32 v110, v2
	v_mov_b32_e32 v111, v2
	v_mov_b32_e32 v112, v2
	v_mov_b32_e32 v113, v2
	v_mov_b32_e32 v130, v2
	v_mov_b32_e32 v131, v2
	v_mov_b32_e32 v132, v2
	v_mov_b32_e32 v133, v2
	v_mov_b32_e32 v134, v2
	v_mov_b32_e32 v135, v2
	v_mov_b32_e32 v136, v2
	v_mov_b32_e32 v137, v2
	s_branch .LBB0_688

.LBB0_836:
	s_add_u32 s28, s6, 0xfffc0080
	s_addc_u32 s29, s7, -1
	s_add_i32 s41, 0, 0x10000
	s_cmp_eq_u32 s40, 12
	s_cselect_b32 s31, s5, s29
	s_cselect_b32 s30, s8, s28
	s_cselect_b32 s29, s9, s33
	s_cselect_b32 s28, s21, s23
	s_add_i32 s53, 0, 0x14000
	s_add_i32 m0, s43, 0xc000
	s_nop 0
	global_load_lds_dwordx4 v166, s[6:7]
	s_add_i32 m0, s43, 0xe000
	s_nop 0
	global_load_lds_dwordx4 v164, s[6:7]
	ds_read_b128 v[130:133], v165
	ds_read_b128 v[134:137], v165 offset:1024
	ds_read_b128 v[138:141], v165 offset:2048
	ds_read_b128 v[142:145], v165 offset:3072
	ds_read_b128 v[146:149], v165 offset:16384
	ds_read_b128 v[150:153], v165 offset:17408
	ds_read_b128 v[154:157], v165 offset:18432
	ds_read_b128 v[168:171], v165 offset:19456
	ds_read_b128 v[172:175], v188
	ds_read_b128 v[176:179], v188 offset:1024
	ds_read_b128 v[180:183], v188 offset:2048
	ds_read_b128 v[190:193], v188 offset:3072
	ds_read_b128 v[194:197], v188 offset:4096
	ds_read_b128 v[198:201], v188 offset:5120
	ds_read_b128 v[202:205], v188 offset:6144
	ds_read_b128 v[206:209], v188 offset:7168
	s_waitcnt vmcnt(8) lgkmcnt(0)
	s_barrier
	v_mfma_f32_16x16x32_bf16 v[126:129], v[130:133], v[172:175], v[126:129]
	v_mfma_f32_16x16x32_bf16 v[122:125], v[138:141], v[172:175], v[122:125]
	v_mfma_f32_16x16x32_bf16 v[114:117], v[130:133], v[180:183], v[114:117]
	v_mfma_f32_16x16x32_bf16 v[106:109], v[138:141], v[180:183], v[106:109]
	v_mfma_f32_16x16x32_bf16 v[98:101], v[130:133], v[194:197], v[98:101]
	v_mfma_f32_16x16x32_bf16 v[90:93], v[138:141], v[194:197], v[90:93]
	v_mfma_f32_16x16x32_bf16 v[82:85], v[130:133], v[202:205], v[82:85]
	v_mfma_f32_16x16x32_bf16 v[74:77], v[138:141], v[202:205], v[74:77]
	v_mfma_f32_16x16x32_bf16 v[126:129], v[134:137], v[176:179], v[126:129]
	v_mfma_f32_16x16x32_bf16 v[122:125], v[142:145], v[176:179], v[122:125]
	v_mfma_f32_16x16x32_bf16 v[114:117], v[134:137], v[190:193], v[114:117]
	v_mfma_f32_16x16x32_bf16 v[106:109], v[142:145], v[190:193], v[106:109]
	v_mfma_f32_16x16x32_bf16 v[98:101], v[134:137], v[198:201], v[98:101]
	v_mfma_f32_16x16x32_bf16 v[90:93], v[142:145], v[198:201], v[90:93]
	v_mfma_f32_16x16x32_bf16 v[82:85], v[134:137], v[206:209], v[82:85]
	v_mfma_f32_16x16x32_bf16 v[74:77], v[142:145], v[206:209], v[74:77]
	v_mfma_f32_16x16x32_bf16 v[118:121], v[146:149], v[172:175], v[118:121]
	v_mfma_f32_16x16x32_bf16 v[110:113], v[154:157], v[172:175], v[110:113]
	v_mfma_f32_16x16x32_bf16 v[102:105], v[146:149], v[180:183], v[102:105]
	v_mfma_f32_16x16x32_bf16 v[94:97], v[154:157], v[180:183], v[94:97]
	v_mfma_f32_16x16x32_bf16 v[86:89], v[146:149], v[194:197], v[86:89]
	v_mfma_f32_16x16x32_bf16 v[78:81], v[154:157], v[194:197], v[78:81]
	v_mfma_f32_16x16x32_bf16 v[70:73], v[146:149], v[202:205], v[70:73]
	v_mfma_f32_16x16x32_bf16 v[66:69], v[154:157], v[202:205], v[66:69]
	v_mfma_f32_16x16x32_bf16 v[118:121], v[150:153], v[176:179], v[118:121]
	v_mfma_f32_16x16x32_bf16 v[110:113], v[168:171], v[176:179], v[110:113]
	v_mfma_f32_16x16x32_bf16 v[102:105], v[150:153], v[190:193], v[102:105]
	v_mfma_f32_16x16x32_bf16 v[94:97], v[168:171], v[190:193], v[94:97]
	v_mfma_f32_16x16x32_bf16 v[86:89], v[150:153], v[198:201], v[86:89]
	v_mfma_f32_16x16x32_bf16 v[78:81], v[168:171], v[198:201], v[78:81]
	v_mfma_f32_16x16x32_bf16 v[70:73], v[150:153], v[206:209], v[70:73]
	v_mfma_f32_16x16x32_bf16 v[66:69], v[168:171], v[206:209], v[66:69]
	s_barrier
	s_add_i32 s41, s41, s42
	v_lshl_add_u64 v[216:217], s[28:29], 0, v[0:1]
	s_mov_b32 m0, s41
	s_nop 0
	global_load_lds_dwordx4 v0, s[28:29]
	s_add_i32 m0, s41, 0x2000
	s_add_u32 s58, s28, 0x40000
	v_lshl_add_u64 v[218:219], s[28:29], 0, v[158:159]
	s_addc_u32 s59, s29, 0
	s_add_i32 s41, s53, s42
	global_load_lds_dwordx4 v158, s[28:29]
	s_mov_b32 m0, s41
	v_lshl_add_u64 v[222:223], s[30:31], 0, v[160:161]
	global_load_lds_dwordx4 v0, s[58:59]
	s_add_i32 m0, s41, 0x2000
	s_nop 0
	global_load_lds_dwordx4 v158, s[58:59]
	s_mov_b32 m0, s43
	v_lshl_add_u64 v[220:221], s[30:31], 0, v[162:163]
	global_load_lds_dwordx4 v162, s[30:31]
	s_mov_b32 m0, s44
	s_nop 0
	global_load_lds_dwordx4 v160, s[30:31]
	ds_read_b128 v[172:175], v188 offset:16384
	ds_read_b128 v[176:179], v188 offset:17408
	ds_read_b128 v[180:183], v188 offset:18432
	ds_read_b128 v[190:193], v188 offset:19456
	ds_read_b128 v[194:197], v188 offset:20480
	ds_read_b128 v[198:201], v188 offset:21504
	ds_read_b128 v[202:205], v188 offset:22528
	ds_read_b128 v[206:209], v188 offset:23552
	s_waitcnt vmcnt(8) lgkmcnt(0)
	s_barrier
	v_mfma_f32_16x16x32_bf16 v[62:65], v[130:133], v[172:175], v[62:65]
	v_mfma_f32_16x16x32_bf16 v[58:61], v[138:141], v[172:175], v[58:61]
	v_mfma_f32_16x16x32_bf16 v[50:53], v[130:133], v[180:183], v[50:53]
	v_mfma_f32_16x16x32_bf16 v[42:45], v[138:141], v[180:183], v[42:45]
	v_mfma_f32_16x16x32_bf16 v[34:37], v[130:133], v[194:197], v[34:37]
	v_mfma_f32_16x16x32_bf16 v[26:29], v[138:141], v[194:197], v[26:29]
	v_mfma_f32_16x16x32_bf16 v[18:21], v[130:133], v[202:205], v[18:21]
	v_mfma_f32_16x16x32_bf16 v[10:13], v[138:141], v[202:205], v[10:13]
	v_mfma_f32_16x16x32_bf16 v[62:65], v[134:137], v[176:179], v[62:65]
	v_mfma_f32_16x16x32_bf16 v[58:61], v[142:145], v[176:179], v[58:61]
	v_mfma_f32_16x16x32_bf16 v[50:53], v[134:137], v[190:193], v[50:53]
	v_mfma_f32_16x16x32_bf16 v[42:45], v[142:145], v[190:193], v[42:45]
	v_mfma_f32_16x16x32_bf16 v[34:37], v[134:137], v[198:201], v[34:37]
	v_mfma_f32_16x16x32_bf16 v[26:29], v[142:145], v[198:201], v[26:29]
	v_mfma_f32_16x16x32_bf16 v[18:21], v[134:137], v[206:209], v[18:21]
	v_mfma_f32_16x16x32_bf16 v[10:13], v[142:145], v[206:209], v[10:13]
	v_mfma_f32_16x16x32_bf16 v[54:57], v[146:149], v[172:175], v[54:57]
	v_mfma_f32_16x16x32_bf16 v[46:49], v[154:157], v[172:175], v[46:49]
	v_mfma_f32_16x16x32_bf16 v[38:41], v[146:149], v[180:183], v[38:41]
	v_mfma_f32_16x16x32_bf16 v[30:33], v[154:157], v[180:183], v[30:33]
	v_mfma_f32_16x16x32_bf16 v[22:25], v[146:149], v[194:197], v[22:25]
	v_mfma_f32_16x16x32_bf16 v[14:17], v[154:157], v[194:197], v[14:17]
	v_mfma_f32_16x16x32_bf16 v[6:9], v[146:149], v[202:205], v[6:9]
	v_mfma_f32_16x16x32_bf16 v[2:5], v[154:157], v[202:205], v[2:5]
	v_mfma_f32_16x16x32_bf16 v[54:57], v[150:153], v[176:179], v[54:57]
	v_mfma_f32_16x16x32_bf16 v[46:49], v[168:171], v[176:179], v[46:49]
	v_mfma_f32_16x16x32_bf16 v[38:41], v[150:153], v[190:193], v[38:41]
	v_mfma_f32_16x16x32_bf16 v[30:33], v[168:171], v[190:193], v[30:33]
	v_mfma_f32_16x16x32_bf16 v[22:25], v[150:153], v[198:201], v[22:25]
	v_mfma_f32_16x16x32_bf16 v[14:17], v[168:171], v[198:201], v[14:17]
	v_mfma_f32_16x16x32_bf16 v[6:9], v[150:153], v[206:209], v[6:9]
	v_mfma_f32_16x16x32_bf16 v[2:5], v[168:171], v[206:209], v[2:5]
	s_barrier
	s_add_i32 s41, 0, 0x18000
	s_add_i32 s53, 0, 0x1c000
	s_add_u32 s30, s30, 0x40000
	s_addc_u32 s31, s31, 0
	s_mov_b32 m0, s45
	s_nop 0
	global_load_lds_dwordx4 v162, s[30:31]
	s_mov_b32 m0, s46
	s_nop 0
	global_load_lds_dwordx4 v160, s[30:31]
	ds_read_b128 v[130:133], v165 offset:32768
	ds_read_b128 v[134:137], v165 offset:33792
	ds_read_b128 v[138:141], v165 offset:34816
	ds_read_b128 v[142:145], v165 offset:35840
	ds_read_b128 v[146:149], v165 offset:49152
	ds_read_b128 v[150:153], v165 offset:50176
	ds_read_b128 v[154:157], v165 offset:51200
	ds_read_b128 v[168:171], v165 offset:52224
	ds_read_b128 v[172:175], v188 offset:32768
	ds_read_b128 v[176:179], v188 offset:33792
	ds_read_b128 v[180:183], v188 offset:34816
	ds_read_b128 v[190:193], v188 offset:35840
	ds_read_b128 v[194:197], v188 offset:36864
	ds_read_b128 v[198:201], v188 offset:37888
	ds_read_b128 v[202:205], v188 offset:38912
	ds_read_b128 v[206:209], v188 offset:39936
	s_waitcnt vmcnt(8) lgkmcnt(0)
	s_barrier
	v_mfma_f32_16x16x32_bf16 v[126:129], v[130:133], v[172:175], v[126:129]
	v_mfma_f32_16x16x32_bf16 v[122:125], v[138:141], v[172:175], v[122:125]
	v_mfma_f32_16x16x32_bf16 v[114:117], v[130:133], v[180:183], v[114:117]
	v_mfma_f32_16x16x32_bf16 v[106:109], v[138:141], v[180:183], v[106:109]
	v_mfma_f32_16x16x32_bf16 v[98:101], v[130:133], v[194:197], v[98:101]
	v_mfma_f32_16x16x32_bf16 v[90:93], v[138:141], v[194:197], v[90:93]
	v_mfma_f32_16x16x32_bf16 v[82:85], v[130:133], v[202:205], v[82:85]
	v_mfma_f32_16x16x32_bf16 v[74:77], v[138:141], v[202:205], v[74:77]
	v_mfma_f32_16x16x32_bf16 v[126:129], v[134:137], v[176:179], v[126:129]
	v_mfma_f32_16x16x32_bf16 v[122:125], v[142:145], v[176:179], v[122:125]
	v_mfma_f32_16x16x32_bf16 v[114:117], v[134:137], v[190:193], v[114:117]
	v_mfma_f32_16x16x32_bf16 v[106:109], v[142:145], v[190:193], v[106:109]
	v_mfma_f32_16x16x32_bf16 v[98:101], v[134:137], v[198:201], v[98:101]
	v_mfma_f32_16x16x32_bf16 v[90:93], v[142:145], v[198:201], v[90:93]
	v_mfma_f32_16x16x32_bf16 v[82:85], v[134:137], v[206:209], v[82:85]
	v_mfma_f32_16x16x32_bf16 v[74:77], v[142:145], v[206:209], v[74:77]
	v_mfma_f32_16x16x32_bf16 v[118:121], v[146:149], v[172:175], v[118:121]
	v_mfma_f32_16x16x32_bf16 v[110:113], v[154:157], v[172:175], v[110:113]
	v_mfma_f32_16x16x32_bf16 v[102:105], v[146:149], v[180:183], v[102:105]
	v_mfma_f32_16x16x32_bf16 v[94:97], v[154:157], v[180:183], v[94:97]
	v_mfma_f32_16x16x32_bf16 v[86:89], v[146:149], v[194:197], v[86:89]
	v_mfma_f32_16x16x32_bf16 v[78:81], v[154:157], v[194:197], v[78:81]
	v_mfma_f32_16x16x32_bf16 v[70:73], v[146:149], v[202:205], v[70:73]
	v_mfma_f32_16x16x32_bf16 v[66:69], v[154:157], v[202:205], v[66:69]
	v_mfma_f32_16x16x32_bf16 v[118:121], v[150:153], v[176:179], v[118:121]
	v_mfma_f32_16x16x32_bf16 v[110:113], v[168:171], v[176:179], v[110:113]
	v_mfma_f32_16x16x32_bf16 v[102:105], v[150:153], v[190:193], v[102:105]
	v_mfma_f32_16x16x32_bf16 v[94:97], v[168:171], v[190:193], v[94:97]
	v_mfma_f32_16x16x32_bf16 v[86:89], v[150:153], v[198:201], v[86:89]
	v_mfma_f32_16x16x32_bf16 v[78:81], v[168:171], v[198:201], v[78:81]
	v_mfma_f32_16x16x32_bf16 v[70:73], v[150:153], v[206:209], v[70:73]
	v_mfma_f32_16x16x32_bf16 v[66:69], v[168:171], v[206:209], v[66:69]
	s_barrier
	s_add_i32 s30, s41, s42
	v_lshl_add_u64 v[216:217], v[216:217], 0, s[56:57]
	s_mov_b32 m0, s30
	s_nop 0
	global_load_lds_dwordx4 v[216:217], off
	s_add_i32 m0, s30, 0x2000
	s_add_u32 s28, s28, 0x40080
	v_lshl_add_u64 v[216:217], v[218:219], 0, s[56:57]
	s_addc_u32 s29, s29, 0
	s_add_i32 s30, s53, s42
	global_load_lds_dwordx4 v[216:217], off
	s_mov_b32 m0, s30
	s_nop 0
	global_load_lds_dwordx4 v0, s[28:29]
	s_add_i32 m0, s30, 0x2000
	s_nop 0
	global_load_lds_dwordx4 v158, s[28:29]
	s_mov_b32 m0, s47
	v_lshl_add_u64 v[216:217], v[220:221], 0, s[56:57]
	global_load_lds_dwordx4 v[216:217], off
	s_mov_b32 m0, s48
	v_lshl_add_u64 v[216:217], v[222:223], 0, s[56:57]
	global_load_lds_dwordx4 v[216:217], off
	ds_read_b128 v[172:175], v188 offset:49152
	ds_read_b128 v[176:179], v188 offset:50176
	ds_read_b128 v[180:183], v188 offset:51200
	ds_read_b128 v[190:193], v188 offset:52224
	ds_read_b128 v[194:197], v188 offset:53248
	ds_read_b128 v[198:201], v188 offset:54272
	ds_read_b128 v[202:205], v188 offset:55296
	ds_read_b128 v[206:209], v188 offset:56320
	s_waitcnt vmcnt(8) lgkmcnt(0)
	s_barrier
	v_mfma_f32_16x16x32_bf16 v[62:65], v[130:133], v[172:175], v[62:65]
	v_mfma_f32_16x16x32_bf16 v[58:61], v[138:141], v[172:175], v[58:61]
	v_mfma_f32_16x16x32_bf16 v[50:53], v[130:133], v[180:183], v[50:53]
	v_mfma_f32_16x16x32_bf16 v[42:45], v[138:141], v[180:183], v[42:45]
	v_mfma_f32_16x16x32_bf16 v[34:37], v[130:133], v[194:197], v[34:37]
	v_mfma_f32_16x16x32_bf16 v[26:29], v[138:141], v[194:197], v[26:29]
	v_mfma_f32_16x16x32_bf16 v[18:21], v[130:133], v[202:205], v[18:21]
	v_mfma_f32_16x16x32_bf16 v[10:13], v[138:141], v[202:205], v[10:13]
	v_mfma_f32_16x16x32_bf16 v[62:65], v[134:137], v[176:179], v[62:65]
	v_mfma_f32_16x16x32_bf16 v[58:61], v[142:145], v[176:179], v[58:61]
	v_mfma_f32_16x16x32_bf16 v[50:53], v[134:137], v[190:193], v[50:53]
	v_mfma_f32_16x16x32_bf16 v[42:45], v[142:145], v[190:193], v[42:45]
	v_mfma_f32_16x16x32_bf16 v[34:37], v[134:137], v[198:201], v[34:37]
	v_mfma_f32_16x16x32_bf16 v[26:29], v[142:145], v[198:201], v[26:29]
	v_mfma_f32_16x16x32_bf16 v[18:21], v[134:137], v[206:209], v[18:21]
	v_mfma_f32_16x16x32_bf16 v[10:13], v[142:145], v[206:209], v[10:13]
	v_mfma_f32_16x16x32_bf16 v[54:57], v[146:149], v[172:175], v[54:57]
	v_mfma_f32_16x16x32_bf16 v[46:49], v[154:157], v[172:175], v[46:49]
	v_mfma_f32_16x16x32_bf16 v[38:41], v[146:149], v[180:183], v[38:41]
	v_mfma_f32_16x16x32_bf16 v[30:33], v[154:157], v[180:183], v[30:33]
	v_mfma_f32_16x16x32_bf16 v[22:25], v[146:149], v[194:197], v[22:25]
	v_mfma_f32_16x16x32_bf16 v[14:17], v[154:157], v[194:197], v[14:17]
	v_mfma_f32_16x16x32_bf16 v[6:9], v[146:149], v[202:205], v[6:9]
	v_mfma_f32_16x16x32_bf16 v[2:5], v[154:157], v[202:205], v[2:5]
	v_mfma_f32_16x16x32_bf16 v[54:57], v[150:153], v[176:179], v[54:57]
	v_mfma_f32_16x16x32_bf16 v[46:49], v[168:171], v[176:179], v[46:49]
	v_mfma_f32_16x16x32_bf16 v[38:41], v[150:153], v[190:193], v[38:41]
	v_mfma_f32_16x16x32_bf16 v[30:33], v[168:171], v[190:193], v[30:33]
	v_mfma_f32_16x16x32_bf16 v[22:25], v[150:153], v[198:201], v[22:25]
	v_mfma_f32_16x16x32_bf16 v[14:17], v[168:171], v[198:201], v[14:17]
	v_mfma_f32_16x16x32_bf16 v[6:9], v[150:153], v[206:209], v[6:9]
	v_mfma_f32_16x16x32_bf16 v[2:5], v[168:171], v[206:209], v[2:5]
	s_barrier
	s_add_i32 s40, s40, 2
	s_add_u32 s23, s23, 0x100
	s_addc_u32 s33, s33, 0
	s_add_u32 s6, s6, 0x100
	s_addc_u32 s7, s7, 0
	s_cmp_gt_u32 s40, 13
	s_cbranch_scc0 .LBB0_836
	s_and_b64 vcc, exec, s[18:19]
	s_cbranch_vccz .LBB0_839
	s_barrier

.LBB0_1525:
	s_add_u32 s36, s26, s34
	s_addc_u32 s37, s27, s35
	s_add_u32 s36, s36, 0x100
	s_addc_u32 s37, s37, 0
	s_add_u32 s82, s8, s34
	s_addc_u32 s83, s9, s35
	s_add_i32 s84, 0, 0x10000
	s_cmpk_eq_i32 s34, 0xb00
	s_cselect_b32 s45, s31, s37
	s_cselect_b32 s44, s30, s36
	s_cselect_b32 s37, s29, s83
	s_cselect_b32 s36, s28, s82
	s_add_i32 s85, 0, 0x14000
	v_lshl_add_u64 v[208:209], v[142:143], 0, s[34:35]
	s_add_i32 m0, s4, 0xc000
	s_nop 0
	global_load_lds_dwordx4 v[208:209], off
	s_add_i32 m0, s4, 0xe000
	v_lshl_add_u64 v[208:209], v[140:141], 0, s[34:35]
	global_load_lds_dwordx4 v[208:209], off
	ds_read_b128 v[146:149], v241
	ds_read_b128 v[150:153], v241 offset:1024
	ds_read_b128 v[154:157], v241 offset:2048
	ds_read_b128 v[158:161], v241 offset:3072
	ds_read_b128 v[162:165], v241 offset:16384
	ds_read_b128 v[168:171], v241 offset:17408
	ds_read_b128 v[172:175], v241 offset:18432
	ds_read_b128 v[176:179], v241 offset:19456
	ds_read_b128 v[180:183], v145
	ds_read_b128 v[184:187], v145 offset:1024
	ds_read_b128 v[188:191], v145 offset:2048
	ds_read_b128 v[192:195], v145 offset:3072
	ds_read_b128 v[196:199], v145 offset:4096
	ds_read_b128 v[200:203], v145 offset:5120
	ds_read_b128 v[204:207], v145 offset:6144
	ds_read_b128 v[216:219], v145 offset:7168
	s_waitcnt vmcnt(8) lgkmcnt(0)
	s_barrier
	v_mfma_f32_16x16x32_bf16 v[134:137], v[146:149], v[180:183], v[134:137]
	v_mfma_f32_16x16x32_bf16 v[130:133], v[154:157], v[180:183], v[130:133]
	v_mfma_f32_16x16x32_bf16 v[110:113], v[146:149], v[188:191], v[110:113]
	v_mfma_f32_16x16x32_bf16 v[106:109], v[154:157], v[188:191], v[106:109]
	v_mfma_f32_16x16x32_bf16 v[94:97], v[146:149], v[196:199], v[94:97]
	v_mfma_f32_16x16x32_bf16 v[90:93], v[154:157], v[196:199], v[90:93]
	v_mfma_f32_16x16x32_bf16 v[78:81], v[146:149], v[204:207], v[78:81]
	v_mfma_f32_16x16x32_bf16 v[74:77], v[154:157], v[204:207], v[74:77]
	v_mfma_f32_16x16x32_bf16 v[134:137], v[150:153], v[184:187], v[134:137]
	v_mfma_f32_16x16x32_bf16 v[130:133], v[158:161], v[184:187], v[130:133]
	v_mfma_f32_16x16x32_bf16 v[110:113], v[150:153], v[192:195], v[110:113]
	v_mfma_f32_16x16x32_bf16 v[106:109], v[158:161], v[192:195], v[106:109]
	v_mfma_f32_16x16x32_bf16 v[94:97], v[150:153], v[200:203], v[94:97]
	v_mfma_f32_16x16x32_bf16 v[90:93], v[158:161], v[200:203], v[90:93]
	v_mfma_f32_16x16x32_bf16 v[78:81], v[150:153], v[216:219], v[78:81]
	v_mfma_f32_16x16x32_bf16 v[74:77], v[158:161], v[216:219], v[74:77]
	v_mfma_f32_16x16x32_bf16 v[122:125], v[162:165], v[180:183], v[122:125]
	v_mfma_f32_16x16x32_bf16 v[114:117], v[172:175], v[180:183], v[114:117]
	v_mfma_f32_16x16x32_bf16 v[102:105], v[162:165], v[188:191], v[102:105]
	v_mfma_f32_16x16x32_bf16 v[98:101], v[172:175], v[188:191], v[98:101]
	v_mfma_f32_16x16x32_bf16 v[86:89], v[162:165], v[196:199], v[86:89]
	v_mfma_f32_16x16x32_bf16 v[82:85], v[172:175], v[196:199], v[82:85]
	v_mfma_f32_16x16x32_bf16 v[70:73], v[162:165], v[204:207], v[70:73]
	v_mfma_f32_16x16x32_bf16 v[66:69], v[172:175], v[204:207], v[66:69]
	v_mfma_f32_16x16x32_bf16 v[122:125], v[168:171], v[184:187], v[122:125]
	v_mfma_f32_16x16x32_bf16 v[114:117], v[176:179], v[184:187], v[114:117]
	v_mfma_f32_16x16x32_bf16 v[102:105], v[168:171], v[192:195], v[102:105]
	v_mfma_f32_16x16x32_bf16 v[98:101], v[176:179], v[192:195], v[98:101]
	v_mfma_f32_16x16x32_bf16 v[86:89], v[168:171], v[200:203], v[86:89]
	v_mfma_f32_16x16x32_bf16 v[82:85], v[176:179], v[200:203], v[82:85]
	v_mfma_f32_16x16x32_bf16 v[70:73], v[168:171], v[216:219], v[70:73]
	v_mfma_f32_16x16x32_bf16 v[66:69], v[176:179], v[216:219], v[66:69]
	s_barrier
	s_add_i32 s82, s84, s70
	v_lshl_add_u64 v[208:209], s[36:37], 0, v[0:1]
	s_mov_b32 m0, s82
	s_nop 0
	global_load_lds_dwordx4 v0, s[36:37]
	s_add_i32 m0, s82, 0x2000
	s_add_u32 s82, s36, 0x60000
	v_lshl_add_u64 v[220:221], s[36:37], 0, v[118:119]
	s_addc_u32 s83, s37, 0
	s_add_i32 s84, s85, s70
	global_load_lds_dwordx4 v118, s[36:37]
	s_mov_b32 m0, s84
	v_lshl_add_u64 v[224:225], s[44:45], 0, v[120:121]
	global_load_lds_dwordx4 v0, s[82:83]
	s_add_i32 m0, s84, 0x2000
	s_nop 0
	global_load_lds_dwordx4 v118, s[82:83]
	s_mov_b32 m0, s4
	v_lshl_add_u64 v[222:223], s[44:45], 0, v[126:127]
	global_load_lds_dwordx4 v126, s[44:45]
	s_mov_b32 m0, s33
	s_nop 0
	global_load_lds_dwordx4 v120, s[44:45]
	ds_read_b128 v[180:183], v145 offset:16384
	ds_read_b128 v[184:187], v145 offset:17408
	ds_read_b128 v[188:191], v145 offset:18432
	ds_read_b128 v[192:195], v145 offset:19456
	ds_read_b128 v[196:199], v145 offset:20480
	ds_read_b128 v[200:203], v145 offset:21504
	ds_read_b128 v[204:207], v145 offset:22528
	ds_read_b128 v[216:219], v145 offset:23552
	s_waitcnt vmcnt(8) lgkmcnt(0)
	s_barrier
	v_mfma_f32_16x16x32_bf16 v[62:65], v[146:149], v[180:183], v[62:65]
	v_mfma_f32_16x16x32_bf16 v[58:61], v[154:157], v[180:183], v[58:61]
	v_mfma_f32_16x16x32_bf16 v[46:49], v[146:149], v[188:191], v[46:49]
	v_mfma_f32_16x16x32_bf16 v[42:45], v[154:157], v[188:191], v[42:45]
	v_mfma_f32_16x16x32_bf16 v[30:33], v[146:149], v[196:199], v[30:33]
	v_mfma_f32_16x16x32_bf16 v[26:29], v[154:157], v[196:199], v[26:29]
	v_mfma_f32_16x16x32_bf16 v[14:17], v[146:149], v[204:207], v[14:17]
	v_mfma_f32_16x16x32_bf16 v[10:13], v[154:157], v[204:207], v[10:13]
	v_mfma_f32_16x16x32_bf16 v[62:65], v[150:153], v[184:187], v[62:65]
	v_mfma_f32_16x16x32_bf16 v[58:61], v[158:161], v[184:187], v[58:61]
	v_mfma_f32_16x16x32_bf16 v[46:49], v[150:153], v[192:195], v[46:49]
	v_mfma_f32_16x16x32_bf16 v[42:45], v[158:161], v[192:195], v[42:45]
	v_mfma_f32_16x16x32_bf16 v[30:33], v[150:153], v[200:203], v[30:33]
	v_mfma_f32_16x16x32_bf16 v[26:29], v[158:161], v[200:203], v[26:29]
	v_mfma_f32_16x16x32_bf16 v[14:17], v[150:153], v[216:219], v[14:17]
	v_mfma_f32_16x16x32_bf16 v[10:13], v[158:161], v[216:219], v[10:13]
	v_mfma_f32_16x16x32_bf16 v[54:57], v[162:165], v[180:183], v[54:57]
	v_mfma_f32_16x16x32_bf16 v[50:53], v[172:175], v[180:183], v[50:53]
	v_mfma_f32_16x16x32_bf16 v[38:41], v[162:165], v[188:191], v[38:41]
	v_mfma_f32_16x16x32_bf16 v[34:37], v[172:175], v[188:191], v[34:37]
	v_mfma_f32_16x16x32_bf16 v[22:25], v[162:165], v[196:199], v[22:25]
	v_mfma_f32_16x16x32_bf16 v[18:21], v[172:175], v[196:199], v[18:21]
	v_mfma_f32_16x16x32_bf16 v[6:9], v[162:165], v[204:207], v[6:9]
	v_mfma_f32_16x16x32_bf16 v[2:5], v[172:175], v[204:207], v[2:5]
	v_mfma_f32_16x16x32_bf16 v[54:57], v[168:171], v[184:187], v[54:57]
	v_mfma_f32_16x16x32_bf16 v[50:53], v[176:179], v[184:187], v[50:53]
	v_mfma_f32_16x16x32_bf16 v[38:41], v[168:171], v[192:195], v[38:41]
	v_mfma_f32_16x16x32_bf16 v[34:37], v[176:179], v[192:195], v[34:37]
	v_mfma_f32_16x16x32_bf16 v[22:25], v[168:171], v[200:203], v[22:25]
	v_mfma_f32_16x16x32_bf16 v[18:21], v[176:179], v[200:203], v[18:21]
	v_mfma_f32_16x16x32_bf16 v[6:9], v[168:171], v[216:219], v[6:9]
	v_mfma_f32_16x16x32_bf16 v[2:5], v[176:179], v[216:219], v[2:5]
	s_barrier
	s_add_i32 s82, 0, 0x18000
	s_add_i32 s83, 0, 0x1c000
	s_add_u32 s44, s44, 0x60000
	s_addc_u32 s45, s45, 0
	s_mov_b32 m0, s71
	s_nop 0
	global_load_lds_dwordx4 v126, s[44:45]
	s_mov_b32 m0, s76
	v_lshl_add_u64 v[242:243], s[44:45], 0, v[120:121]
	global_load_lds_dwordx4 v120, s[44:45]
	ds_read_b128 v[146:149], v241 offset:32768
	ds_read_b128 v[150:153], v241 offset:33792
	ds_read_b128 v[154:157], v241 offset:34816
	ds_read_b128 v[158:161], v241 offset:35840
	ds_read_b128 v[162:165], v241 offset:49152
	ds_read_b128 v[168:171], v241 offset:50176
	ds_read_b128 v[172:175], v241 offset:51200
	ds_read_b128 v[176:179], v241 offset:52224
	ds_read_b128 v[180:183], v145 offset:32768
	ds_read_b128 v[184:187], v145 offset:33792
	ds_read_b128 v[188:191], v145 offset:34816
	ds_read_b128 v[192:195], v145 offset:35840
	ds_read_b128 v[196:199], v145 offset:36864
	ds_read_b128 v[200:203], v145 offset:37888
	ds_read_b128 v[204:207], v145 offset:38912
	ds_read_b128 v[216:219], v145 offset:39936
	s_waitcnt vmcnt(8) lgkmcnt(0)
	s_barrier
	v_mfma_f32_16x16x32_bf16 v[134:137], v[146:149], v[180:183], v[134:137]
	v_mfma_f32_16x16x32_bf16 v[130:133], v[154:157], v[180:183], v[130:133]
	v_mfma_f32_16x16x32_bf16 v[110:113], v[146:149], v[188:191], v[110:113]
	v_mfma_f32_16x16x32_bf16 v[106:109], v[154:157], v[188:191], v[106:109]
	v_mfma_f32_16x16x32_bf16 v[94:97], v[146:149], v[196:199], v[94:97]
	v_mfma_f32_16x16x32_bf16 v[90:93], v[154:157], v[196:199], v[90:93]
	v_mfma_f32_16x16x32_bf16 v[78:81], v[146:149], v[204:207], v[78:81]
	v_mfma_f32_16x16x32_bf16 v[74:77], v[154:157], v[204:207], v[74:77]
	v_mfma_f32_16x16x32_bf16 v[134:137], v[150:153], v[184:187], v[134:137]
	v_mfma_f32_16x16x32_bf16 v[130:133], v[158:161], v[184:187], v[130:133]
	v_mfma_f32_16x16x32_bf16 v[110:113], v[150:153], v[192:195], v[110:113]
	v_mfma_f32_16x16x32_bf16 v[106:109], v[158:161], v[192:195], v[106:109]
	v_mfma_f32_16x16x32_bf16 v[94:97], v[150:153], v[200:203], v[94:97]
	v_mfma_f32_16x16x32_bf16 v[90:93], v[158:161], v[200:203], v[90:93]
	v_mfma_f32_16x16x32_bf16 v[78:81], v[150:153], v[216:219], v[78:81]
	v_mfma_f32_16x16x32_bf16 v[74:77], v[158:161], v[216:219], v[74:77]
	v_mfma_f32_16x16x32_bf16 v[122:125], v[162:165], v[180:183], v[122:125]
	v_mfma_f32_16x16x32_bf16 v[114:117], v[172:175], v[180:183], v[114:117]
	v_mfma_f32_16x16x32_bf16 v[102:105], v[162:165], v[188:191], v[102:105]
	v_mfma_f32_16x16x32_bf16 v[98:101], v[172:175], v[188:191], v[98:101]
	v_mfma_f32_16x16x32_bf16 v[86:89], v[162:165], v[196:199], v[86:89]
	v_mfma_f32_16x16x32_bf16 v[82:85], v[172:175], v[196:199], v[82:85]
	v_mfma_f32_16x16x32_bf16 v[70:73], v[162:165], v[204:207], v[70:73]
	v_mfma_f32_16x16x32_bf16 v[66:69], v[172:175], v[204:207], v[66:69]
	v_mfma_f32_16x16x32_bf16 v[122:125], v[168:171], v[184:187], v[122:125]
	v_mfma_f32_16x16x32_bf16 v[114:117], v[176:179], v[184:187], v[114:117]
	v_mfma_f32_16x16x32_bf16 v[102:105], v[168:171], v[192:195], v[102:105]
	v_mfma_f32_16x16x32_bf16 v[98:101], v[176:179], v[192:195], v[98:101]
	v_mfma_f32_16x16x32_bf16 v[86:89], v[168:171], v[200:203], v[86:89]
	v_mfma_f32_16x16x32_bf16 v[82:85], v[176:179], v[200:203], v[82:85]
	v_mfma_f32_16x16x32_bf16 v[70:73], v[168:171], v[216:219], v[70:73]
	v_mfma_f32_16x16x32_bf16 v[66:69], v[176:179], v[216:219], v[66:69]
	s_barrier
	s_add_i32 s44, s82, s70
	v_lshl_add_u64 v[208:209], v[208:209], 0, s[56:57]
	s_mov_b32 m0, s44
	s_nop 0
	global_load_lds_dwordx4 v[208:209], off
	s_add_i32 m0, s44, 0x2000
	s_add_u32 s36, s36, 0x60080
	v_lshl_add_u64 v[208:209], v[220:221], 0, s[56:57]
	s_addc_u32 s37, s37, 0
	s_add_i32 s44, s83, s70
	global_load_lds_dwordx4 v[208:209], off
	s_mov_b32 m0, s44
	s_nop 0
	global_load_lds_dwordx4 v0, s[36:37]
	s_add_i32 m0, s44, 0x2000
	s_nop 0
	global_load_lds_dwordx4 v118, s[36:37]
	s_mov_b32 m0, s77
	v_lshl_add_u64 v[208:209], v[222:223], 0, s[56:57]
	global_load_lds_dwordx4 v[208:209], off
	s_mov_b32 m0, s79
	v_lshl_add_u64 v[208:209], v[224:225], 0, s[56:57]
	global_load_lds_dwordx4 v[208:209], off
	ds_read_b128 v[180:183], v145 offset:49152
	ds_read_b128 v[184:187], v145 offset:50176
	ds_read_b128 v[188:191], v145 offset:51200
	ds_read_b128 v[192:195], v145 offset:52224
	ds_read_b128 v[196:199], v145 offset:53248
	ds_read_b128 v[200:203], v145 offset:54272
	ds_read_b128 v[204:207], v145 offset:55296
	ds_read_b128 v[216:219], v145 offset:56320
	s_waitcnt vmcnt(8) lgkmcnt(0)
	s_barrier
	v_mfma_f32_16x16x32_bf16 v[62:65], v[146:149], v[180:183], v[62:65]
	v_mfma_f32_16x16x32_bf16 v[58:61], v[154:157], v[180:183], v[58:61]
	v_mfma_f32_16x16x32_bf16 v[46:49], v[146:149], v[188:191], v[46:49]
	v_mfma_f32_16x16x32_bf16 v[42:45], v[154:157], v[188:191], v[42:45]
	v_mfma_f32_16x16x32_bf16 v[30:33], v[146:149], v[196:199], v[30:33]
	v_mfma_f32_16x16x32_bf16 v[26:29], v[154:157], v[196:199], v[26:29]
	v_mfma_f32_16x16x32_bf16 v[14:17], v[146:149], v[204:207], v[14:17]
	v_mfma_f32_16x16x32_bf16 v[10:13], v[154:157], v[204:207], v[10:13]
	v_mfma_f32_16x16x32_bf16 v[62:65], v[150:153], v[184:187], v[62:65]
	v_mfma_f32_16x16x32_bf16 v[58:61], v[158:161], v[184:187], v[58:61]
	v_mfma_f32_16x16x32_bf16 v[46:49], v[150:153], v[192:195], v[46:49]
	v_mfma_f32_16x16x32_bf16 v[42:45], v[158:161], v[192:195], v[42:45]
	v_mfma_f32_16x16x32_bf16 v[30:33], v[150:153], v[200:203], v[30:33]
	v_mfma_f32_16x16x32_bf16 v[26:29], v[158:161], v[200:203], v[26:29]
	v_mfma_f32_16x16x32_bf16 v[14:17], v[150:153], v[216:219], v[14:17]
	v_mfma_f32_16x16x32_bf16 v[10:13], v[158:161], v[216:219], v[10:13]
	v_mfma_f32_16x16x32_bf16 v[54:57], v[162:165], v[180:183], v[54:57]
	v_mfma_f32_16x16x32_bf16 v[50:53], v[172:175], v[180:183], v[50:53]
	v_mfma_f32_16x16x32_bf16 v[38:41], v[162:165], v[188:191], v[38:41]
	v_mfma_f32_16x16x32_bf16 v[34:37], v[172:175], v[188:191], v[34:37]
	v_mfma_f32_16x16x32_bf16 v[22:25], v[162:165], v[196:199], v[22:25]
	v_mfma_f32_16x16x32_bf16 v[18:21], v[172:175], v[196:199], v[18:21]
	v_mfma_f32_16x16x32_bf16 v[6:9], v[162:165], v[204:207], v[6:9]
	v_mfma_f32_16x16x32_bf16 v[2:5], v[172:175], v[204:207], v[2:5]
	v_mfma_f32_16x16x32_bf16 v[54:57], v[168:171], v[184:187], v[54:57]
	v_mfma_f32_16x16x32_bf16 v[50:53], v[176:179], v[184:187], v[50:53]
	v_mfma_f32_16x16x32_bf16 v[38:41], v[168:171], v[192:195], v[38:41]
	v_mfma_f32_16x16x32_bf16 v[34:37], v[176:179], v[192:195], v[34:37]
	v_mfma_f32_16x16x32_bf16 v[22:25], v[168:171], v[200:203], v[22:25]
	v_mfma_f32_16x16x32_bf16 v[18:21], v[176:179], v[200:203], v[18:21]
	v_mfma_f32_16x16x32_bf16 v[6:9], v[168:171], v[216:219], v[6:9]
	v_mfma_f32_16x16x32_bf16 v[2:5], v[176:179], v[216:219], v[2:5]
	s_barrier
	s_add_i32 s59, s59, 2
	s_add_u32 s34, s34, 0x100
	s_addc_u32 s35, s35, 0
	s_cmp_gt_u32 s59, 21
	s_cbranch_scc0 .LBB0_1525
	s_add_u32 s34, s8, 0xffffff00
	s_addc_u32 s35, s9, -1
	s_and_b64 vcc, exec, s[42:43]
	s_cbranch_vccnz .LBB0_1528
	v_mov_b32_e32 v2, 0
	s_mov_b32 s16, s80
	s_mov_b32 s47, s81
	s_mov_b64 s[26:27], s[30:31]
	s_mov_b32 s68, s58
	v_mov_b32_e32 v3, v2
	v_mov_b32_e32 v4, v2
	v_mov_b32_e32 v5, v2
	v_mov_b32_e32 v6, v2
	v_mov_b32_e32 v7, v2
	v_mov_b32_e32 v8, v2
	v_mov_b32_e32 v9, v2
	v_mov_b32_e32 v18, v2
	v_mov_b32_e32 v19, v2
	v_mov_b32_e32 v20, v2
	v_mov_b32_e32 v21, v2
	v_mov_b32_e32 v22, v2
	v_mov_b32_e32 v23, v2
	v_mov_b32_e32 v24, v2
	v_mov_b32_e32 v25, v2
	v_mov_b32_e32 v34, v2
	v_mov_b32_e32 v35, v2
	v_mov_b32_e32 v36, v2
	v_mov_b32_e32 v37, v2
	v_mov_b32_e32 v38, v2
	v_mov_b32_e32 v39, v2
	v_mov_b32_e32 v40, v2
	v_mov_b32_e32 v41, v2
	v_mov_b32_e32 v50, v2
	v_mov_b32_e32 v51, v2
	v_mov_b32_e32 v52, v2
	v_mov_b32_e32 v53, v2
	v_mov_b32_e32 v54, v2
	v_mov_b32_e32 v55, v2
	v_mov_b32_e32 v56, v2
	v_mov_b32_e32 v57, v2
	v_mov_b32_e32 v10, v2
	v_mov_b32_e32 v11, v2
	v_mov_b32_e32 v12, v2
	v_mov_b32_e32 v13, v2
	v_mov_b32_e32 v14, v2
	v_mov_b32_e32 v15, v2
	v_mov_b32_e32 v16, v2
	v_mov_b32_e32 v17, v2
	v_mov_b32_e32 v26, v2
	v_mov_b32_e32 v27, v2
	v_mov_b32_e32 v28, v2
	v_mov_b32_e32 v29, v2
	v_mov_b32_e32 v30, v2
	v_mov_b32_e32 v31, v2
	v_mov_b32_e32 v32, v2
	v_mov_b32_e32 v33, v2
	v_mov_b32_e32 v42, v2
	v_mov_b32_e32 v43, v2
	v_mov_b32_e32 v44, v2
	v_mov_b32_e32 v45, v2
	v_mov_b32_e32 v46, v2
	v_mov_b32_e32 v47, v2
	v_mov_b32_e32 v48, v2
	v_mov_b32_e32 v49, v2
	v_mov_b32_e32 v58, v2
	v_mov_b32_e32 v59, v2
	v_mov_b32_e32 v60, v2
	v_mov_b32_e32 v61, v2
	v_mov_b32_e32 v62, v2
	v_mov_b32_e32 v63, v2
	v_mov_b32_e32 v64, v2
	v_mov_b32_e32 v65, v2
	v_mov_b32_e32 v66, v2
	v_mov_b32_e32 v67, v2
	v_mov_b32_e32 v68, v2
	v_mov_b32_e32 v69, v2
	v_mov_b32_e32 v70, v2
	v_mov_b32_e32 v71, v2
	v_mov_b32_e32 v72, v2
	v_mov_b32_e32 v73, v2
	v_mov_b32_e32 v82, v2
	v_mov_b32_e32 v83, v2
	v_mov_b32_e32 v84, v2
	v_mov_b32_e32 v85, v2
	v_mov_b32_e32 v86, v2
	v_mov_b32_e32 v87, v2
	v_mov_b32_e32 v88, v2
	v_mov_b32_e32 v89, v2
	v_mov_b32_e32 v98, v2
	v_mov_b32_e32 v99, v2
	v_mov_b32_e32 v100, v2
	v_mov_b32_e32 v101, v2
	v_mov_b32_e32 v102, v2
	v_mov_b32_e32 v103, v2
	v_mov_b32_e32 v104, v2
	v_mov_b32_e32 v105, v2
	v_mov_b32_e32 v114, v2
	v_mov_b32_e32 v115, v2
	v_mov_b32_e32 v116, v2
	v_mov_b32_e32 v117, v2
	v_mov_b32_e32 v122, v2
	v_mov_b32_e32 v123, v2
	v_mov_b32_e32 v124, v2
	v_mov_b32_e32 v125, v2
	v_mov_b32_e32 v74, v2
	v_mov_b32_e32 v75, v2
	v_mov_b32_e32 v76, v2
	v_mov_b32_e32 v77, v2
	v_mov_b32_e32 v78, v2
	v_mov_b32_e32 v79, v2
	v_mov_b32_e32 v80, v2
	v_mov_b32_e32 v81, v2
	v_mov_b32_e32 v90, v2
	v_mov_b32_e32 v91, v2
	v_mov_b32_e32 v92, v2
	v_mov_b32_e32 v93, v2
	v_mov_b32_e32 v94, v2
	v_mov_b32_e32 v95, v2
	v_mov_b32_e32 v96, v2
	v_mov_b32_e32 v97, v2
	v_mov_b32_e32 v106, v2
	v_mov_b32_e32 v107, v2
	v_mov_b32_e32 v108, v2
	v_mov_b32_e32 v109, v2
	v_mov_b32_e32 v110, v2
	v_mov_b32_e32 v111, v2
	v_mov_b32_e32 v112, v2
	v_mov_b32_e32 v113, v2
	v_mov_b32_e32 v130, v2
	v_mov_b32_e32 v131, v2
	v_mov_b32_e32 v132, v2
	v_mov_b32_e32 v133, v2
	v_mov_b32_e32 v134, v2
	v_mov_b32_e32 v135, v2
	v_mov_b32_e32 v136, v2
	v_mov_b32_e32 v137, v2
	s_andn2_b64 vcc, exec, s[40:41]
	s_cbranch_vccnz .LBB0_1529
	s_branch .LBB0_1531

.LBB0_1623:
	s_add_u32 s36, s26, s34
	s_addc_u32 s37, s27, s35
	s_add_u32 s36, s36, 0x100
	s_addc_u32 s37, s37, 0
	s_add_u32 s80, s8, s34
	s_addc_u32 s81, s9, s35
	s_add_i32 s82, 0, 0x10000
	s_cmpk_eq_i32 s34, 0xb00
	s_cselect_b32 s43, s31, s37
	s_cselect_b32 s42, s30, s36
	s_cselect_b32 s37, s29, s81
	s_cselect_b32 s36, s28, s80
	s_add_i32 s83, 0, 0x14000
	v_lshl_add_u64 v[208:209], v[142:143], 0, s[34:35]
	s_add_i32 m0, s4, 0xc000
	s_nop 0
	global_load_lds_dwordx4 v[208:209], off
	s_add_i32 m0, s4, 0xe000
	v_lshl_add_u64 v[208:209], v[140:141], 0, s[34:35]
	global_load_lds_dwordx4 v[208:209], off
	ds_read_b128 v[146:149], v241
	ds_read_b128 v[150:153], v241 offset:1024
	ds_read_b128 v[154:157], v241 offset:2048
	ds_read_b128 v[158:161], v241 offset:3072
	ds_read_b128 v[162:165], v241 offset:16384
	ds_read_b128 v[168:171], v241 offset:17408
	ds_read_b128 v[172:175], v241 offset:18432
	ds_read_b128 v[176:179], v241 offset:19456
	ds_read_b128 v[180:183], v145
	ds_read_b128 v[184:187], v145 offset:1024
	ds_read_b128 v[188:191], v145 offset:2048
	ds_read_b128 v[192:195], v145 offset:3072
	ds_read_b128 v[196:199], v145 offset:4096
	ds_read_b128 v[200:203], v145 offset:5120
	ds_read_b128 v[204:207], v145 offset:6144
	ds_read_b128 v[216:219], v145 offset:7168
	s_waitcnt vmcnt(8) lgkmcnt(0)
	s_barrier
	v_mfma_f32_16x16x32_bf16 v[134:137], v[146:149], v[180:183], v[134:137]
	v_mfma_f32_16x16x32_bf16 v[130:133], v[154:157], v[180:183], v[130:133]
	v_mfma_f32_16x16x32_bf16 v[110:113], v[146:149], v[188:191], v[110:113]
	v_mfma_f32_16x16x32_bf16 v[106:109], v[154:157], v[188:191], v[106:109]
	v_mfma_f32_16x16x32_bf16 v[94:97], v[146:149], v[196:199], v[94:97]
	v_mfma_f32_16x16x32_bf16 v[90:93], v[154:157], v[196:199], v[90:93]
	v_mfma_f32_16x16x32_bf16 v[78:81], v[146:149], v[204:207], v[78:81]
	v_mfma_f32_16x16x32_bf16 v[74:77], v[154:157], v[204:207], v[74:77]
	v_mfma_f32_16x16x32_bf16 v[134:137], v[150:153], v[184:187], v[134:137]
	v_mfma_f32_16x16x32_bf16 v[130:133], v[158:161], v[184:187], v[130:133]
	v_mfma_f32_16x16x32_bf16 v[110:113], v[150:153], v[192:195], v[110:113]
	v_mfma_f32_16x16x32_bf16 v[106:109], v[158:161], v[192:195], v[106:109]
	v_mfma_f32_16x16x32_bf16 v[94:97], v[150:153], v[200:203], v[94:97]
	v_mfma_f32_16x16x32_bf16 v[90:93], v[158:161], v[200:203], v[90:93]
	v_mfma_f32_16x16x32_bf16 v[78:81], v[150:153], v[216:219], v[78:81]
	v_mfma_f32_16x16x32_bf16 v[74:77], v[158:161], v[216:219], v[74:77]
	v_mfma_f32_16x16x32_bf16 v[122:125], v[162:165], v[180:183], v[122:125]
	v_mfma_f32_16x16x32_bf16 v[114:117], v[172:175], v[180:183], v[114:117]
	v_mfma_f32_16x16x32_bf16 v[102:105], v[162:165], v[188:191], v[102:105]
	v_mfma_f32_16x16x32_bf16 v[98:101], v[172:175], v[188:191], v[98:101]
	v_mfma_f32_16x16x32_bf16 v[86:89], v[162:165], v[196:199], v[86:89]
	v_mfma_f32_16x16x32_bf16 v[82:85], v[172:175], v[196:199], v[82:85]
	v_mfma_f32_16x16x32_bf16 v[70:73], v[162:165], v[204:207], v[70:73]
	v_mfma_f32_16x16x32_bf16 v[66:69], v[172:175], v[204:207], v[66:69]
	v_mfma_f32_16x16x32_bf16 v[122:125], v[168:171], v[184:187], v[122:125]
	v_mfma_f32_16x16x32_bf16 v[114:117], v[176:179], v[184:187], v[114:117]
	v_mfma_f32_16x16x32_bf16 v[102:105], v[168:171], v[192:195], v[102:105]
	v_mfma_f32_16x16x32_bf16 v[98:101], v[176:179], v[192:195], v[98:101]
	v_mfma_f32_16x16x32_bf16 v[86:89], v[168:171], v[200:203], v[86:89]
	v_mfma_f32_16x16x32_bf16 v[82:85], v[176:179], v[200:203], v[82:85]
	v_mfma_f32_16x16x32_bf16 v[70:73], v[168:171], v[216:219], v[70:73]
	v_mfma_f32_16x16x32_bf16 v[66:69], v[176:179], v[216:219], v[66:69]
	s_barrier
	s_add_i32 s80, s82, s53
	v_lshl_add_u64 v[208:209], s[36:37], 0, v[0:1]
	s_mov_b32 m0, s80
	s_nop 0
	global_load_lds_dwordx4 v0, s[36:37]
	s_add_i32 m0, s80, 0x2000
	s_add_u32 s80, s36, 0x60000
	v_lshl_add_u64 v[220:221], s[36:37], 0, v[118:119]
	s_addc_u32 s81, s37, 0
	s_add_i32 s82, s83, s53
	global_load_lds_dwordx4 v118, s[36:37]
	s_mov_b32 m0, s82
	v_lshl_add_u64 v[224:225], s[42:43], 0, v[120:121]
	global_load_lds_dwordx4 v0, s[80:81]
	s_add_i32 m0, s82, 0x2000
	s_nop 0
	global_load_lds_dwordx4 v118, s[80:81]
	s_mov_b32 m0, s4
	v_lshl_add_u64 v[222:223], s[42:43], 0, v[126:127]
	global_load_lds_dwordx4 v126, s[42:43]
	s_mov_b32 m0, s33
	s_nop 0
	global_load_lds_dwordx4 v120, s[42:43]
	ds_read_b128 v[180:183], v145 offset:16384
	ds_read_b128 v[184:187], v145 offset:17408
	ds_read_b128 v[188:191], v145 offset:18432
	ds_read_b128 v[192:195], v145 offset:19456
	ds_read_b128 v[196:199], v145 offset:20480
	ds_read_b128 v[200:203], v145 offset:21504
	ds_read_b128 v[204:207], v145 offset:22528
	ds_read_b128 v[216:219], v145 offset:23552
	s_waitcnt vmcnt(8) lgkmcnt(0)
	s_barrier
	v_mfma_f32_16x16x32_bf16 v[62:65], v[146:149], v[180:183], v[62:65]
	v_mfma_f32_16x16x32_bf16 v[58:61], v[154:157], v[180:183], v[58:61]
	v_mfma_f32_16x16x32_bf16 v[46:49], v[146:149], v[188:191], v[46:49]
	v_mfma_f32_16x16x32_bf16 v[42:45], v[154:157], v[188:191], v[42:45]
	v_mfma_f32_16x16x32_bf16 v[30:33], v[146:149], v[196:199], v[30:33]
	v_mfma_f32_16x16x32_bf16 v[26:29], v[154:157], v[196:199], v[26:29]
	v_mfma_f32_16x16x32_bf16 v[14:17], v[146:149], v[204:207], v[14:17]
	v_mfma_f32_16x16x32_bf16 v[10:13], v[154:157], v[204:207], v[10:13]
	v_mfma_f32_16x16x32_bf16 v[62:65], v[150:153], v[184:187], v[62:65]
	v_mfma_f32_16x16x32_bf16 v[58:61], v[158:161], v[184:187], v[58:61]
	v_mfma_f32_16x16x32_bf16 v[46:49], v[150:153], v[192:195], v[46:49]
	v_mfma_f32_16x16x32_bf16 v[42:45], v[158:161], v[192:195], v[42:45]
	v_mfma_f32_16x16x32_bf16 v[30:33], v[150:153], v[200:203], v[30:33]
	v_mfma_f32_16x16x32_bf16 v[26:29], v[158:161], v[200:203], v[26:29]
	v_mfma_f32_16x16x32_bf16 v[14:17], v[150:153], v[216:219], v[14:17]
	v_mfma_f32_16x16x32_bf16 v[10:13], v[158:161], v[216:219], v[10:13]
	v_mfma_f32_16x16x32_bf16 v[54:57], v[162:165], v[180:183], v[54:57]
	v_mfma_f32_16x16x32_bf16 v[50:53], v[172:175], v[180:183], v[50:53]
	v_mfma_f32_16x16x32_bf16 v[38:41], v[162:165], v[188:191], v[38:41]
	v_mfma_f32_16x16x32_bf16 v[34:37], v[172:175], v[188:191], v[34:37]
	v_mfma_f32_16x16x32_bf16 v[22:25], v[162:165], v[196:199], v[22:25]
	v_mfma_f32_16x16x32_bf16 v[18:21], v[172:175], v[196:199], v[18:21]
	v_mfma_f32_16x16x32_bf16 v[6:9], v[162:165], v[204:207], v[6:9]
	v_mfma_f32_16x16x32_bf16 v[2:5], v[172:175], v[204:207], v[2:5]
	v_mfma_f32_16x16x32_bf16 v[54:57], v[168:171], v[184:187], v[54:57]
	v_mfma_f32_16x16x32_bf16 v[50:53], v[176:179], v[184:187], v[50:53]
	v_mfma_f32_16x16x32_bf16 v[38:41], v[168:171], v[192:195], v[38:41]
	v_mfma_f32_16x16x32_bf16 v[34:37], v[176:179], v[192:195], v[34:37]
	v_mfma_f32_16x16x32_bf16 v[22:25], v[168:171], v[200:203], v[22:25]
	v_mfma_f32_16x16x32_bf16 v[18:21], v[176:179], v[200:203], v[18:21]
	v_mfma_f32_16x16x32_bf16 v[6:9], v[168:171], v[216:219], v[6:9]
	v_mfma_f32_16x16x32_bf16 v[2:5], v[176:179], v[216:219], v[2:5]
	s_barrier
	s_add_i32 s80, 0, 0x18000
	s_add_i32 s81, 0, 0x1c000
	s_add_u32 s42, s42, 0x60000
	s_addc_u32 s43, s43, 0
	s_mov_b32 m0, s62
	s_nop 0
	global_load_lds_dwordx4 v126, s[42:43]
	s_mov_b32 m0, s63
	v_lshl_add_u64 v[242:243], s[42:43], 0, v[120:121]
	global_load_lds_dwordx4 v120, s[42:43]
	ds_read_b128 v[146:149], v241 offset:32768
	ds_read_b128 v[150:153], v241 offset:33792
	ds_read_b128 v[154:157], v241 offset:34816
	ds_read_b128 v[158:161], v241 offset:35840
	ds_read_b128 v[162:165], v241 offset:49152
	ds_read_b128 v[168:171], v241 offset:50176
	ds_read_b128 v[172:175], v241 offset:51200
	ds_read_b128 v[176:179], v241 offset:52224
	ds_read_b128 v[180:183], v145 offset:32768
	ds_read_b128 v[184:187], v145 offset:33792
	ds_read_b128 v[188:191], v145 offset:34816
	ds_read_b128 v[192:195], v145 offset:35840
	ds_read_b128 v[196:199], v145 offset:36864
	ds_read_b128 v[200:203], v145 offset:37888
	ds_read_b128 v[204:207], v145 offset:38912
	ds_read_b128 v[216:219], v145 offset:39936
	s_waitcnt vmcnt(8) lgkmcnt(0)
	s_barrier
	v_mfma_f32_16x16x32_bf16 v[134:137], v[146:149], v[180:183], v[134:137]
	v_mfma_f32_16x16x32_bf16 v[130:133], v[154:157], v[180:183], v[130:133]
	v_mfma_f32_16x16x32_bf16 v[110:113], v[146:149], v[188:191], v[110:113]
	v_mfma_f32_16x16x32_bf16 v[106:109], v[154:157], v[188:191], v[106:109]
	v_mfma_f32_16x16x32_bf16 v[94:97], v[146:149], v[196:199], v[94:97]
	v_mfma_f32_16x16x32_bf16 v[90:93], v[154:157], v[196:199], v[90:93]
	v_mfma_f32_16x16x32_bf16 v[78:81], v[146:149], v[204:207], v[78:81]
	v_mfma_f32_16x16x32_bf16 v[74:77], v[154:157], v[204:207], v[74:77]
	v_mfma_f32_16x16x32_bf16 v[134:137], v[150:153], v[184:187], v[134:137]
	v_mfma_f32_16x16x32_bf16 v[130:133], v[158:161], v[184:187], v[130:133]
	v_mfma_f32_16x16x32_bf16 v[110:113], v[150:153], v[192:195], v[110:113]
	v_mfma_f32_16x16x32_bf16 v[106:109], v[158:161], v[192:195], v[106:109]
	v_mfma_f32_16x16x32_bf16 v[94:97], v[150:153], v[200:203], v[94:97]
	v_mfma_f32_16x16x32_bf16 v[90:93], v[158:161], v[200:203], v[90:93]
	v_mfma_f32_16x16x32_bf16 v[78:81], v[150:153], v[216:219], v[78:81]
	v_mfma_f32_16x16x32_bf16 v[74:77], v[158:161], v[216:219], v[74:77]
	v_mfma_f32_16x16x32_bf16 v[122:125], v[162:165], v[180:183], v[122:125]
	v_mfma_f32_16x16x32_bf16 v[114:117], v[172:175], v[180:183], v[114:117]
	v_mfma_f32_16x16x32_bf16 v[102:105], v[162:165], v[188:191], v[102:105]
	v_mfma_f32_16x16x32_bf16 v[98:101], v[172:175], v[188:191], v[98:101]
	v_mfma_f32_16x16x32_bf16 v[86:89], v[162:165], v[196:199], v[86:89]
	v_mfma_f32_16x16x32_bf16 v[82:85], v[172:175], v[196:199], v[82:85]
	v_mfma_f32_16x16x32_bf16 v[70:73], v[162:165], v[204:207], v[70:73]
	v_mfma_f32_16x16x32_bf16 v[66:69], v[172:175], v[204:207], v[66:69]
	v_mfma_f32_16x16x32_bf16 v[122:125], v[168:171], v[184:187], v[122:125]
	v_mfma_f32_16x16x32_bf16 v[114:117], v[176:179], v[184:187], v[114:117]
	v_mfma_f32_16x16x32_bf16 v[102:105], v[168:171], v[192:195], v[102:105]
	v_mfma_f32_16x16x32_bf16 v[98:101], v[176:179], v[192:195], v[98:101]
	v_mfma_f32_16x16x32_bf16 v[86:89], v[168:171], v[200:203], v[86:89]
	v_mfma_f32_16x16x32_bf16 v[82:85], v[176:179], v[200:203], v[82:85]
	v_mfma_f32_16x16x32_bf16 v[70:73], v[168:171], v[216:219], v[70:73]
	v_mfma_f32_16x16x32_bf16 v[66:69], v[176:179], v[216:219], v[66:69]
	s_barrier
	s_add_i32 s42, s80, s53
	v_lshl_add_u64 v[208:209], v[208:209], 0, s[56:57]
	s_mov_b32 m0, s42
	s_nop 0
	global_load_lds_dwordx4 v[208:209], off
	s_add_i32 m0, s42, 0x2000
	s_add_u32 s36, s36, 0x60080
	v_lshl_add_u64 v[208:209], v[220:221], 0, s[56:57]
	s_addc_u32 s37, s37, 0
	s_add_i32 s42, s81, s53
	global_load_lds_dwordx4 v[208:209], off
	s_mov_b32 m0, s42
	s_nop 0
	global_load_lds_dwordx4 v0, s[36:37]
	s_add_i32 m0, s42, 0x2000
	s_nop 0
	global_load_lds_dwordx4 v118, s[36:37]
	s_mov_b32 m0, s70
	v_lshl_add_u64 v[208:209], v[222:223], 0, s[56:57]
	global_load_lds_dwordx4 v[208:209], off
	s_mov_b32 m0, s71
	v_lshl_add_u64 v[208:209], v[224:225], 0, s[56:57]
	global_load_lds_dwordx4 v[208:209], off
	ds_read_b128 v[180:183], v145 offset:49152
	ds_read_b128 v[184:187], v145 offset:50176
	ds_read_b128 v[188:191], v145 offset:51200
	ds_read_b128 v[192:195], v145 offset:52224
	ds_read_b128 v[196:199], v145 offset:53248
	ds_read_b128 v[200:203], v145 offset:54272
	ds_read_b128 v[204:207], v145 offset:55296
	ds_read_b128 v[216:219], v145 offset:56320
	s_waitcnt vmcnt(8) lgkmcnt(0)
	s_barrier
	v_mfma_f32_16x16x32_bf16 v[62:65], v[146:149], v[180:183], v[62:65]
	v_mfma_f32_16x16x32_bf16 v[58:61], v[154:157], v[180:183], v[58:61]
	v_mfma_f32_16x16x32_bf16 v[46:49], v[146:149], v[188:191], v[46:49]
	v_mfma_f32_16x16x32_bf16 v[42:45], v[154:157], v[188:191], v[42:45]
	v_mfma_f32_16x16x32_bf16 v[30:33], v[146:149], v[196:199], v[30:33]
	v_mfma_f32_16x16x32_bf16 v[26:29], v[154:157], v[196:199], v[26:29]
	v_mfma_f32_16x16x32_bf16 v[14:17], v[146:149], v[204:207], v[14:17]
	v_mfma_f32_16x16x32_bf16 v[10:13], v[154:157], v[204:207], v[10:13]
	v_mfma_f32_16x16x32_bf16 v[62:65], v[150:153], v[184:187], v[62:65]
	v_mfma_f32_16x16x32_bf16 v[58:61], v[158:161], v[184:187], v[58:61]
	v_mfma_f32_16x16x32_bf16 v[46:49], v[150:153], v[192:195], v[46:49]
	v_mfma_f32_16x16x32_bf16 v[42:45], v[158:161], v[192:195], v[42:45]
	v_mfma_f32_16x16x32_bf16 v[30:33], v[150:153], v[200:203], v[30:33]
	v_mfma_f32_16x16x32_bf16 v[26:29], v[158:161], v[200:203], v[26:29]
	v_mfma_f32_16x16x32_bf16 v[14:17], v[150:153], v[216:219], v[14:17]
	v_mfma_f32_16x16x32_bf16 v[10:13], v[158:161], v[216:219], v[10:13]
	v_mfma_f32_16x16x32_bf16 v[54:57], v[162:165], v[180:183], v[54:57]
	v_mfma_f32_16x16x32_bf16 v[50:53], v[172:175], v[180:183], v[50:53]
	v_mfma_f32_16x16x32_bf16 v[38:41], v[162:165], v[188:191], v[38:41]
	v_mfma_f32_16x16x32_bf16 v[34:37], v[172:175], v[188:191], v[34:37]
	v_mfma_f32_16x16x32_bf16 v[22:25], v[162:165], v[196:199], v[22:25]
	v_mfma_f32_16x16x32_bf16 v[18:21], v[172:175], v[196:199], v[18:21]
	v_mfma_f32_16x16x32_bf16 v[6:9], v[162:165], v[204:207], v[6:9]
	v_mfma_f32_16x16x32_bf16 v[2:5], v[172:175], v[204:207], v[2:5]
	v_mfma_f32_16x16x32_bf16 v[54:57], v[168:171], v[184:187], v[54:57]
	v_mfma_f32_16x16x32_bf16 v[50:53], v[176:179], v[184:187], v[50:53]
	v_mfma_f32_16x16x32_bf16 v[38:41], v[168:171], v[192:195], v[38:41]
	v_mfma_f32_16x16x32_bf16 v[34:37], v[176:179], v[192:195], v[34:37]
	v_mfma_f32_16x16x32_bf16 v[22:25], v[168:171], v[200:203], v[22:25]
	v_mfma_f32_16x16x32_bf16 v[18:21], v[176:179], v[200:203], v[18:21]
	v_mfma_f32_16x16x32_bf16 v[6:9], v[168:171], v[216:219], v[6:9]
	v_mfma_f32_16x16x32_bf16 v[2:5], v[176:179], v[216:219], v[2:5]
	s_barrier
	s_add_i32 s59, s59, 2
	s_add_u32 s34, s34, 0x100
	s_addc_u32 s35, s35, 0
	s_cmp_gt_u32 s59, 21
	s_cbranch_scc0 .LBB0_1623
	s_add_u32 s34, s8, 0xffffff00
	s_addc_u32 s35, s9, -1
	s_and_b64 vcc, exec, s[40:41]
	s_cbranch_vccnz .LBB0_1626
	v_mov_b32_e32 v2, 0
	s_mov_b32 s16, s77
	s_mov_b32 s76, s79
	s_mov_b64 s[26:27], s[30:31]
	s_mov_b32 s68, s58
	v_mov_b32_e32 v3, v2
	v_mov_b32_e32 v4, v2
	v_mov_b32_e32 v5, v2
	v_mov_b32_e32 v6, v2
	v_mov_b32_e32 v7, v2
	v_mov_b32_e32 v8, v2
	v_mov_b32_e32 v9, v2
	v_mov_b32_e32 v18, v2
	v_mov_b32_e32 v19, v2
	v_mov_b32_e32 v20, v2
	v_mov_b32_e32 v21, v2
	v_mov_b32_e32 v22, v2
	v_mov_b32_e32 v23, v2
	v_mov_b32_e32 v24, v2
	v_mov_b32_e32 v25, v2
	v_mov_b32_e32 v34, v2
	v_mov_b32_e32 v35, v2
	v_mov_b32_e32 v36, v2
	v_mov_b32_e32 v37, v2
	v_mov_b32_e32 v38, v2
	v_mov_b32_e32 v39, v2
	v_mov_b32_e32 v40, v2
	v_mov_b32_e32 v41, v2
	v_mov_b32_e32 v50, v2
	v_mov_b32_e32 v51, v2
	v_mov_b32_e32 v52, v2
	v_mov_b32_e32 v53, v2
	v_mov_b32_e32 v54, v2
	v_mov_b32_e32 v55, v2
	v_mov_b32_e32 v56, v2
	v_mov_b32_e32 v57, v2
	v_mov_b32_e32 v10, v2
	v_mov_b32_e32 v11, v2
	v_mov_b32_e32 v12, v2
	v_mov_b32_e32 v13, v2
	v_mov_b32_e32 v14, v2
	v_mov_b32_e32 v15, v2
	v_mov_b32_e32 v16, v2
	v_mov_b32_e32 v17, v2
	v_mov_b32_e32 v26, v2
	v_mov_b32_e32 v27, v2
	v_mov_b32_e32 v28, v2
	v_mov_b32_e32 v29, v2
	v_mov_b32_e32 v30, v2
	v_mov_b32_e32 v31, v2
	v_mov_b32_e32 v32, v2
	v_mov_b32_e32 v33, v2
	v_mov_b32_e32 v42, v2
	v_mov_b32_e32 v43, v2
	v_mov_b32_e32 v44, v2
	v_mov_b32_e32 v45, v2
	v_mov_b32_e32 v46, v2
	v_mov_b32_e32 v47, v2
	v_mov_b32_e32 v48, v2
	v_mov_b32_e32 v49, v2
	v_mov_b32_e32 v58, v2
	v_mov_b32_e32 v59, v2
	v_mov_b32_e32 v60, v2
	v_mov_b32_e32 v61, v2
	v_mov_b32_e32 v62, v2
	v_mov_b32_e32 v63, v2
	v_mov_b32_e32 v64, v2
	v_mov_b32_e32 v65, v2
	v_mov_b32_e32 v66, v2
	v_mov_b32_e32 v67, v2
	v_mov_b32_e32 v68, v2
	v_mov_b32_e32 v69, v2
	v_mov_b32_e32 v70, v2
	v_mov_b32_e32 v71, v2
	v_mov_b32_e32 v72, v2
	v_mov_b32_e32 v73, v2
	v_mov_b32_e32 v82, v2
	v_mov_b32_e32 v83, v2
	v_mov_b32_e32 v84, v2
	v_mov_b32_e32 v85, v2
	v_mov_b32_e32 v86, v2
	v_mov_b32_e32 v87, v2
	v_mov_b32_e32 v88, v2
	v_mov_b32_e32 v89, v2
	v_mov_b32_e32 v98, v2
	v_mov_b32_e32 v99, v2
	v_mov_b32_e32 v100, v2
	v_mov_b32_e32 v101, v2
	v_mov_b32_e32 v102, v2
	v_mov_b32_e32 v103, v2
	v_mov_b32_e32 v104, v2
	v_mov_b32_e32 v105, v2
	v_mov_b32_e32 v114, v2
	v_mov_b32_e32 v115, v2
	v_mov_b32_e32 v116, v2
	v_mov_b32_e32 v117, v2
	v_mov_b32_e32 v122, v2
	v_mov_b32_e32 v123, v2
	v_mov_b32_e32 v124, v2
	v_mov_b32_e32 v125, v2
	v_mov_b32_e32 v74, v2
	v_mov_b32_e32 v75, v2
	v_mov_b32_e32 v76, v2
	v_mov_b32_e32 v77, v2
	v_mov_b32_e32 v78, v2
	v_mov_b32_e32 v79, v2
	v_mov_b32_e32 v80, v2
	v_mov_b32_e32 v81, v2
	v_mov_b32_e32 v90, v2
	v_mov_b32_e32 v91, v2
	v_mov_b32_e32 v92, v2
	v_mov_b32_e32 v93, v2
	v_mov_b32_e32 v94, v2
	v_mov_b32_e32 v95, v2
	v_mov_b32_e32 v96, v2
	v_mov_b32_e32 v97, v2
	v_mov_b32_e32 v106, v2
	v_mov_b32_e32 v107, v2
	v_mov_b32_e32 v108, v2
	v_mov_b32_e32 v109, v2
	v_mov_b32_e32 v110, v2
	v_mov_b32_e32 v111, v2
	v_mov_b32_e32 v112, v2
	v_mov_b32_e32 v113, v2
	v_mov_b32_e32 v130, v2
	v_mov_b32_e32 v131, v2
	v_mov_b32_e32 v132, v2
	v_mov_b32_e32 v133, v2
	v_mov_b32_e32 v134, v2
	v_mov_b32_e32 v135, v2
	v_mov_b32_e32 v136, v2
	v_mov_b32_e32 v137, v2
	s_andn2_b64 vcc, exec, s[38:39]
	s_cbranch_vccnz .LBB0_1627
	s_branch .LBB0_1628

.LBB0_1783:
	s_add_u32 s28, s6, 0xfffc0080
	s_addc_u32 s29, s7, -1
	s_add_i32 s53, 0, 0x10000
	s_cmp_eq_u32 s41, 12
	s_cselect_b32 s31, s8, s29
	s_cselect_b32 s30, s9, s28
	s_cselect_b32 s29, s21, s40
	s_cselect_b32 s28, s23, s33
	s_add_i32 s62, 0, 0x14000
	s_add_i32 m0, s37, 0xc000
	s_nop 0
	global_load_lds_dwordx4 v166, s[6:7]
	s_add_i32 m0, s37, 0xe000
	s_nop 0
	global_load_lds_dwordx4 v164, s[6:7]
	ds_read_b128 v[130:133], v165
	ds_read_b128 v[134:137], v165 offset:1024
	ds_read_b128 v[138:141], v165 offset:2048
	ds_read_b128 v[142:145], v165 offset:3072
	ds_read_b128 v[146:149], v165 offset:16384
	ds_read_b128 v[150:153], v165 offset:17408
	ds_read_b128 v[154:157], v165 offset:18432
	ds_read_b128 v[168:171], v165 offset:19456
	ds_read_b128 v[172:175], v183
	ds_read_b128 v[184:187], v183 offset:1024
	ds_read_b128 v[188:191], v183 offset:2048
	ds_read_b128 v[192:195], v183 offset:3072
	ds_read_b128 v[196:199], v183 offset:4096
	ds_read_b128 v[200:203], v183 offset:5120
	ds_read_b128 v[204:207], v183 offset:6144
	ds_read_b128 v[216:219], v183 offset:7168
	s_waitcnt vmcnt(8) lgkmcnt(0)
	s_barrier
	v_mfma_f32_16x16x32_bf16 v[126:129], v[130:133], v[172:175], v[126:129]
	v_mfma_f32_16x16x32_bf16 v[122:125], v[138:141], v[172:175], v[122:125]
	v_mfma_f32_16x16x32_bf16 v[114:117], v[130:133], v[188:191], v[114:117]
	v_mfma_f32_16x16x32_bf16 v[106:109], v[138:141], v[188:191], v[106:109]
	v_mfma_f32_16x16x32_bf16 v[98:101], v[130:133], v[196:199], v[98:101]
	v_mfma_f32_16x16x32_bf16 v[90:93], v[138:141], v[196:199], v[90:93]
	v_mfma_f32_16x16x32_bf16 v[82:85], v[130:133], v[204:207], v[82:85]
	v_mfma_f32_16x16x32_bf16 v[74:77], v[138:141], v[204:207], v[74:77]
	v_mfma_f32_16x16x32_bf16 v[126:129], v[134:137], v[184:187], v[126:129]
	v_mfma_f32_16x16x32_bf16 v[122:125], v[142:145], v[184:187], v[122:125]
	v_mfma_f32_16x16x32_bf16 v[114:117], v[134:137], v[192:195], v[114:117]
	v_mfma_f32_16x16x32_bf16 v[106:109], v[142:145], v[192:195], v[106:109]
	v_mfma_f32_16x16x32_bf16 v[98:101], v[134:137], v[200:203], v[98:101]
	v_mfma_f32_16x16x32_bf16 v[90:93], v[142:145], v[200:203], v[90:93]
	v_mfma_f32_16x16x32_bf16 v[82:85], v[134:137], v[216:219], v[82:85]
	v_mfma_f32_16x16x32_bf16 v[74:77], v[142:145], v[216:219], v[74:77]
	v_mfma_f32_16x16x32_bf16 v[118:121], v[146:149], v[172:175], v[118:121]
	v_mfma_f32_16x16x32_bf16 v[110:113], v[154:157], v[172:175], v[110:113]
	v_mfma_f32_16x16x32_bf16 v[102:105], v[146:149], v[188:191], v[102:105]
	v_mfma_f32_16x16x32_bf16 v[94:97], v[154:157], v[188:191], v[94:97]
	v_mfma_f32_16x16x32_bf16 v[86:89], v[146:149], v[196:199], v[86:89]
	v_mfma_f32_16x16x32_bf16 v[78:81], v[154:157], v[196:199], v[78:81]
	v_mfma_f32_16x16x32_bf16 v[70:73], v[146:149], v[204:207], v[70:73]
	v_mfma_f32_16x16x32_bf16 v[66:69], v[154:157], v[204:207], v[66:69]
	v_mfma_f32_16x16x32_bf16 v[118:121], v[150:153], v[184:187], v[118:121]
	v_mfma_f32_16x16x32_bf16 v[110:113], v[168:171], v[184:187], v[110:113]
	v_mfma_f32_16x16x32_bf16 v[102:105], v[150:153], v[192:195], v[102:105]
	v_mfma_f32_16x16x32_bf16 v[94:97], v[168:171], v[192:195], v[94:97]
	v_mfma_f32_16x16x32_bf16 v[86:89], v[150:153], v[200:203], v[86:89]
	v_mfma_f32_16x16x32_bf16 v[78:81], v[168:171], v[200:203], v[78:81]
	v_mfma_f32_16x16x32_bf16 v[70:73], v[150:153], v[216:219], v[70:73]
	v_mfma_f32_16x16x32_bf16 v[66:69], v[168:171], v[216:219], v[66:69]
	s_barrier
	s_add_i32 s53, s53, s36
	v_lshl_add_u64 v[176:177], s[28:29], 0, v[162:163]
	s_mov_b32 m0, s53
	s_nop 0
	global_load_lds_dwordx4 v162, s[28:29]
	s_add_i32 m0, s53, 0x2000
	s_add_u32 s58, s28, 0x40000
	v_lshl_add_u64 v[208:209], s[28:29], 0, v[158:159]
	s_addc_u32 s59, s29, 0
	s_add_i32 s53, s62, s36
	global_load_lds_dwordx4 v158, s[28:29]
	s_mov_b32 m0, s53
	v_lshl_add_u64 v[222:223], s[30:31], 0, v[160:161]
	global_load_lds_dwordx4 v162, s[58:59]
	s_add_i32 m0, s53, 0x2000
	s_nop 0
	global_load_lds_dwordx4 v158, s[58:59]
	s_mov_b32 m0, s37
	v_lshl_add_u64 v[220:221], s[30:31], 0, v[0:1]
	global_load_lds_dwordx4 v0, s[30:31]
	s_mov_b32 m0, s44
	s_nop 0
	global_load_lds_dwordx4 v160, s[30:31]
	ds_read_b128 v[172:175], v183 offset:16384
	ds_read_b128 v[184:187], v183 offset:17408
	ds_read_b128 v[188:191], v183 offset:18432
	ds_read_b128 v[192:195], v183 offset:19456
	ds_read_b128 v[196:199], v183 offset:20480
	ds_read_b128 v[200:203], v183 offset:21504
	ds_read_b128 v[204:207], v183 offset:22528
	ds_read_b128 v[216:219], v183 offset:23552
	s_waitcnt vmcnt(8) lgkmcnt(0)
	s_barrier
	v_mfma_f32_16x16x32_bf16 v[62:65], v[130:133], v[172:175], v[62:65]
	v_mfma_f32_16x16x32_bf16 v[58:61], v[138:141], v[172:175], v[58:61]
	v_mfma_f32_16x16x32_bf16 v[50:53], v[130:133], v[188:191], v[50:53]
	v_mfma_f32_16x16x32_bf16 v[42:45], v[138:141], v[188:191], v[42:45]
	v_mfma_f32_16x16x32_bf16 v[34:37], v[130:133], v[196:199], v[34:37]
	v_mfma_f32_16x16x32_bf16 v[26:29], v[138:141], v[196:199], v[26:29]
	v_mfma_f32_16x16x32_bf16 v[18:21], v[130:133], v[204:207], v[18:21]
	v_mfma_f32_16x16x32_bf16 v[10:13], v[138:141], v[204:207], v[10:13]
	v_mfma_f32_16x16x32_bf16 v[62:65], v[134:137], v[184:187], v[62:65]
	v_mfma_f32_16x16x32_bf16 v[58:61], v[142:145], v[184:187], v[58:61]
	v_mfma_f32_16x16x32_bf16 v[50:53], v[134:137], v[192:195], v[50:53]
	v_mfma_f32_16x16x32_bf16 v[42:45], v[142:145], v[192:195], v[42:45]
	v_mfma_f32_16x16x32_bf16 v[34:37], v[134:137], v[200:203], v[34:37]
	v_mfma_f32_16x16x32_bf16 v[26:29], v[142:145], v[200:203], v[26:29]
	v_mfma_f32_16x16x32_bf16 v[18:21], v[134:137], v[216:219], v[18:21]
	v_mfma_f32_16x16x32_bf16 v[10:13], v[142:145], v[216:219], v[10:13]
	v_mfma_f32_16x16x32_bf16 v[54:57], v[146:149], v[172:175], v[54:57]
	v_mfma_f32_16x16x32_bf16 v[46:49], v[154:157], v[172:175], v[46:49]
	v_mfma_f32_16x16x32_bf16 v[38:41], v[146:149], v[188:191], v[38:41]
	v_mfma_f32_16x16x32_bf16 v[30:33], v[154:157], v[188:191], v[30:33]
	v_mfma_f32_16x16x32_bf16 v[22:25], v[146:149], v[196:199], v[22:25]
	v_mfma_f32_16x16x32_bf16 v[14:17], v[154:157], v[196:199], v[14:17]
	v_mfma_f32_16x16x32_bf16 v[6:9], v[146:149], v[204:207], v[6:9]
	v_mfma_f32_16x16x32_bf16 v[2:5], v[154:157], v[204:207], v[2:5]
	v_mfma_f32_16x16x32_bf16 v[54:57], v[150:153], v[184:187], v[54:57]
	v_mfma_f32_16x16x32_bf16 v[46:49], v[168:171], v[184:187], v[46:49]
	v_mfma_f32_16x16x32_bf16 v[38:41], v[150:153], v[192:195], v[38:41]
	v_mfma_f32_16x16x32_bf16 v[30:33], v[168:171], v[192:195], v[30:33]
	v_mfma_f32_16x16x32_bf16 v[22:25], v[150:153], v[200:203], v[22:25]
	v_mfma_f32_16x16x32_bf16 v[14:17], v[168:171], v[200:203], v[14:17]
	v_mfma_f32_16x16x32_bf16 v[6:9], v[150:153], v[216:219], v[6:9]
	v_mfma_f32_16x16x32_bf16 v[2:5], v[168:171], v[216:219], v[2:5]
	s_barrier
	s_add_i32 s53, 0, 0x18000
	s_add_i32 s58, 0, 0x1c000
	s_add_u32 s30, s30, 0x40000
	s_addc_u32 s31, s31, 0
	s_mov_b32 m0, s45
	s_nop 0
	global_load_lds_dwordx4 v0, s[30:31]
	s_mov_b32 m0, s46
	v_lshl_add_u64 v[224:225], s[30:31], 0, v[160:161]
	global_load_lds_dwordx4 v160, s[30:31]
	ds_read_b128 v[130:133], v165 offset:32768
	ds_read_b128 v[134:137], v165 offset:33792
	ds_read_b128 v[138:141], v165 offset:34816
	ds_read_b128 v[142:145], v165 offset:35840
	ds_read_b128 v[146:149], v165 offset:49152
	ds_read_b128 v[150:153], v165 offset:50176
	ds_read_b128 v[154:157], v165 offset:51200
	ds_read_b128 v[168:171], v165 offset:52224
	ds_read_b128 v[172:175], v183 offset:32768
	ds_read_b128 v[184:187], v183 offset:33792
	ds_read_b128 v[188:191], v183 offset:34816
	ds_read_b128 v[192:195], v183 offset:35840
	ds_read_b128 v[196:199], v183 offset:36864
	ds_read_b128 v[200:203], v183 offset:37888
	ds_read_b128 v[204:207], v183 offset:38912
	ds_read_b128 v[216:219], v183 offset:39936
	s_waitcnt vmcnt(8) lgkmcnt(0)
	s_barrier
	v_mfma_f32_16x16x32_bf16 v[126:129], v[130:133], v[172:175], v[126:129]
	v_mfma_f32_16x16x32_bf16 v[122:125], v[138:141], v[172:175], v[122:125]
	v_mfma_f32_16x16x32_bf16 v[114:117], v[130:133], v[188:191], v[114:117]
	v_mfma_f32_16x16x32_bf16 v[106:109], v[138:141], v[188:191], v[106:109]
	v_mfma_f32_16x16x32_bf16 v[98:101], v[130:133], v[196:199], v[98:101]
	v_mfma_f32_16x16x32_bf16 v[90:93], v[138:141], v[196:199], v[90:93]
	v_mfma_f32_16x16x32_bf16 v[82:85], v[130:133], v[204:207], v[82:85]
	v_mfma_f32_16x16x32_bf16 v[74:77], v[138:141], v[204:207], v[74:77]
	v_mfma_f32_16x16x32_bf16 v[126:129], v[134:137], v[184:187], v[126:129]
	v_mfma_f32_16x16x32_bf16 v[122:125], v[142:145], v[184:187], v[122:125]
	v_mfma_f32_16x16x32_bf16 v[114:117], v[134:137], v[192:195], v[114:117]
	v_mfma_f32_16x16x32_bf16 v[106:109], v[142:145], v[192:195], v[106:109]
	v_mfma_f32_16x16x32_bf16 v[98:101], v[134:137], v[200:203], v[98:101]
	v_mfma_f32_16x16x32_bf16 v[90:93], v[142:145], v[200:203], v[90:93]
	v_mfma_f32_16x16x32_bf16 v[82:85], v[134:137], v[216:219], v[82:85]
	v_mfma_f32_16x16x32_bf16 v[74:77], v[142:145], v[216:219], v[74:77]
	v_mfma_f32_16x16x32_bf16 v[118:121], v[146:149], v[172:175], v[118:121]
	v_mfma_f32_16x16x32_bf16 v[110:113], v[154:157], v[172:175], v[110:113]
	v_mfma_f32_16x16x32_bf16 v[102:105], v[146:149], v[188:191], v[102:105]
	v_mfma_f32_16x16x32_bf16 v[94:97], v[154:157], v[188:191], v[94:97]
	v_mfma_f32_16x16x32_bf16 v[86:89], v[146:149], v[196:199], v[86:89]
	v_mfma_f32_16x16x32_bf16 v[78:81], v[154:157], v[196:199], v[78:81]
	v_mfma_f32_16x16x32_bf16 v[70:73], v[146:149], v[204:207], v[70:73]
	v_mfma_f32_16x16x32_bf16 v[66:69], v[154:157], v[204:207], v[66:69]
	v_mfma_f32_16x16x32_bf16 v[118:121], v[150:153], v[184:187], v[118:121]
	v_mfma_f32_16x16x32_bf16 v[110:113], v[168:171], v[184:187], v[110:113]
	v_mfma_f32_16x16x32_bf16 v[102:105], v[150:153], v[192:195], v[102:105]
	v_mfma_f32_16x16x32_bf16 v[94:97], v[168:171], v[192:195], v[94:97]
	v_mfma_f32_16x16x32_bf16 v[86:89], v[150:153], v[200:203], v[86:89]
	v_mfma_f32_16x16x32_bf16 v[78:81], v[168:171], v[200:203], v[78:81]
	v_mfma_f32_16x16x32_bf16 v[70:73], v[150:153], v[216:219], v[70:73]
	v_mfma_f32_16x16x32_bf16 v[66:69], v[168:171], v[216:219], v[66:69]
	s_barrier
	s_add_i32 s30, s53, s36
	v_lshl_add_u64 v[176:177], v[176:177], 0, s[56:57]
	s_mov_b32 m0, s30
	s_nop 0
	global_load_lds_dwordx4 v[176:177], off
	s_add_i32 m0, s30, 0x2000
	s_add_u32 s28, s28, 0x40080
	v_lshl_add_u64 v[176:177], v[208:209], 0, s[56:57]
	s_addc_u32 s29, s29, 0
	s_add_i32 s30, s58, s36
	global_load_lds_dwordx4 v[176:177], off
	s_mov_b32 m0, s30
	s_nop 0
	global_load_lds_dwordx4 v162, s[28:29]
	s_add_i32 m0, s30, 0x2000
	s_nop 0
	global_load_lds_dwordx4 v158, s[28:29]
	s_mov_b32 m0, s47
	v_lshl_add_u64 v[176:177], v[220:221], 0, s[56:57]
	global_load_lds_dwordx4 v[176:177], off
	s_mov_b32 m0, s48
	v_lshl_add_u64 v[176:177], v[222:223], 0, s[56:57]
	global_load_lds_dwordx4 v[176:177], off
	ds_read_b128 v[172:175], v183 offset:49152
	ds_read_b128 v[184:187], v183 offset:50176
	ds_read_b128 v[188:191], v183 offset:51200
	ds_read_b128 v[192:195], v183 offset:52224
	ds_read_b128 v[196:199], v183 offset:53248
	ds_read_b128 v[200:203], v183 offset:54272
	ds_read_b128 v[204:207], v183 offset:55296
	ds_read_b128 v[216:219], v183 offset:56320
	s_waitcnt vmcnt(8) lgkmcnt(0)
	s_barrier
	v_mfma_f32_16x16x32_bf16 v[62:65], v[130:133], v[172:175], v[62:65]
	v_mfma_f32_16x16x32_bf16 v[58:61], v[138:141], v[172:175], v[58:61]
	v_mfma_f32_16x16x32_bf16 v[50:53], v[130:133], v[188:191], v[50:53]
	v_mfma_f32_16x16x32_bf16 v[42:45], v[138:141], v[188:191], v[42:45]
	v_mfma_f32_16x16x32_bf16 v[34:37], v[130:133], v[196:199], v[34:37]
	v_mfma_f32_16x16x32_bf16 v[26:29], v[138:141], v[196:199], v[26:29]
	v_mfma_f32_16x16x32_bf16 v[18:21], v[130:133], v[204:207], v[18:21]
	v_mfma_f32_16x16x32_bf16 v[10:13], v[138:141], v[204:207], v[10:13]
	v_mfma_f32_16x16x32_bf16 v[62:65], v[134:137], v[184:187], v[62:65]
	v_mfma_f32_16x16x32_bf16 v[58:61], v[142:145], v[184:187], v[58:61]
	v_mfma_f32_16x16x32_bf16 v[50:53], v[134:137], v[192:195], v[50:53]
	v_mfma_f32_16x16x32_bf16 v[42:45], v[142:145], v[192:195], v[42:45]
	v_mfma_f32_16x16x32_bf16 v[34:37], v[134:137], v[200:203], v[34:37]
	v_mfma_f32_16x16x32_bf16 v[26:29], v[142:145], v[200:203], v[26:29]
	v_mfma_f32_16x16x32_bf16 v[18:21], v[134:137], v[216:219], v[18:21]
	v_mfma_f32_16x16x32_bf16 v[10:13], v[142:145], v[216:219], v[10:13]
	v_mfma_f32_16x16x32_bf16 v[54:57], v[146:149], v[172:175], v[54:57]
	v_mfma_f32_16x16x32_bf16 v[46:49], v[154:157], v[172:175], v[46:49]
	v_mfma_f32_16x16x32_bf16 v[38:41], v[146:149], v[188:191], v[38:41]
	v_mfma_f32_16x16x32_bf16 v[30:33], v[154:157], v[188:191], v[30:33]
	v_mfma_f32_16x16x32_bf16 v[22:25], v[146:149], v[196:199], v[22:25]
	v_mfma_f32_16x16x32_bf16 v[14:17], v[154:157], v[196:199], v[14:17]
	v_mfma_f32_16x16x32_bf16 v[6:9], v[146:149], v[204:207], v[6:9]
	v_mfma_f32_16x16x32_bf16 v[2:5], v[154:157], v[204:207], v[2:5]
	v_mfma_f32_16x16x32_bf16 v[54:57], v[150:153], v[184:187], v[54:57]
	v_mfma_f32_16x16x32_bf16 v[46:49], v[168:171], v[184:187], v[46:49]
	v_mfma_f32_16x16x32_bf16 v[38:41], v[150:153], v[192:195], v[38:41]
	v_mfma_f32_16x16x32_bf16 v[30:33], v[168:171], v[192:195], v[30:33]
	v_mfma_f32_16x16x32_bf16 v[22:25], v[150:153], v[200:203], v[22:25]
	v_mfma_f32_16x16x32_bf16 v[14:17], v[168:171], v[200:203], v[14:17]
	v_mfma_f32_16x16x32_bf16 v[6:9], v[150:153], v[216:219], v[6:9]
	v_mfma_f32_16x16x32_bf16 v[2:5], v[168:171], v[216:219], v[2:5]
	s_barrier
	s_add_i32 s41, s41, 2
	s_add_u32 s33, s33, 0x100
	s_addc_u32 s40, s40, 0
	s_add_u32 s6, s6, 0x100
	s_addc_u32 s7, s7, 0
	s_cmp_gt_u32 s41, 13
	s_cbranch_scc0 .LBB0_1783
	s_and_b64 vcc, exec, s[18:19]
	s_cbranch_vccz .LBB0_1786
	s_barrier

.LBB0_1799:
	s_add_u32 s26, s24, 0xfffc0080
	s_addc_u32 s27, s25, -1
	s_add_i32 s48, 0, 0x10000
	s_cmp_eq_u32 s47, 12
	s_cselect_b32 s29, s8, s27
	s_cselect_b32 s28, s9, s26
	s_cselect_b32 s27, s15, s46
	s_cselect_b32 s26, s17, s45
	s_add_i32 s52, 0, 0x14000
	s_add_i32 m0, s36, 0xc000
	s_nop 0
	global_load_lds_dwordx4 v140, s[24:25]
	s_add_i32 m0, s36, 0xe000
	s_nop 0
	global_load_lds_dwordx4 v138, s[24:25]
	ds_read_b128 v[148:151], v139
	ds_read_b128 v[152:155], v139 offset:1024
	ds_read_b128 v[156:159], v139 offset:2048
	ds_read_b128 v[160:163], v139 offset:3072
	ds_read_b128 v[164:167], v139 offset:16384
	ds_read_b128 v[168:171], v139 offset:17408
	ds_read_b128 v[172:175], v139 offset:18432
	ds_read_b128 v[180:183], v139 offset:19456
	ds_read_b128 v[184:187], v146
	ds_read_b128 v[188:191], v146 offset:1024
	ds_read_b128 v[192:195], v146 offset:2048
	ds_read_b128 v[196:199], v146 offset:3072
	ds_read_b128 v[200:203], v146 offset:4096
	ds_read_b128 v[204:207], v146 offset:5120
	ds_read_b128 v[216:219], v146 offset:6144
	ds_read_b128 v[220:223], v146 offset:7168
	s_waitcnt vmcnt(8) lgkmcnt(0)
	s_barrier
	v_mfma_f32_16x16x32_bf16 v[126:129], v[148:151], v[184:187], v[126:129]
	v_mfma_f32_16x16x32_bf16 v[122:125], v[156:159], v[184:187], v[122:125]
	v_mfma_f32_16x16x32_bf16 v[118:121], v[148:151], v[192:195], v[118:121]
	v_mfma_f32_16x16x32_bf16 v[110:113], v[156:159], v[192:195], v[110:113]
	v_mfma_f32_16x16x32_bf16 v[102:105], v[148:151], v[200:203], v[102:105]
	v_mfma_f32_16x16x32_bf16 v[94:97], v[156:159], v[200:203], v[94:97]
	v_mfma_f32_16x16x32_bf16 v[86:89], v[148:151], v[216:219], v[86:89]
	v_mfma_f32_16x16x32_bf16 v[78:81], v[156:159], v[216:219], v[78:81]
	v_mfma_f32_16x16x32_bf16 v[126:129], v[152:155], v[188:191], v[126:129]
	v_mfma_f32_16x16x32_bf16 v[122:125], v[160:163], v[188:191], v[122:125]
	v_mfma_f32_16x16x32_bf16 v[118:121], v[152:155], v[196:199], v[118:121]
	v_mfma_f32_16x16x32_bf16 v[110:113], v[160:163], v[196:199], v[110:113]
	v_mfma_f32_16x16x32_bf16 v[102:105], v[152:155], v[204:207], v[102:105]
	v_mfma_f32_16x16x32_bf16 v[94:97], v[160:163], v[204:207], v[94:97]
	v_mfma_f32_16x16x32_bf16 v[86:89], v[152:155], v[220:223], v[86:89]
	v_mfma_f32_16x16x32_bf16 v[78:81], v[160:163], v[220:223], v[78:81]
	v_mfma_f32_16x16x32_bf16 v[114:117], v[164:167], v[184:187], v[114:117]
	v_mfma_f32_16x16x32_bf16 v[106:109], v[172:175], v[184:187], v[106:109]
	v_mfma_f32_16x16x32_bf16 v[98:101], v[164:167], v[192:195], v[98:101]
	v_mfma_f32_16x16x32_bf16 v[90:93], v[172:175], v[192:195], v[90:93]
	v_mfma_f32_16x16x32_bf16 v[82:85], v[164:167], v[200:203], v[82:85]
	v_mfma_f32_16x16x32_bf16 v[74:77], v[172:175], v[200:203], v[74:77]
	v_mfma_f32_16x16x32_bf16 v[70:73], v[164:167], v[216:219], v[70:73]
	v_mfma_f32_16x16x32_bf16 v[66:69], v[172:175], v[216:219], v[66:69]
	v_mfma_f32_16x16x32_bf16 v[114:117], v[168:171], v[188:191], v[114:117]
	v_mfma_f32_16x16x32_bf16 v[106:109], v[180:183], v[188:191], v[106:109]
	v_mfma_f32_16x16x32_bf16 v[98:101], v[168:171], v[196:199], v[98:101]
	v_mfma_f32_16x16x32_bf16 v[90:93], v[180:183], v[196:199], v[90:93]
	v_mfma_f32_16x16x32_bf16 v[82:85], v[168:171], v[204:207], v[82:85]
	v_mfma_f32_16x16x32_bf16 v[74:77], v[180:183], v[204:207], v[74:77]
	v_mfma_f32_16x16x32_bf16 v[70:73], v[168:171], v[220:223], v[70:73]
	v_mfma_f32_16x16x32_bf16 v[66:69], v[180:183], v[220:223], v[66:69]
	s_barrier
	s_add_i32 s48, s48, s35
	v_lshl_add_u64 v[142:143], s[26:27], 0, v[134:135]
	s_mov_b32 m0, s48
	s_nop 0
	global_load_lds_dwordx4 v134, s[26:27]
	s_add_i32 m0, s48, 0x2000
	s_add_u32 s48, s26, 0x40000
	v_lshl_add_u64 v[176:177], s[26:27], 0, v[130:131]
	s_addc_u32 s49, s27, 0
	s_add_i32 s52, s52, s35
	global_load_lds_dwordx4 v130, s[26:27]
	s_mov_b32 m0, s52
	v_lshl_add_u64 v[224:225], s[28:29], 0, v[132:133]
	global_load_lds_dwordx4 v134, s[48:49]
	s_add_i32 m0, s52, 0x2000
	s_nop 0
	global_load_lds_dwordx4 v130, s[48:49]
	s_mov_b32 m0, s36
	v_lshl_add_u64 v[208:209], s[28:29], 0, v[136:137]
	global_load_lds_dwordx4 v136, s[28:29]
	s_mov_b32 m0, s37
	s_nop 0
	global_load_lds_dwordx4 v132, s[28:29]
	ds_read_b128 v[184:187], v146 offset:16384
	ds_read_b128 v[188:191], v146 offset:17408
	ds_read_b128 v[192:195], v146 offset:18432
	ds_read_b128 v[196:199], v146 offset:19456
	ds_read_b128 v[200:203], v146 offset:20480
	ds_read_b128 v[204:207], v146 offset:21504
	ds_read_b128 v[216:219], v146 offset:22528
	ds_read_b128 v[220:223], v146 offset:23552
	s_waitcnt vmcnt(8) lgkmcnt(0)
	s_barrier
	v_mfma_f32_16x16x32_bf16 v[62:65], v[148:151], v[184:187], v[62:65]
	v_mfma_f32_16x16x32_bf16 v[58:61], v[156:159], v[184:187], v[58:61]
	v_mfma_f32_16x16x32_bf16 v[54:57], v[148:151], v[192:195], v[54:57]
	v_mfma_f32_16x16x32_bf16 v[46:49], v[156:159], v[192:195], v[46:49]
	v_mfma_f32_16x16x32_bf16 v[38:41], v[148:151], v[200:203], v[38:41]
	v_mfma_f32_16x16x32_bf16 v[30:33], v[156:159], v[200:203], v[30:33]
	v_mfma_f32_16x16x32_bf16 v[22:25], v[148:151], v[216:219], v[22:25]
	v_mfma_f32_16x16x32_bf16 v[14:17], v[156:159], v[216:219], v[14:17]
	v_mfma_f32_16x16x32_bf16 v[62:65], v[152:155], v[188:191], v[62:65]
	v_mfma_f32_16x16x32_bf16 v[58:61], v[160:163], v[188:191], v[58:61]
	v_mfma_f32_16x16x32_bf16 v[54:57], v[152:155], v[196:199], v[54:57]
	v_mfma_f32_16x16x32_bf16 v[46:49], v[160:163], v[196:199], v[46:49]
	v_mfma_f32_16x16x32_bf16 v[38:41], v[152:155], v[204:207], v[38:41]
	v_mfma_f32_16x16x32_bf16 v[30:33], v[160:163], v[204:207], v[30:33]
	v_mfma_f32_16x16x32_bf16 v[22:25], v[152:155], v[220:223], v[22:25]
	v_mfma_f32_16x16x32_bf16 v[14:17], v[160:163], v[220:223], v[14:17]
	v_mfma_f32_16x16x32_bf16 v[50:53], v[164:167], v[184:187], v[50:53]
	v_mfma_f32_16x16x32_bf16 v[42:45], v[172:175], v[184:187], v[42:45]
	v_mfma_f32_16x16x32_bf16 v[34:37], v[164:167], v[192:195], v[34:37]
	v_mfma_f32_16x16x32_bf16 v[26:29], v[172:175], v[192:195], v[26:29]
	v_mfma_f32_16x16x32_bf16 v[18:21], v[164:167], v[200:203], v[18:21]
	v_mfma_f32_16x16x32_bf16 v[10:13], v[172:175], v[200:203], v[10:13]
	v_mfma_f32_16x16x32_bf16 v[6:9], v[164:167], v[216:219], v[6:9]
	v_mfma_f32_16x16x32_bf16 v[2:5], v[172:175], v[216:219], v[2:5]
	v_mfma_f32_16x16x32_bf16 v[50:53], v[168:171], v[188:191], v[50:53]
	v_mfma_f32_16x16x32_bf16 v[42:45], v[180:183], v[188:191], v[42:45]
	v_mfma_f32_16x16x32_bf16 v[34:37], v[168:171], v[196:199], v[34:37]
	v_mfma_f32_16x16x32_bf16 v[26:29], v[180:183], v[196:199], v[26:29]
	v_mfma_f32_16x16x32_bf16 v[18:21], v[168:171], v[204:207], v[18:21]
	v_mfma_f32_16x16x32_bf16 v[10:13], v[180:183], v[204:207], v[10:13]
	v_mfma_f32_16x16x32_bf16 v[6:9], v[168:171], v[220:223], v[6:9]
	v_mfma_f32_16x16x32_bf16 v[2:5], v[180:183], v[220:223], v[2:5]
	s_barrier
	s_add_i32 s48, 0, 0x18000
	s_add_i32 s49, 0, 0x1c000
	s_add_u32 s28, s28, 0x40000
	s_addc_u32 s29, s29, 0
	s_mov_b32 m0, s4
	s_nop 0
	global_load_lds_dwordx4 v136, s[28:29]
	s_mov_b32 m0, s33
	s_nop 0
	global_load_lds_dwordx4 v132, s[28:29]
	ds_read_b128 v[148:151], v139 offset:32768
	ds_read_b128 v[152:155], v139 offset:33792
	ds_read_b128 v[156:159], v139 offset:34816
	ds_read_b128 v[160:163], v139 offset:35840
	ds_read_b128 v[164:167], v139 offset:49152
	ds_read_b128 v[168:171], v139 offset:50176
	ds_read_b128 v[172:175], v139 offset:51200
	ds_read_b128 v[180:183], v139 offset:52224
	ds_read_b128 v[184:187], v146 offset:32768
	ds_read_b128 v[188:191], v146 offset:33792
	ds_read_b128 v[192:195], v146 offset:34816
	ds_read_b128 v[196:199], v146 offset:35840
	ds_read_b128 v[200:203], v146 offset:36864
	ds_read_b128 v[204:207], v146 offset:37888
	ds_read_b128 v[216:219], v146 offset:38912
	ds_read_b128 v[220:223], v146 offset:39936
	s_waitcnt vmcnt(8) lgkmcnt(0)
	s_barrier
	v_mfma_f32_16x16x32_bf16 v[126:129], v[148:151], v[184:187], v[126:129]
	v_mfma_f32_16x16x32_bf16 v[122:125], v[156:159], v[184:187], v[122:125]
	v_mfma_f32_16x16x32_bf16 v[118:121], v[148:151], v[192:195], v[118:121]
	v_mfma_f32_16x16x32_bf16 v[110:113], v[156:159], v[192:195], v[110:113]
	v_mfma_f32_16x16x32_bf16 v[102:105], v[148:151], v[200:203], v[102:105]
	v_mfma_f32_16x16x32_bf16 v[94:97], v[156:159], v[200:203], v[94:97]
	v_mfma_f32_16x16x32_bf16 v[86:89], v[148:151], v[216:219], v[86:89]
	v_mfma_f32_16x16x32_bf16 v[78:81], v[156:159], v[216:219], v[78:81]
	v_mfma_f32_16x16x32_bf16 v[126:129], v[152:155], v[188:191], v[126:129]
	v_mfma_f32_16x16x32_bf16 v[122:125], v[160:163], v[188:191], v[122:125]
	v_mfma_f32_16x16x32_bf16 v[118:121], v[152:155], v[196:199], v[118:121]
	v_mfma_f32_16x16x32_bf16 v[110:113], v[160:163], v[196:199], v[110:113]
	v_mfma_f32_16x16x32_bf16 v[102:105], v[152:155], v[204:207], v[102:105]
	v_mfma_f32_16x16x32_bf16 v[94:97], v[160:163], v[204:207], v[94:97]
	v_mfma_f32_16x16x32_bf16 v[86:89], v[152:155], v[220:223], v[86:89]
	v_mfma_f32_16x16x32_bf16 v[78:81], v[160:163], v[220:223], v[78:81]
	v_mfma_f32_16x16x32_bf16 v[114:117], v[164:167], v[184:187], v[114:117]
	v_mfma_f32_16x16x32_bf16 v[106:109], v[172:175], v[184:187], v[106:109]
	v_mfma_f32_16x16x32_bf16 v[98:101], v[164:167], v[192:195], v[98:101]
	v_mfma_f32_16x16x32_bf16 v[90:93], v[172:175], v[192:195], v[90:93]
	v_mfma_f32_16x16x32_bf16 v[82:85], v[164:167], v[200:203], v[82:85]
	v_mfma_f32_16x16x32_bf16 v[74:77], v[172:175], v[200:203], v[74:77]
	v_mfma_f32_16x16x32_bf16 v[70:73], v[164:167], v[216:219], v[70:73]
	v_mfma_f32_16x16x32_bf16 v[66:69], v[172:175], v[216:219], v[66:69]
	v_mfma_f32_16x16x32_bf16 v[114:117], v[168:171], v[188:191], v[114:117]
	v_mfma_f32_16x16x32_bf16 v[106:109], v[180:183], v[188:191], v[106:109]
	v_mfma_f32_16x16x32_bf16 v[98:101], v[168:171], v[196:199], v[98:101]
	v_mfma_f32_16x16x32_bf16 v[90:93], v[180:183], v[196:199], v[90:93]
	v_mfma_f32_16x16x32_bf16 v[82:85], v[168:171], v[204:207], v[82:85]
	v_mfma_f32_16x16x32_bf16 v[74:77], v[180:183], v[204:207], v[74:77]
	v_mfma_f32_16x16x32_bf16 v[70:73], v[168:171], v[220:223], v[70:73]
	v_mfma_f32_16x16x32_bf16 v[66:69], v[180:183], v[220:223], v[66:69]
	s_barrier
	s_add_i32 s28, s48, s35
	v_lshl_add_u64 v[142:143], v[142:143], 0, s[56:57]
	s_mov_b32 m0, s28
	s_nop 0
	global_load_lds_dwordx4 v[142:143], off
	s_add_i32 m0, s28, 0x2000
	s_add_u32 s26, s26, 0x40080
	v_lshl_add_u64 v[142:143], v[176:177], 0, s[56:57]
	s_addc_u32 s27, s27, 0
	s_add_i32 s28, s49, s35
	global_load_lds_dwordx4 v[142:143], off
	s_mov_b32 m0, s28
	s_nop 0
	global_load_lds_dwordx4 v134, s[26:27]
	s_add_i32 m0, s28, 0x2000
	s_nop 0
	global_load_lds_dwordx4 v130, s[26:27]
	s_mov_b32 m0, s38
	v_lshl_add_u64 v[142:143], v[208:209], 0, s[56:57]
	global_load_lds_dwordx4 v[142:143], off
	s_mov_b32 m0, s39
	v_lshl_add_u64 v[142:143], v[224:225], 0, s[56:57]
	global_load_lds_dwordx4 v[142:143], off
	ds_read_b128 v[184:187], v146 offset:49152
	ds_read_b128 v[188:191], v146 offset:50176
	ds_read_b128 v[192:195], v146 offset:51200
	ds_read_b128 v[196:199], v146 offset:52224
	ds_read_b128 v[200:203], v146 offset:53248
	ds_read_b128 v[204:207], v146 offset:54272
	ds_read_b128 v[216:219], v146 offset:55296
	ds_read_b128 v[220:223], v146 offset:56320
	s_waitcnt vmcnt(8) lgkmcnt(0)
	s_barrier
	v_mfma_f32_16x16x32_bf16 v[62:65], v[148:151], v[184:187], v[62:65]
	v_mfma_f32_16x16x32_bf16 v[58:61], v[156:159], v[184:187], v[58:61]
	v_mfma_f32_16x16x32_bf16 v[54:57], v[148:151], v[192:195], v[54:57]
	v_mfma_f32_16x16x32_bf16 v[46:49], v[156:159], v[192:195], v[46:49]
	v_mfma_f32_16x16x32_bf16 v[38:41], v[148:151], v[200:203], v[38:41]
	v_mfma_f32_16x16x32_bf16 v[30:33], v[156:159], v[200:203], v[30:33]
	v_mfma_f32_16x16x32_bf16 v[22:25], v[148:151], v[216:219], v[22:25]
	v_mfma_f32_16x16x32_bf16 v[14:17], v[156:159], v[216:219], v[14:17]
	v_mfma_f32_16x16x32_bf16 v[62:65], v[152:155], v[188:191], v[62:65]
	v_mfma_f32_16x16x32_bf16 v[58:61], v[160:163], v[188:191], v[58:61]
	v_mfma_f32_16x16x32_bf16 v[54:57], v[152:155], v[196:199], v[54:57]
	v_mfma_f32_16x16x32_bf16 v[46:49], v[160:163], v[196:199], v[46:49]
	v_mfma_f32_16x16x32_bf16 v[38:41], v[152:155], v[204:207], v[38:41]
	v_mfma_f32_16x16x32_bf16 v[30:33], v[160:163], v[204:207], v[30:33]
	v_mfma_f32_16x16x32_bf16 v[22:25], v[152:155], v[220:223], v[22:25]
	v_mfma_f32_16x16x32_bf16 v[14:17], v[160:163], v[220:223], v[14:17]
	v_mfma_f32_16x16x32_bf16 v[50:53], v[164:167], v[184:187], v[50:53]
	v_mfma_f32_16x16x32_bf16 v[42:45], v[172:175], v[184:187], v[42:45]
	v_mfma_f32_16x16x32_bf16 v[34:37], v[164:167], v[192:195], v[34:37]
	v_mfma_f32_16x16x32_bf16 v[26:29], v[172:175], v[192:195], v[26:29]
	v_mfma_f32_16x16x32_bf16 v[18:21], v[164:167], v[200:203], v[18:21]
	v_mfma_f32_16x16x32_bf16 v[10:13], v[172:175], v[200:203], v[10:13]
	v_mfma_f32_16x16x32_bf16 v[6:9], v[164:167], v[216:219], v[6:9]
	v_mfma_f32_16x16x32_bf16 v[2:5], v[172:175], v[216:219], v[2:5]
	v_mfma_f32_16x16x32_bf16 v[50:53], v[168:171], v[188:191], v[50:53]
	v_mfma_f32_16x16x32_bf16 v[42:45], v[180:183], v[188:191], v[42:45]
	v_mfma_f32_16x16x32_bf16 v[34:37], v[168:171], v[196:199], v[34:37]
	v_mfma_f32_16x16x32_bf16 v[26:29], v[180:183], v[196:199], v[26:29]
	v_mfma_f32_16x16x32_bf16 v[18:21], v[168:171], v[204:207], v[18:21]
	v_mfma_f32_16x16x32_bf16 v[10:13], v[180:183], v[204:207], v[10:13]
	v_mfma_f32_16x16x32_bf16 v[6:9], v[168:171], v[220:223], v[6:9]
	v_mfma_f32_16x16x32_bf16 v[2:5], v[180:183], v[220:223], v[2:5]
	s_barrier
	s_add_i32 s47, s47, 2
	s_add_u32 s45, s45, 0x100
	s_addc_u32 s46, s46, 0
	s_add_u32 s24, s24, 0x100
	s_addc_u32 s25, s25, 0
	s_cmp_gt_u32 s47, 13
	s_cbranch_scc0 .LBB0_1799
	s_and_b64 vcc, exec, s[12:13]
	s_cbranch_vccz .LBB0_1802
	s_barrier

.LBB0_2626:
	s_add_u32 s26, s6, 0xfffc0080
	s_addc_u32 s27, s7, -1
	s_add_i32 s50, 0, 0x10000
	s_cmp_eq_u32 s49, 12
	s_cselect_b32 s29, s21, s27
	s_cselect_b32 s28, s33, s26
	s_cselect_b32 s27, s19, s48
	s_cselect_b32 s26, s40, s41
	s_add_i32 s58, 0, 0x14000
	s_add_i32 m0, s36, 0xc000
	s_nop 0
	global_load_lds_dwordx4 v168, s[6:7]
	s_add_i32 m0, s36, 0xe000
	s_nop 0
	global_load_lds_dwordx4 v166, s[6:7]
	ds_read_b128 v[130:133], v167
	ds_read_b128 v[134:137], v167 offset:1024
	ds_read_b128 v[138:141], v167 offset:2048
	ds_read_b128 v[142:145], v167 offset:3072
	ds_read_b128 v[146:149], v167 offset:16384
	ds_read_b128 v[150:153], v167 offset:17408
	ds_read_b128 v[154:157], v167 offset:18432
	ds_read_b128 v[170:173], v167 offset:19456
	ds_read_b128 v[174:177], v183
	ds_read_b128 v[184:187], v183 offset:1024
	ds_read_b128 v[188:191], v183 offset:2048
	ds_read_b128 v[192:195], v183 offset:3072
	ds_read_b128 v[196:199], v183 offset:4096
	ds_read_b128 v[200:203], v183 offset:5120
	ds_read_b128 v[204:207], v183 offset:6144
	ds_read_b128 v[216:219], v183 offset:7168
	s_waitcnt vmcnt(8) lgkmcnt(0)
	s_barrier
	v_mfma_f32_16x16x32_bf16 v[126:129], v[130:133], v[174:177], v[126:129]
	v_mfma_f32_16x16x32_bf16 v[122:125], v[138:141], v[174:177], v[122:125]
	v_mfma_f32_16x16x32_bf16 v[110:113], v[130:133], v[188:191], v[110:113]
	v_mfma_f32_16x16x32_bf16 v[106:109], v[138:141], v[188:191], v[106:109]
	v_mfma_f32_16x16x32_bf16 v[94:97], v[130:133], v[196:199], v[94:97]
	v_mfma_f32_16x16x32_bf16 v[90:93], v[138:141], v[196:199], v[90:93]
	v_mfma_f32_16x16x32_bf16 v[78:81], v[130:133], v[204:207], v[78:81]
	v_mfma_f32_16x16x32_bf16 v[74:77], v[138:141], v[204:207], v[74:77]
	v_mfma_f32_16x16x32_bf16 v[126:129], v[134:137], v[184:187], v[126:129]
	v_mfma_f32_16x16x32_bf16 v[122:125], v[142:145], v[184:187], v[122:125]
	v_mfma_f32_16x16x32_bf16 v[110:113], v[134:137], v[192:195], v[110:113]
	v_mfma_f32_16x16x32_bf16 v[106:109], v[142:145], v[192:195], v[106:109]
	v_mfma_f32_16x16x32_bf16 v[94:97], v[134:137], v[200:203], v[94:97]
	v_mfma_f32_16x16x32_bf16 v[90:93], v[142:145], v[200:203], v[90:93]
	v_mfma_f32_16x16x32_bf16 v[78:81], v[134:137], v[216:219], v[78:81]
	v_mfma_f32_16x16x32_bf16 v[74:77], v[142:145], v[216:219], v[74:77]
	v_mfma_f32_16x16x32_bf16 v[118:121], v[146:149], v[174:177], v[118:121]
	v_mfma_f32_16x16x32_bf16 v[114:117], v[154:157], v[174:177], v[114:117]
	v_mfma_f32_16x16x32_bf16 v[102:105], v[146:149], v[188:191], v[102:105]
	v_mfma_f32_16x16x32_bf16 v[98:101], v[154:157], v[188:191], v[98:101]
	v_mfma_f32_16x16x32_bf16 v[86:89], v[146:149], v[196:199], v[86:89]
	v_mfma_f32_16x16x32_bf16 v[82:85], v[154:157], v[196:199], v[82:85]
	v_mfma_f32_16x16x32_bf16 v[70:73], v[146:149], v[204:207], v[70:73]
	v_mfma_f32_16x16x32_bf16 v[66:69], v[154:157], v[204:207], v[66:69]
	v_mfma_f32_16x16x32_bf16 v[118:121], v[150:153], v[184:187], v[118:121]
	v_mfma_f32_16x16x32_bf16 v[114:117], v[170:173], v[184:187], v[114:117]
	v_mfma_f32_16x16x32_bf16 v[102:105], v[150:153], v[192:195], v[102:105]
	v_mfma_f32_16x16x32_bf16 v[98:101], v[170:173], v[192:195], v[98:101]
	v_mfma_f32_16x16x32_bf16 v[86:89], v[150:153], v[200:203], v[86:89]
	v_mfma_f32_16x16x32_bf16 v[82:85], v[170:173], v[200:203], v[82:85]
	v_mfma_f32_16x16x32_bf16 v[70:73], v[150:153], v[216:219], v[70:73]
	v_mfma_f32_16x16x32_bf16 v[66:69], v[170:173], v[216:219], v[66:69]
	s_barrier
	s_add_i32 s50, s50, s35
	v_lshl_add_u64 v[178:179], s[26:27], 0, v[162:163]
	s_mov_b32 m0, s50
	s_nop 0
	global_load_lds_dwordx4 v162, s[26:27]
	s_add_i32 m0, s50, 0x2000
	s_add_u32 s52, s26, 0x40000
	v_lshl_add_u64 v[208:209], s[26:27], 0, v[158:159]
	s_addc_u32 s53, s27, 0
	s_add_i32 s50, s58, s35
	global_load_lds_dwordx4 v158, s[26:27]
	s_mov_b32 m0, s50
	v_lshl_add_u64 v[222:223], s[28:29], 0, v[160:161]
	global_load_lds_dwordx4 v162, s[52:53]
	s_add_i32 m0, s50, 0x2000
	s_nop 0
	global_load_lds_dwordx4 v158, s[52:53]
	s_mov_b32 m0, s36
	v_lshl_add_u64 v[220:221], s[28:29], 0, v[164:165]
	global_load_lds_dwordx4 v164, s[28:29]
	s_mov_b32 m0, s37
	s_nop 0
	global_load_lds_dwordx4 v160, s[28:29]
	ds_read_b128 v[174:177], v183 offset:16384
	ds_read_b128 v[184:187], v183 offset:17408
	ds_read_b128 v[188:191], v183 offset:18432
	ds_read_b128 v[192:195], v183 offset:19456
	ds_read_b128 v[196:199], v183 offset:20480
	ds_read_b128 v[200:203], v183 offset:21504
	ds_read_b128 v[204:207], v183 offset:22528
	ds_read_b128 v[216:219], v183 offset:23552
	s_waitcnt vmcnt(8) lgkmcnt(0)
	s_barrier
	v_mfma_f32_16x16x32_bf16 v[62:65], v[130:133], v[174:177], v[62:65]
	v_mfma_f32_16x16x32_bf16 v[58:61], v[138:141], v[174:177], v[58:61]
	v_mfma_f32_16x16x32_bf16 v[46:49], v[130:133], v[188:191], v[46:49]
	v_mfma_f32_16x16x32_bf16 v[42:45], v[138:141], v[188:191], v[42:45]
	v_mfma_f32_16x16x32_bf16 v[30:33], v[130:133], v[196:199], v[30:33]
	v_mfma_f32_16x16x32_bf16 v[26:29], v[138:141], v[196:199], v[26:29]
	v_mfma_f32_16x16x32_bf16 v[14:17], v[130:133], v[204:207], v[14:17]
	v_mfma_f32_16x16x32_bf16 v[10:13], v[138:141], v[204:207], v[10:13]
	v_mfma_f32_16x16x32_bf16 v[62:65], v[134:137], v[184:187], v[62:65]
	v_mfma_f32_16x16x32_bf16 v[58:61], v[142:145], v[184:187], v[58:61]
	v_mfma_f32_16x16x32_bf16 v[46:49], v[134:137], v[192:195], v[46:49]
	v_mfma_f32_16x16x32_bf16 v[42:45], v[142:145], v[192:195], v[42:45]
	v_mfma_f32_16x16x32_bf16 v[30:33], v[134:137], v[200:203], v[30:33]
	v_mfma_f32_16x16x32_bf16 v[26:29], v[142:145], v[200:203], v[26:29]
	v_mfma_f32_16x16x32_bf16 v[14:17], v[134:137], v[216:219], v[14:17]
	v_mfma_f32_16x16x32_bf16 v[10:13], v[142:145], v[216:219], v[10:13]
	v_mfma_f32_16x16x32_bf16 v[54:57], v[146:149], v[174:177], v[54:57]
	v_mfma_f32_16x16x32_bf16 v[50:53], v[154:157], v[174:177], v[50:53]
	v_mfma_f32_16x16x32_bf16 v[38:41], v[146:149], v[188:191], v[38:41]
	v_mfma_f32_16x16x32_bf16 v[34:37], v[154:157], v[188:191], v[34:37]
	v_mfma_f32_16x16x32_bf16 v[22:25], v[146:149], v[196:199], v[22:25]
	v_mfma_f32_16x16x32_bf16 v[18:21], v[154:157], v[196:199], v[18:21]
	v_mfma_f32_16x16x32_bf16 v[6:9], v[146:149], v[204:207], v[6:9]
	v_mfma_f32_16x16x32_bf16 v[2:5], v[154:157], v[204:207], v[2:5]
	v_mfma_f32_16x16x32_bf16 v[54:57], v[150:153], v[184:187], v[54:57]
	v_mfma_f32_16x16x32_bf16 v[50:53], v[170:173], v[184:187], v[50:53]
	v_mfma_f32_16x16x32_bf16 v[38:41], v[150:153], v[192:195], v[38:41]
	v_mfma_f32_16x16x32_bf16 v[34:37], v[170:173], v[192:195], v[34:37]
	v_mfma_f32_16x16x32_bf16 v[22:25], v[150:153], v[200:203], v[22:25]
	v_mfma_f32_16x16x32_bf16 v[18:21], v[170:173], v[200:203], v[18:21]
	v_mfma_f32_16x16x32_bf16 v[6:9], v[150:153], v[216:219], v[6:9]
	v_mfma_f32_16x16x32_bf16 v[2:5], v[170:173], v[216:219], v[2:5]
	s_barrier
	s_add_i32 s50, 0, 0x18000
	s_add_i32 s52, 0, 0x1c000
	s_add_u32 s28, s28, 0x40000
	s_addc_u32 s29, s29, 0
	s_mov_b32 m0, s42
	s_nop 0
	global_load_lds_dwordx4 v164, s[28:29]
	s_mov_b32 m0, s43
	s_nop 0
	global_load_lds_dwordx4 v160, s[28:29]
	ds_read_b128 v[130:133], v167 offset:32768
	ds_read_b128 v[134:137], v167 offset:33792
	ds_read_b128 v[138:141], v167 offset:34816
	ds_read_b128 v[142:145], v167 offset:35840
	ds_read_b128 v[146:149], v167 offset:49152
	ds_read_b128 v[150:153], v167 offset:50176
	ds_read_b128 v[154:157], v167 offset:51200
	ds_read_b128 v[170:173], v167 offset:52224
	ds_read_b128 v[174:177], v183 offset:32768
	ds_read_b128 v[184:187], v183 offset:33792
	ds_read_b128 v[188:191], v183 offset:34816
	ds_read_b128 v[192:195], v183 offset:35840
	ds_read_b128 v[196:199], v183 offset:36864
	ds_read_b128 v[200:203], v183 offset:37888
	ds_read_b128 v[204:207], v183 offset:38912
	ds_read_b128 v[216:219], v183 offset:39936
	s_waitcnt vmcnt(8) lgkmcnt(0)
	s_barrier
	v_mfma_f32_16x16x32_bf16 v[126:129], v[130:133], v[174:177], v[126:129]
	v_mfma_f32_16x16x32_bf16 v[122:125], v[138:141], v[174:177], v[122:125]
	v_mfma_f32_16x16x32_bf16 v[110:113], v[130:133], v[188:191], v[110:113]
	v_mfma_f32_16x16x32_bf16 v[106:109], v[138:141], v[188:191], v[106:109]
	v_mfma_f32_16x16x32_bf16 v[94:97], v[130:133], v[196:199], v[94:97]
	v_mfma_f32_16x16x32_bf16 v[90:93], v[138:141], v[196:199], v[90:93]
	v_mfma_f32_16x16x32_bf16 v[78:81], v[130:133], v[204:207], v[78:81]
	v_mfma_f32_16x16x32_bf16 v[74:77], v[138:141], v[204:207], v[74:77]
	v_mfma_f32_16x16x32_bf16 v[126:129], v[134:137], v[184:187], v[126:129]
	v_mfma_f32_16x16x32_bf16 v[122:125], v[142:145], v[184:187], v[122:125]
	v_mfma_f32_16x16x32_bf16 v[110:113], v[134:137], v[192:195], v[110:113]
	v_mfma_f32_16x16x32_bf16 v[106:109], v[142:145], v[192:195], v[106:109]
	v_mfma_f32_16x16x32_bf16 v[94:97], v[134:137], v[200:203], v[94:97]
	v_mfma_f32_16x16x32_bf16 v[90:93], v[142:145], v[200:203], v[90:93]
	v_mfma_f32_16x16x32_bf16 v[78:81], v[134:137], v[216:219], v[78:81]
	v_mfma_f32_16x16x32_bf16 v[74:77], v[142:145], v[216:219], v[74:77]
	v_mfma_f32_16x16x32_bf16 v[118:121], v[146:149], v[174:177], v[118:121]
	v_mfma_f32_16x16x32_bf16 v[114:117], v[154:157], v[174:177], v[114:117]
	v_mfma_f32_16x16x32_bf16 v[102:105], v[146:149], v[188:191], v[102:105]
	v_mfma_f32_16x16x32_bf16 v[98:101], v[154:157], v[188:191], v[98:101]
	v_mfma_f32_16x16x32_bf16 v[86:89], v[146:149], v[196:199], v[86:89]
	v_mfma_f32_16x16x32_bf16 v[82:85], v[154:157], v[196:199], v[82:85]
	v_mfma_f32_16x16x32_bf16 v[70:73], v[146:149], v[204:207], v[70:73]
	v_mfma_f32_16x16x32_bf16 v[66:69], v[154:157], v[204:207], v[66:69]
	v_mfma_f32_16x16x32_bf16 v[118:121], v[150:153], v[184:187], v[118:121]
	v_mfma_f32_16x16x32_bf16 v[114:117], v[170:173], v[184:187], v[114:117]
	v_mfma_f32_16x16x32_bf16 v[102:105], v[150:153], v[192:195], v[102:105]
	v_mfma_f32_16x16x32_bf16 v[98:101], v[170:173], v[192:195], v[98:101]
	v_mfma_f32_16x16x32_bf16 v[86:89], v[150:153], v[200:203], v[86:89]
	v_mfma_f32_16x16x32_bf16 v[82:85], v[170:173], v[200:203], v[82:85]
	v_mfma_f32_16x16x32_bf16 v[70:73], v[150:153], v[216:219], v[70:73]
	v_mfma_f32_16x16x32_bf16 v[66:69], v[170:173], v[216:219], v[66:69]
	s_barrier
	s_add_i32 s28, s50, s35
	v_lshl_add_u64 v[178:179], v[178:179], 0, s[56:57]
	s_mov_b32 m0, s28
	s_nop 0
	global_load_lds_dwordx4 v[178:179], off
	s_add_i32 m0, s28, 0x2000
	s_add_u32 s26, s26, 0x40080
	v_lshl_add_u64 v[178:179], v[208:209], 0, s[56:57]
	s_addc_u32 s27, s27, 0
	s_add_i32 s28, s52, s35
	global_load_lds_dwordx4 v[178:179], off
	s_mov_b32 m0, s28
	s_nop 0
	global_load_lds_dwordx4 v162, s[26:27]
	s_add_i32 m0, s28, 0x2000
	s_nop 0
	global_load_lds_dwordx4 v158, s[26:27]
	s_mov_b32 m0, s44
	v_lshl_add_u64 v[178:179], v[220:221], 0, s[56:57]
	global_load_lds_dwordx4 v[178:179], off
	s_mov_b32 m0, s45
	v_lshl_add_u64 v[178:179], v[222:223], 0, s[56:57]
	global_load_lds_dwordx4 v[178:179], off
	ds_read_b128 v[174:177], v183 offset:49152
	ds_read_b128 v[184:187], v183 offset:50176
	ds_read_b128 v[188:191], v183 offset:51200
	ds_read_b128 v[192:195], v183 offset:52224
	ds_read_b128 v[196:199], v183 offset:53248
	ds_read_b128 v[200:203], v183 offset:54272
	ds_read_b128 v[204:207], v183 offset:55296
	ds_read_b128 v[216:219], v183 offset:56320
	s_waitcnt vmcnt(8) lgkmcnt(0)
	s_barrier
	v_mfma_f32_16x16x32_bf16 v[62:65], v[130:133], v[174:177], v[62:65]
	v_mfma_f32_16x16x32_bf16 v[58:61], v[138:141], v[174:177], v[58:61]
	v_mfma_f32_16x16x32_bf16 v[46:49], v[130:133], v[188:191], v[46:49]
	v_mfma_f32_16x16x32_bf16 v[42:45], v[138:141], v[188:191], v[42:45]
	v_mfma_f32_16x16x32_bf16 v[30:33], v[130:133], v[196:199], v[30:33]
	v_mfma_f32_16x16x32_bf16 v[26:29], v[138:141], v[196:199], v[26:29]
	v_mfma_f32_16x16x32_bf16 v[14:17], v[130:133], v[204:207], v[14:17]
	v_mfma_f32_16x16x32_bf16 v[10:13], v[138:141], v[204:207], v[10:13]
	v_mfma_f32_16x16x32_bf16 v[62:65], v[134:137], v[184:187], v[62:65]
	v_mfma_f32_16x16x32_bf16 v[58:61], v[142:145], v[184:187], v[58:61]
	v_mfma_f32_16x16x32_bf16 v[46:49], v[134:137], v[192:195], v[46:49]
	v_mfma_f32_16x16x32_bf16 v[42:45], v[142:145], v[192:195], v[42:45]
	v_mfma_f32_16x16x32_bf16 v[30:33], v[134:137], v[200:203], v[30:33]
	v_mfma_f32_16x16x32_bf16 v[26:29], v[142:145], v[200:203], v[26:29]
	v_mfma_f32_16x16x32_bf16 v[14:17], v[134:137], v[216:219], v[14:17]
	v_mfma_f32_16x16x32_bf16 v[10:13], v[142:145], v[216:219], v[10:13]
	v_mfma_f32_16x16x32_bf16 v[54:57], v[146:149], v[174:177], v[54:57]
	v_mfma_f32_16x16x32_bf16 v[50:53], v[154:157], v[174:177], v[50:53]
	v_mfma_f32_16x16x32_bf16 v[38:41], v[146:149], v[188:191], v[38:41]
	v_mfma_f32_16x16x32_bf16 v[34:37], v[154:157], v[188:191], v[34:37]
	v_mfma_f32_16x16x32_bf16 v[22:25], v[146:149], v[196:199], v[22:25]
	v_mfma_f32_16x16x32_bf16 v[18:21], v[154:157], v[196:199], v[18:21]
	v_mfma_f32_16x16x32_bf16 v[6:9], v[146:149], v[204:207], v[6:9]
	v_mfma_f32_16x16x32_bf16 v[2:5], v[154:157], v[204:207], v[2:5]
	v_mfma_f32_16x16x32_bf16 v[54:57], v[150:153], v[184:187], v[54:57]
	v_mfma_f32_16x16x32_bf16 v[50:53], v[170:173], v[184:187], v[50:53]
	v_mfma_f32_16x16x32_bf16 v[38:41], v[150:153], v[192:195], v[38:41]
	v_mfma_f32_16x16x32_bf16 v[34:37], v[170:173], v[192:195], v[34:37]
	v_mfma_f32_16x16x32_bf16 v[22:25], v[150:153], v[200:203], v[22:25]
	v_mfma_f32_16x16x32_bf16 v[18:21], v[170:173], v[200:203], v[18:21]
	v_mfma_f32_16x16x32_bf16 v[6:9], v[150:153], v[216:219], v[6:9]
	v_mfma_f32_16x16x32_bf16 v[2:5], v[170:173], v[216:219], v[2:5]
	s_barrier
	s_add_i32 s49, s49, 2
	s_add_u32 s41, s41, 0x100
	s_addc_u32 s48, s48, 0
	s_add_u32 s6, s6, 0x100
	s_addc_u32 s7, s7, 0
	s_cmp_gt_u32 s49, 13
	s_cbranch_scc0 .LBB0_2626
	s_and_b64 vcc, exec, s[16:17]
	s_cbranch_vccz .LBB0_2629
	s_barrier

.LBB0_2703:
	s_add_u32 s44, s24, s36
	s_addc_u32 s45, s25, s37
	s_add_u32 s44, s44, 0x100
	s_addc_u32 s45, s45, 0
	s_add_u32 s50, s59, s36
	s_addc_u32 s64, s82, s37
	s_add_i32 s65, 0, 0x10000
	s_cmpk_eq_i32 s36, 0x1f00
	s_cselect_b32 s47, s29, s45
	s_cselect_b32 s46, s83, s44
	s_cselect_b32 s45, s27, s64
	s_cselect_b32 s44, s84, s50
	s_add_i32 s50, 0, 0x14000
	v_lshl_add_u64 v[164:165], v[144:145], 0, s[36:37]
	s_add_i32 m0, s4, 0xc000
	s_nop 0
	global_load_lds_dwordx4 v[164:165], off
	s_add_i32 m0, s4, 0xe000
	v_lshl_add_u64 v[164:165], v[142:143], 0, s[36:37]
	global_load_lds_dwordx4 v[164:165], off
	ds_read_b128 v[148:151], v241
	ds_read_b128 v[152:155], v241 offset:1024
	ds_read_b128 v[156:159], v241 offset:2048
	ds_read_b128 v[160:163], v241 offset:3072
	ds_read_b128 v[168:171], v241 offset:16384
	ds_read_b128 v[172:175], v241 offset:17408
	ds_read_b128 v[176:179], v241 offset:18432
	ds_read_b128 v[180:183], v241 offset:19456
	ds_read_b128 v[184:187], v147
	ds_read_b128 v[188:191], v147 offset:1024
	ds_read_b128 v[192:195], v147 offset:2048
	ds_read_b128 v[196:199], v147 offset:3072
	ds_read_b128 v[200:203], v147 offset:4096
	ds_read_b128 v[204:207], v147 offset:5120
	ds_read_b128 v[216:219], v147 offset:6144
	ds_read_b128 v[220:223], v147 offset:7168
	s_waitcnt vmcnt(8) lgkmcnt(0)
	s_barrier
	v_mfma_f32_16x16x32_bf16 v[134:137], v[148:151], v[184:187], v[134:137]
	v_mfma_f32_16x16x32_bf16 v[130:133], v[156:159], v[184:187], v[130:133]
	v_mfma_f32_16x16x32_bf16 v[110:113], v[148:151], v[192:195], v[110:113]
	v_mfma_f32_16x16x32_bf16 v[106:109], v[156:159], v[192:195], v[106:109]
	v_mfma_f32_16x16x32_bf16 v[94:97], v[148:151], v[200:203], v[94:97]
	v_mfma_f32_16x16x32_bf16 v[90:93], v[156:159], v[200:203], v[90:93]
	v_mfma_f32_16x16x32_bf16 v[78:81], v[148:151], v[216:219], v[78:81]
	v_mfma_f32_16x16x32_bf16 v[74:77], v[156:159], v[216:219], v[74:77]
	v_mfma_f32_16x16x32_bf16 v[134:137], v[152:155], v[188:191], v[134:137]
	v_mfma_f32_16x16x32_bf16 v[130:133], v[160:163], v[188:191], v[130:133]
	v_mfma_f32_16x16x32_bf16 v[110:113], v[152:155], v[196:199], v[110:113]
	v_mfma_f32_16x16x32_bf16 v[106:109], v[160:163], v[196:199], v[106:109]
	v_mfma_f32_16x16x32_bf16 v[94:97], v[152:155], v[204:207], v[94:97]
	v_mfma_f32_16x16x32_bf16 v[90:93], v[160:163], v[204:207], v[90:93]
	v_mfma_f32_16x16x32_bf16 v[78:81], v[152:155], v[220:223], v[78:81]
	v_mfma_f32_16x16x32_bf16 v[74:77], v[160:163], v[220:223], v[74:77]
	v_mfma_f32_16x16x32_bf16 v[122:125], v[168:171], v[184:187], v[122:125]
	v_mfma_f32_16x16x32_bf16 v[114:117], v[176:179], v[184:187], v[114:117]
	v_mfma_f32_16x16x32_bf16 v[102:105], v[168:171], v[192:195], v[102:105]
	v_mfma_f32_16x16x32_bf16 v[98:101], v[176:179], v[192:195], v[98:101]
	v_mfma_f32_16x16x32_bf16 v[86:89], v[168:171], v[200:203], v[86:89]
	v_mfma_f32_16x16x32_bf16 v[82:85], v[176:179], v[200:203], v[82:85]
	v_mfma_f32_16x16x32_bf16 v[70:73], v[168:171], v[216:219], v[70:73]
	v_mfma_f32_16x16x32_bf16 v[66:69], v[176:179], v[216:219], v[66:69]
	v_mfma_f32_16x16x32_bf16 v[122:125], v[172:175], v[188:191], v[122:125]
	v_mfma_f32_16x16x32_bf16 v[114:117], v[180:183], v[188:191], v[114:117]
	v_mfma_f32_16x16x32_bf16 v[102:105], v[172:175], v[196:199], v[102:105]
	v_mfma_f32_16x16x32_bf16 v[98:101], v[180:183], v[196:199], v[98:101]
	v_mfma_f32_16x16x32_bf16 v[86:89], v[172:175], v[204:207], v[86:89]
	v_mfma_f32_16x16x32_bf16 v[82:85], v[180:183], v[204:207], v[82:85]
	v_mfma_f32_16x16x32_bf16 v[70:73], v[172:175], v[220:223], v[70:73]
	v_mfma_f32_16x16x32_bf16 v[66:69], v[180:183], v[220:223], v[66:69]
	s_barrier
	s_add_i32 s64, s65, s77
	v_lshl_add_u64 v[164:165], s[44:45], 0, v[126:127]
	s_mov_b32 m0, s64
	s_nop 0
	global_load_lds_dwordx4 v126, s[44:45]
	s_add_i32 m0, s64, 0x2000
	s_add_u32 s92, s44, 0x100000
	v_lshl_add_u64 v[208:209], s[44:45], 0, v[118:119]
	s_addc_u32 s93, s45, 0
	s_add_i32 s50, s50, s77
	global_load_lds_dwordx4 v118, s[44:45]
	s_mov_b32 m0, s50
	v_lshl_add_u64 v[242:243], s[46:47], 0, v[120:121]
	global_load_lds_dwordx4 v126, s[92:93]
	s_add_i32 m0, s50, 0x2000
	s_nop 0
	global_load_lds_dwordx4 v118, s[92:93]
	s_mov_b32 m0, s4
	v_lshl_add_u64 v[224:225], s[46:47], 0, v[128:129]
	global_load_lds_dwordx4 v128, s[46:47]
	s_mov_b32 m0, s33
	s_nop 0
	global_load_lds_dwordx4 v120, s[46:47]
	ds_read_b128 v[184:187], v147 offset:16384
	ds_read_b128 v[188:191], v147 offset:17408
	ds_read_b128 v[192:195], v147 offset:18432
	ds_read_b128 v[196:199], v147 offset:19456
	ds_read_b128 v[200:203], v147 offset:20480
	ds_read_b128 v[204:207], v147 offset:21504
	ds_read_b128 v[216:219], v147 offset:22528
	ds_read_b128 v[220:223], v147 offset:23552
	s_waitcnt vmcnt(8) lgkmcnt(0)
	s_barrier
	v_mfma_f32_16x16x32_bf16 v[62:65], v[148:151], v[184:187], v[62:65]
	v_mfma_f32_16x16x32_bf16 v[58:61], v[156:159], v[184:187], v[58:61]
	v_mfma_f32_16x16x32_bf16 v[46:49], v[148:151], v[192:195], v[46:49]
	v_mfma_f32_16x16x32_bf16 v[42:45], v[156:159], v[192:195], v[42:45]
	v_mfma_f32_16x16x32_bf16 v[30:33], v[148:151], v[200:203], v[30:33]
	v_mfma_f32_16x16x32_bf16 v[26:29], v[156:159], v[200:203], v[26:29]
	v_mfma_f32_16x16x32_bf16 v[14:17], v[148:151], v[216:219], v[14:17]
	v_mfma_f32_16x16x32_bf16 v[10:13], v[156:159], v[216:219], v[10:13]
	v_mfma_f32_16x16x32_bf16 v[62:65], v[152:155], v[188:191], v[62:65]
	v_mfma_f32_16x16x32_bf16 v[58:61], v[160:163], v[188:191], v[58:61]
	v_mfma_f32_16x16x32_bf16 v[46:49], v[152:155], v[196:199], v[46:49]
	v_mfma_f32_16x16x32_bf16 v[42:45], v[160:163], v[196:199], v[42:45]
	v_mfma_f32_16x16x32_bf16 v[30:33], v[152:155], v[204:207], v[30:33]
	v_mfma_f32_16x16x32_bf16 v[26:29], v[160:163], v[204:207], v[26:29]
	v_mfma_f32_16x16x32_bf16 v[14:17], v[152:155], v[220:223], v[14:17]
	v_mfma_f32_16x16x32_bf16 v[10:13], v[160:163], v[220:223], v[10:13]
	v_mfma_f32_16x16x32_bf16 v[54:57], v[168:171], v[184:187], v[54:57]
	v_mfma_f32_16x16x32_bf16 v[50:53], v[176:179], v[184:187], v[50:53]
	v_mfma_f32_16x16x32_bf16 v[38:41], v[168:171], v[192:195], v[38:41]
	v_mfma_f32_16x16x32_bf16 v[34:37], v[176:179], v[192:195], v[34:37]
	v_mfma_f32_16x16x32_bf16 v[22:25], v[168:171], v[200:203], v[22:25]
	v_mfma_f32_16x16x32_bf16 v[18:21], v[176:179], v[200:203], v[18:21]
	v_mfma_f32_16x16x32_bf16 v[6:9], v[168:171], v[216:219], v[6:9]
	v_mfma_f32_16x16x32_bf16 v[2:5], v[176:179], v[216:219], v[2:5]
	v_mfma_f32_16x16x32_bf16 v[54:57], v[172:175], v[188:191], v[54:57]
	v_mfma_f32_16x16x32_bf16 v[50:53], v[180:183], v[188:191], v[50:53]
	v_mfma_f32_16x16x32_bf16 v[38:41], v[172:175], v[196:199], v[38:41]
	v_mfma_f32_16x16x32_bf16 v[34:37], v[180:183], v[196:199], v[34:37]
	v_mfma_f32_16x16x32_bf16 v[22:25], v[172:175], v[204:207], v[22:25]
	v_mfma_f32_16x16x32_bf16 v[18:21], v[180:183], v[204:207], v[18:21]
	v_mfma_f32_16x16x32_bf16 v[6:9], v[172:175], v[220:223], v[6:9]
	v_mfma_f32_16x16x32_bf16 v[2:5], v[180:183], v[220:223], v[2:5]
	s_barrier
	s_add_i32 s50, 0, 0x18000
	s_add_i32 s64, 0, 0x1c000
	s_add_u32 s46, s46, 0x100000
	s_addc_u32 s47, s47, 0
	s_mov_b32 m0, s78
	s_nop 0
	global_load_lds_dwordx4 v128, s[46:47]
	s_mov_b32 m0, s79
	v_lshl_add_u64 v[244:245], s[46:47], 0, v[120:121]
	global_load_lds_dwordx4 v120, s[46:47]
	ds_read_b128 v[148:151], v241 offset:32768
	ds_read_b128 v[152:155], v241 offset:33792
	ds_read_b128 v[156:159], v241 offset:34816
	ds_read_b128 v[160:163], v241 offset:35840
	ds_read_b128 v[168:171], v241 offset:49152
	ds_read_b128 v[172:175], v241 offset:50176
	ds_read_b128 v[176:179], v241 offset:51200
	ds_read_b128 v[180:183], v241 offset:52224
	ds_read_b128 v[184:187], v147 offset:32768
	ds_read_b128 v[188:191], v147 offset:33792
	ds_read_b128 v[192:195], v147 offset:34816
	ds_read_b128 v[196:199], v147 offset:35840
	ds_read_b128 v[200:203], v147 offset:36864
	ds_read_b128 v[204:207], v147 offset:37888
	ds_read_b128 v[216:219], v147 offset:38912
	ds_read_b128 v[220:223], v147 offset:39936
	s_waitcnt vmcnt(8) lgkmcnt(0)
	s_barrier
	v_mfma_f32_16x16x32_bf16 v[134:137], v[148:151], v[184:187], v[134:137]
	v_mfma_f32_16x16x32_bf16 v[130:133], v[156:159], v[184:187], v[130:133]
	v_mfma_f32_16x16x32_bf16 v[110:113], v[148:151], v[192:195], v[110:113]
	v_mfma_f32_16x16x32_bf16 v[106:109], v[156:159], v[192:195], v[106:109]
	v_mfma_f32_16x16x32_bf16 v[94:97], v[148:151], v[200:203], v[94:97]
	v_mfma_f32_16x16x32_bf16 v[90:93], v[156:159], v[200:203], v[90:93]
	v_mfma_f32_16x16x32_bf16 v[78:81], v[148:151], v[216:219], v[78:81]
	v_mfma_f32_16x16x32_bf16 v[74:77], v[156:159], v[216:219], v[74:77]
	v_mfma_f32_16x16x32_bf16 v[134:137], v[152:155], v[188:191], v[134:137]
	v_mfma_f32_16x16x32_bf16 v[130:133], v[160:163], v[188:191], v[130:133]
	v_mfma_f32_16x16x32_bf16 v[110:113], v[152:155], v[196:199], v[110:113]
	v_mfma_f32_16x16x32_bf16 v[106:109], v[160:163], v[196:199], v[106:109]
	v_mfma_f32_16x16x32_bf16 v[94:97], v[152:155], v[204:207], v[94:97]
	v_mfma_f32_16x16x32_bf16 v[90:93], v[160:163], v[204:207], v[90:93]
	v_mfma_f32_16x16x32_bf16 v[78:81], v[152:155], v[220:223], v[78:81]
	v_mfma_f32_16x16x32_bf16 v[74:77], v[160:163], v[220:223], v[74:77]
	v_mfma_f32_16x16x32_bf16 v[122:125], v[168:171], v[184:187], v[122:125]
	v_mfma_f32_16x16x32_bf16 v[114:117], v[176:179], v[184:187], v[114:117]
	v_mfma_f32_16x16x32_bf16 v[102:105], v[168:171], v[192:195], v[102:105]
	v_mfma_f32_16x16x32_bf16 v[98:101], v[176:179], v[192:195], v[98:101]
	v_mfma_f32_16x16x32_bf16 v[86:89], v[168:171], v[200:203], v[86:89]
	v_mfma_f32_16x16x32_bf16 v[82:85], v[176:179], v[200:203], v[82:85]
	v_mfma_f32_16x16x32_bf16 v[70:73], v[168:171], v[216:219], v[70:73]
	v_mfma_f32_16x16x32_bf16 v[66:69], v[176:179], v[216:219], v[66:69]
	v_mfma_f32_16x16x32_bf16 v[122:125], v[172:175], v[188:191], v[122:125]
	v_mfma_f32_16x16x32_bf16 v[114:117], v[180:183], v[188:191], v[114:117]
	v_mfma_f32_16x16x32_bf16 v[102:105], v[172:175], v[196:199], v[102:105]
	v_mfma_f32_16x16x32_bf16 v[98:101], v[180:183], v[196:199], v[98:101]
	v_mfma_f32_16x16x32_bf16 v[86:89], v[172:175], v[204:207], v[86:89]
	v_mfma_f32_16x16x32_bf16 v[82:85], v[180:183], v[204:207], v[82:85]
	v_mfma_f32_16x16x32_bf16 v[70:73], v[172:175], v[220:223], v[70:73]
	v_mfma_f32_16x16x32_bf16 v[66:69], v[180:183], v[220:223], v[66:69]
	s_barrier
	s_add_i32 s46, s50, s77
	v_lshl_add_u64 v[164:165], v[164:165], 0, s[56:57]
	s_mov_b32 m0, s46
	s_nop 0
	global_load_lds_dwordx4 v[164:165], off
	s_add_i32 m0, s46, 0x2000
	s_add_u32 s44, s44, 0x100080
	v_lshl_add_u64 v[164:165], v[208:209], 0, s[56:57]
	s_addc_u32 s45, s45, 0
	s_add_i32 s46, s64, s77
	global_load_lds_dwordx4 v[164:165], off
	s_mov_b32 m0, s46
	s_nop 0
	global_load_lds_dwordx4 v126, s[44:45]
	s_add_i32 m0, s46, 0x2000
	s_nop 0
	global_load_lds_dwordx4 v118, s[44:45]
	s_mov_b32 m0, s80
	v_lshl_add_u64 v[164:165], v[224:225], 0, s[56:57]
	global_load_lds_dwordx4 v[164:165], off
	s_mov_b32 m0, s81
	v_lshl_add_u64 v[164:165], v[242:243], 0, s[56:57]
	global_load_lds_dwordx4 v[164:165], off
	ds_read_b128 v[184:187], v147 offset:49152
	ds_read_b128 v[188:191], v147 offset:50176
	ds_read_b128 v[192:195], v147 offset:51200
	ds_read_b128 v[196:199], v147 offset:52224
	ds_read_b128 v[200:203], v147 offset:53248
	ds_read_b128 v[204:207], v147 offset:54272
	ds_read_b128 v[216:219], v147 offset:55296
	ds_read_b128 v[220:223], v147 offset:56320
	s_waitcnt vmcnt(8) lgkmcnt(0)
	s_barrier
	v_mfma_f32_16x16x32_bf16 v[62:65], v[148:151], v[184:187], v[62:65]
	v_mfma_f32_16x16x32_bf16 v[58:61], v[156:159], v[184:187], v[58:61]
	v_mfma_f32_16x16x32_bf16 v[46:49], v[148:151], v[192:195], v[46:49]
	v_mfma_f32_16x16x32_bf16 v[42:45], v[156:159], v[192:195], v[42:45]
	v_mfma_f32_16x16x32_bf16 v[30:33], v[148:151], v[200:203], v[30:33]
	v_mfma_f32_16x16x32_bf16 v[26:29], v[156:159], v[200:203], v[26:29]
	v_mfma_f32_16x16x32_bf16 v[14:17], v[148:151], v[216:219], v[14:17]
	v_mfma_f32_16x16x32_bf16 v[10:13], v[156:159], v[216:219], v[10:13]
	v_mfma_f32_16x16x32_bf16 v[62:65], v[152:155], v[188:191], v[62:65]
	v_mfma_f32_16x16x32_bf16 v[58:61], v[160:163], v[188:191], v[58:61]
	v_mfma_f32_16x16x32_bf16 v[46:49], v[152:155], v[196:199], v[46:49]
	v_mfma_f32_16x16x32_bf16 v[42:45], v[160:163], v[196:199], v[42:45]
	v_mfma_f32_16x16x32_bf16 v[30:33], v[152:155], v[204:207], v[30:33]
	v_mfma_f32_16x16x32_bf16 v[26:29], v[160:163], v[204:207], v[26:29]
	v_mfma_f32_16x16x32_bf16 v[14:17], v[152:155], v[220:223], v[14:17]
	v_mfma_f32_16x16x32_bf16 v[10:13], v[160:163], v[220:223], v[10:13]
	v_mfma_f32_16x16x32_bf16 v[54:57], v[168:171], v[184:187], v[54:57]
	v_mfma_f32_16x16x32_bf16 v[50:53], v[176:179], v[184:187], v[50:53]
	v_mfma_f32_16x16x32_bf16 v[38:41], v[168:171], v[192:195], v[38:41]
	v_mfma_f32_16x16x32_bf16 v[34:37], v[176:179], v[192:195], v[34:37]
	v_mfma_f32_16x16x32_bf16 v[22:25], v[168:171], v[200:203], v[22:25]
	v_mfma_f32_16x16x32_bf16 v[18:21], v[176:179], v[200:203], v[18:21]
	v_mfma_f32_16x16x32_bf16 v[6:9], v[168:171], v[216:219], v[6:9]
	v_mfma_f32_16x16x32_bf16 v[2:5], v[176:179], v[216:219], v[2:5]
	v_mfma_f32_16x16x32_bf16 v[54:57], v[172:175], v[188:191], v[54:57]
	v_mfma_f32_16x16x32_bf16 v[50:53], v[180:183], v[188:191], v[50:53]
	v_mfma_f32_16x16x32_bf16 v[38:41], v[172:175], v[196:199], v[38:41]
	v_mfma_f32_16x16x32_bf16 v[34:37], v[180:183], v[196:199], v[34:37]
	v_mfma_f32_16x16x32_bf16 v[22:25], v[172:175], v[204:207], v[22:25]
	v_mfma_f32_16x16x32_bf16 v[18:21], v[180:183], v[204:207], v[18:21]
	v_mfma_f32_16x16x32_bf16 v[6:9], v[172:175], v[220:223], v[6:9]
	v_mfma_f32_16x16x32_bf16 v[2:5], v[180:183], v[220:223], v[2:5]
	s_barrier
	s_add_i32 s85, s85, 2
	s_add_u32 s36, s36, 0x100
	s_addc_u32 s37, s37, 0
	s_cmp_gt_u32 s85, 61
	s_cbranch_scc0 .LBB0_2703
	s_add_u32 s36, s59, 0xffffff00
	s_addc_u32 s37, s82, -1
	s_andn2_b64 vcc, exec, s[42:43]
	s_cbranch_vccnz .LBB0_2706
	v_mov_b32_e32 v2, 0
	s_mov_b32 s12, s26
	s_mov_b32 s53, s28
	s_mov_b64 s[24:25], s[34:35]
	s_mov_b32 s68, s58
	v_mov_b32_e32 v3, v2
	v_mov_b32_e32 v4, v2
	v_mov_b32_e32 v5, v2
	v_mov_b32_e32 v6, v2
	v_mov_b32_e32 v7, v2
	v_mov_b32_e32 v8, v2
	v_mov_b32_e32 v9, v2
	v_mov_b32_e32 v18, v2
	v_mov_b32_e32 v19, v2
	v_mov_b32_e32 v20, v2
	v_mov_b32_e32 v21, v2
	v_mov_b32_e32 v22, v2
	v_mov_b32_e32 v23, v2
	v_mov_b32_e32 v24, v2
	v_mov_b32_e32 v25, v2
	v_mov_b32_e32 v34, v2
	v_mov_b32_e32 v35, v2
	v_mov_b32_e32 v36, v2
	v_mov_b32_e32 v37, v2
	v_mov_b32_e32 v38, v2
	v_mov_b32_e32 v39, v2
	v_mov_b32_e32 v40, v2
	v_mov_b32_e32 v41, v2
	v_mov_b32_e32 v50, v2
	v_mov_b32_e32 v51, v2
	v_mov_b32_e32 v52, v2
	v_mov_b32_e32 v53, v2
	v_mov_b32_e32 v54, v2
	v_mov_b32_e32 v55, v2
	v_mov_b32_e32 v56, v2
	v_mov_b32_e32 v57, v2
	v_mov_b32_e32 v10, v2
	v_mov_b32_e32 v11, v2
	v_mov_b32_e32 v12, v2
	v_mov_b32_e32 v13, v2
	v_mov_b32_e32 v14, v2
	v_mov_b32_e32 v15, v2
	v_mov_b32_e32 v16, v2
	v_mov_b32_e32 v17, v2
	v_mov_b32_e32 v26, v2
	v_mov_b32_e32 v27, v2
	v_mov_b32_e32 v28, v2
	v_mov_b32_e32 v29, v2
	v_mov_b32_e32 v30, v2
	v_mov_b32_e32 v31, v2
	v_mov_b32_e32 v32, v2
	v_mov_b32_e32 v33, v2
	v_mov_b32_e32 v42, v2
	v_mov_b32_e32 v43, v2
	v_mov_b32_e32 v44, v2
	v_mov_b32_e32 v45, v2
	v_mov_b32_e32 v46, v2
	v_mov_b32_e32 v47, v2
	v_mov_b32_e32 v48, v2
	v_mov_b32_e32 v49, v2
	v_mov_b32_e32 v58, v2
	v_mov_b32_e32 v59, v2
	v_mov_b32_e32 v60, v2
	v_mov_b32_e32 v61, v2
	v_mov_b32_e32 v62, v2
	v_mov_b32_e32 v63, v2
	v_mov_b32_e32 v64, v2
	v_mov_b32_e32 v65, v2
	v_mov_b32_e32 v66, v2
	v_mov_b32_e32 v67, v2
	v_mov_b32_e32 v68, v2
	v_mov_b32_e32 v69, v2
	v_mov_b32_e32 v70, v2
	v_mov_b32_e32 v71, v2
	v_mov_b32_e32 v72, v2
	v_mov_b32_e32 v73, v2
	v_mov_b32_e32 v82, v2
	v_mov_b32_e32 v83, v2
	v_mov_b32_e32 v84, v2
	v_mov_b32_e32 v85, v2
	v_mov_b32_e32 v86, v2
	v_mov_b32_e32 v87, v2
	v_mov_b32_e32 v88, v2
	v_mov_b32_e32 v89, v2
	v_mov_b32_e32 v98, v2
	v_mov_b32_e32 v99, v2
	v_mov_b32_e32 v100, v2
	v_mov_b32_e32 v101, v2
	v_mov_b32_e32 v102, v2
	v_mov_b32_e32 v103, v2
	v_mov_b32_e32 v104, v2
	v_mov_b32_e32 v105, v2
	v_mov_b32_e32 v114, v2
	v_mov_b32_e32 v115, v2
	v_mov_b32_e32 v116, v2
	v_mov_b32_e32 v117, v2
	v_mov_b32_e32 v122, v2
	v_mov_b32_e32 v123, v2
	v_mov_b32_e32 v124, v2
	v_mov_b32_e32 v125, v2
	v_mov_b32_e32 v74, v2
	v_mov_b32_e32 v75, v2
	v_mov_b32_e32 v76, v2
	v_mov_b32_e32 v77, v2
	v_mov_b32_e32 v78, v2
	v_mov_b32_e32 v79, v2
	v_mov_b32_e32 v80, v2
	v_mov_b32_e32 v81, v2
	v_mov_b32_e32 v90, v2
	v_mov_b32_e32 v91, v2
	v_mov_b32_e32 v92, v2
	v_mov_b32_e32 v93, v2
	v_mov_b32_e32 v94, v2
	v_mov_b32_e32 v95, v2
	v_mov_b32_e32 v96, v2
	v_mov_b32_e32 v97, v2
	v_mov_b32_e32 v106, v2
	v_mov_b32_e32 v107, v2
	v_mov_b32_e32 v108, v2
	v_mov_b32_e32 v109, v2
	v_mov_b32_e32 v110, v2
	v_mov_b32_e32 v111, v2
	v_mov_b32_e32 v112, v2
	v_mov_b32_e32 v113, v2
	v_mov_b32_e32 v130, v2
	v_mov_b32_e32 v131, v2
	v_mov_b32_e32 v132, v2
	v_mov_b32_e32 v133, v2
	v_mov_b32_e32 v134, v2
	v_mov_b32_e32 v135, v2
	v_mov_b32_e32 v136, v2
	v_mov_b32_e32 v137, v2
	s_movk_i32 s92, 0x2b20
	s_andn2_b64 vcc, exec, s[40:41]
	s_cbranch_vccnz .LBB0_2707
	s_branch .LBB0_2708

.LBB0_2796:
	s_add_u32 s44, s24, s36
	s_addc_u32 s45, s25, s37
	s_add_u32 s44, s44, 0x100
	s_addc_u32 s45, s45, 0
	s_add_u32 s50, s59, s36
	s_addc_u32 s64, s81, s37
	s_add_i32 s65, 0, 0x10000
	s_cmpk_eq_i32 s36, 0x1f00
	s_cselect_b32 s47, s29, s45
	s_cselect_b32 s46, s82, s44
	s_cselect_b32 s45, s27, s64
	s_cselect_b32 s44, s83, s50
	s_add_i32 s50, 0, 0x14000
	v_lshl_add_u64 v[164:165], v[144:145], 0, s[36:37]
	s_add_i32 m0, s4, 0xc000
	s_nop 0
	global_load_lds_dwordx4 v[164:165], off
	s_add_i32 m0, s4, 0xe000
	v_lshl_add_u64 v[164:165], v[142:143], 0, s[36:37]
	global_load_lds_dwordx4 v[164:165], off
	ds_read_b128 v[148:151], v241
	ds_read_b128 v[152:155], v241 offset:1024
	ds_read_b128 v[156:159], v241 offset:2048
	ds_read_b128 v[160:163], v241 offset:3072
	ds_read_b128 v[168:171], v241 offset:16384
	ds_read_b128 v[172:175], v241 offset:17408
	ds_read_b128 v[176:179], v241 offset:18432
	ds_read_b128 v[180:183], v241 offset:19456
	ds_read_b128 v[184:187], v147
	ds_read_b128 v[188:191], v147 offset:1024
	ds_read_b128 v[192:195], v147 offset:2048
	ds_read_b128 v[196:199], v147 offset:3072
	ds_read_b128 v[200:203], v147 offset:4096
	ds_read_b128 v[204:207], v147 offset:5120
	ds_read_b128 v[216:219], v147 offset:6144
	ds_read_b128 v[220:223], v147 offset:7168
	s_waitcnt vmcnt(8) lgkmcnt(0)
	s_barrier
	v_mfma_f32_16x16x32_bf16 v[134:137], v[148:151], v[184:187], v[134:137]
	v_mfma_f32_16x16x32_bf16 v[130:133], v[156:159], v[184:187], v[130:133]
	v_mfma_f32_16x16x32_bf16 v[110:113], v[148:151], v[192:195], v[110:113]
	v_mfma_f32_16x16x32_bf16 v[106:109], v[156:159], v[192:195], v[106:109]
	v_mfma_f32_16x16x32_bf16 v[94:97], v[148:151], v[200:203], v[94:97]
	v_mfma_f32_16x16x32_bf16 v[90:93], v[156:159], v[200:203], v[90:93]
	v_mfma_f32_16x16x32_bf16 v[78:81], v[148:151], v[216:219], v[78:81]
	v_mfma_f32_16x16x32_bf16 v[74:77], v[156:159], v[216:219], v[74:77]
	v_mfma_f32_16x16x32_bf16 v[134:137], v[152:155], v[188:191], v[134:137]
	v_mfma_f32_16x16x32_bf16 v[130:133], v[160:163], v[188:191], v[130:133]
	v_mfma_f32_16x16x32_bf16 v[110:113], v[152:155], v[196:199], v[110:113]
	v_mfma_f32_16x16x32_bf16 v[106:109], v[160:163], v[196:199], v[106:109]
	v_mfma_f32_16x16x32_bf16 v[94:97], v[152:155], v[204:207], v[94:97]
	v_mfma_f32_16x16x32_bf16 v[90:93], v[160:163], v[204:207], v[90:93]
	v_mfma_f32_16x16x32_bf16 v[78:81], v[152:155], v[220:223], v[78:81]
	v_mfma_f32_16x16x32_bf16 v[74:77], v[160:163], v[220:223], v[74:77]
	v_mfma_f32_16x16x32_bf16 v[122:125], v[168:171], v[184:187], v[122:125]
	v_mfma_f32_16x16x32_bf16 v[114:117], v[176:179], v[184:187], v[114:117]
	v_mfma_f32_16x16x32_bf16 v[102:105], v[168:171], v[192:195], v[102:105]
	v_mfma_f32_16x16x32_bf16 v[98:101], v[176:179], v[192:195], v[98:101]
	v_mfma_f32_16x16x32_bf16 v[86:89], v[168:171], v[200:203], v[86:89]
	v_mfma_f32_16x16x32_bf16 v[82:85], v[176:179], v[200:203], v[82:85]
	v_mfma_f32_16x16x32_bf16 v[70:73], v[168:171], v[216:219], v[70:73]
	v_mfma_f32_16x16x32_bf16 v[66:69], v[176:179], v[216:219], v[66:69]
	v_mfma_f32_16x16x32_bf16 v[122:125], v[172:175], v[188:191], v[122:125]
	v_mfma_f32_16x16x32_bf16 v[114:117], v[180:183], v[188:191], v[114:117]
	v_mfma_f32_16x16x32_bf16 v[102:105], v[172:175], v[196:199], v[102:105]
	v_mfma_f32_16x16x32_bf16 v[98:101], v[180:183], v[196:199], v[98:101]
	v_mfma_f32_16x16x32_bf16 v[86:89], v[172:175], v[204:207], v[86:89]
	v_mfma_f32_16x16x32_bf16 v[82:85], v[180:183], v[204:207], v[82:85]
	v_mfma_f32_16x16x32_bf16 v[70:73], v[172:175], v[220:223], v[70:73]
	v_mfma_f32_16x16x32_bf16 v[66:69], v[180:183], v[220:223], v[66:69]
	s_barrier
	s_add_i32 s64, s65, s71
	v_lshl_add_u64 v[164:165], s[44:45], 0, v[126:127]
	s_mov_b32 m0, s64
	s_nop 0
	global_load_lds_dwordx4 v126, s[44:45]
	s_add_i32 m0, s64, 0x2000
	s_add_u32 s92, s44, 0x100000
	v_lshl_add_u64 v[208:209], s[44:45], 0, v[118:119]
	s_addc_u32 s93, s45, 0
	s_add_i32 s50, s50, s71
	global_load_lds_dwordx4 v118, s[44:45]
	s_mov_b32 m0, s50
	v_lshl_add_u64 v[242:243], s[46:47], 0, v[120:121]
	global_load_lds_dwordx4 v126, s[92:93]
	s_add_i32 m0, s50, 0x2000
	s_nop 0
	global_load_lds_dwordx4 v118, s[92:93]
	s_mov_b32 m0, s4
	v_lshl_add_u64 v[224:225], s[46:47], 0, v[128:129]
	global_load_lds_dwordx4 v128, s[46:47]
	s_mov_b32 m0, s33
	s_nop 0
	global_load_lds_dwordx4 v120, s[46:47]
	ds_read_b128 v[184:187], v147 offset:16384
	ds_read_b128 v[188:191], v147 offset:17408
	ds_read_b128 v[192:195], v147 offset:18432
	ds_read_b128 v[196:199], v147 offset:19456
	ds_read_b128 v[200:203], v147 offset:20480
	ds_read_b128 v[204:207], v147 offset:21504
	ds_read_b128 v[216:219], v147 offset:22528
	ds_read_b128 v[220:223], v147 offset:23552
	s_waitcnt vmcnt(8) lgkmcnt(0)
	s_barrier
	v_mfma_f32_16x16x32_bf16 v[62:65], v[148:151], v[184:187], v[62:65]
	v_mfma_f32_16x16x32_bf16 v[58:61], v[156:159], v[184:187], v[58:61]
	v_mfma_f32_16x16x32_bf16 v[46:49], v[148:151], v[192:195], v[46:49]
	v_mfma_f32_16x16x32_bf16 v[42:45], v[156:159], v[192:195], v[42:45]
	v_mfma_f32_16x16x32_bf16 v[30:33], v[148:151], v[200:203], v[30:33]
	v_mfma_f32_16x16x32_bf16 v[26:29], v[156:159], v[200:203], v[26:29]
	v_mfma_f32_16x16x32_bf16 v[14:17], v[148:151], v[216:219], v[14:17]
	v_mfma_f32_16x16x32_bf16 v[10:13], v[156:159], v[216:219], v[10:13]
	v_mfma_f32_16x16x32_bf16 v[62:65], v[152:155], v[188:191], v[62:65]
	v_mfma_f32_16x16x32_bf16 v[58:61], v[160:163], v[188:191], v[58:61]
	v_mfma_f32_16x16x32_bf16 v[46:49], v[152:155], v[196:199], v[46:49]
	v_mfma_f32_16x16x32_bf16 v[42:45], v[160:163], v[196:199], v[42:45]
	v_mfma_f32_16x16x32_bf16 v[30:33], v[152:155], v[204:207], v[30:33]
	v_mfma_f32_16x16x32_bf16 v[26:29], v[160:163], v[204:207], v[26:29]
	v_mfma_f32_16x16x32_bf16 v[14:17], v[152:155], v[220:223], v[14:17]
	v_mfma_f32_16x16x32_bf16 v[10:13], v[160:163], v[220:223], v[10:13]
	v_mfma_f32_16x16x32_bf16 v[54:57], v[168:171], v[184:187], v[54:57]
	v_mfma_f32_16x16x32_bf16 v[50:53], v[176:179], v[184:187], v[50:53]
	v_mfma_f32_16x16x32_bf16 v[38:41], v[168:171], v[192:195], v[38:41]
	v_mfma_f32_16x16x32_bf16 v[34:37], v[176:179], v[192:195], v[34:37]
	v_mfma_f32_16x16x32_bf16 v[22:25], v[168:171], v[200:203], v[22:25]
	v_mfma_f32_16x16x32_bf16 v[18:21], v[176:179], v[200:203], v[18:21]
	v_mfma_f32_16x16x32_bf16 v[6:9], v[168:171], v[216:219], v[6:9]
	v_mfma_f32_16x16x32_bf16 v[2:5], v[176:179], v[216:219], v[2:5]
	v_mfma_f32_16x16x32_bf16 v[54:57], v[172:175], v[188:191], v[54:57]
	v_mfma_f32_16x16x32_bf16 v[50:53], v[180:183], v[188:191], v[50:53]
	v_mfma_f32_16x16x32_bf16 v[38:41], v[172:175], v[196:199], v[38:41]
	v_mfma_f32_16x16x32_bf16 v[34:37], v[180:183], v[196:199], v[34:37]
	v_mfma_f32_16x16x32_bf16 v[22:25], v[172:175], v[204:207], v[22:25]
	v_mfma_f32_16x16x32_bf16 v[18:21], v[180:183], v[204:207], v[18:21]
	v_mfma_f32_16x16x32_bf16 v[6:9], v[172:175], v[220:223], v[6:9]
	v_mfma_f32_16x16x32_bf16 v[2:5], v[180:183], v[220:223], v[2:5]
	s_barrier
	s_add_i32 s50, 0, 0x18000
	s_add_i32 s64, 0, 0x1c000
	s_add_u32 s46, s46, 0x100000
	s_addc_u32 s47, s47, 0
	s_mov_b32 m0, s76
	s_nop 0
	global_load_lds_dwordx4 v128, s[46:47]
	s_mov_b32 m0, s77
	v_lshl_add_u64 v[244:245], s[46:47], 0, v[120:121]
	global_load_lds_dwordx4 v120, s[46:47]
	ds_read_b128 v[148:151], v241 offset:32768
	ds_read_b128 v[152:155], v241 offset:33792
	ds_read_b128 v[156:159], v241 offset:34816
	ds_read_b128 v[160:163], v241 offset:35840
	ds_read_b128 v[168:171], v241 offset:49152
	ds_read_b128 v[172:175], v241 offset:50176
	ds_read_b128 v[176:179], v241 offset:51200
	ds_read_b128 v[180:183], v241 offset:52224
	ds_read_b128 v[184:187], v147 offset:32768
	ds_read_b128 v[188:191], v147 offset:33792
	ds_read_b128 v[192:195], v147 offset:34816
	ds_read_b128 v[196:199], v147 offset:35840
	ds_read_b128 v[200:203], v147 offset:36864
	ds_read_b128 v[204:207], v147 offset:37888
	ds_read_b128 v[216:219], v147 offset:38912
	ds_read_b128 v[220:223], v147 offset:39936
	s_waitcnt vmcnt(8) lgkmcnt(0)
	s_barrier
	v_mfma_f32_16x16x32_bf16 v[134:137], v[148:151], v[184:187], v[134:137]
	v_mfma_f32_16x16x32_bf16 v[130:133], v[156:159], v[184:187], v[130:133]
	v_mfma_f32_16x16x32_bf16 v[110:113], v[148:151], v[192:195], v[110:113]
	v_mfma_f32_16x16x32_bf16 v[106:109], v[156:159], v[192:195], v[106:109]
	v_mfma_f32_16x16x32_bf16 v[94:97], v[148:151], v[200:203], v[94:97]
	v_mfma_f32_16x16x32_bf16 v[90:93], v[156:159], v[200:203], v[90:93]
	v_mfma_f32_16x16x32_bf16 v[78:81], v[148:151], v[216:219], v[78:81]
	v_mfma_f32_16x16x32_bf16 v[74:77], v[156:159], v[216:219], v[74:77]
	v_mfma_f32_16x16x32_bf16 v[134:137], v[152:155], v[188:191], v[134:137]
	v_mfma_f32_16x16x32_bf16 v[130:133], v[160:163], v[188:191], v[130:133]
	v_mfma_f32_16x16x32_bf16 v[110:113], v[152:155], v[196:199], v[110:113]
	v_mfma_f32_16x16x32_bf16 v[106:109], v[160:163], v[196:199], v[106:109]
	v_mfma_f32_16x16x32_bf16 v[94:97], v[152:155], v[204:207], v[94:97]
	v_mfma_f32_16x16x32_bf16 v[90:93], v[160:163], v[204:207], v[90:93]
	v_mfma_f32_16x16x32_bf16 v[78:81], v[152:155], v[220:223], v[78:81]
	v_mfma_f32_16x16x32_bf16 v[74:77], v[160:163], v[220:223], v[74:77]
	v_mfma_f32_16x16x32_bf16 v[122:125], v[168:171], v[184:187], v[122:125]
	v_mfma_f32_16x16x32_bf16 v[114:117], v[176:179], v[184:187], v[114:117]
	v_mfma_f32_16x16x32_bf16 v[102:105], v[168:171], v[192:195], v[102:105]
	v_mfma_f32_16x16x32_bf16 v[98:101], v[176:179], v[192:195], v[98:101]
	v_mfma_f32_16x16x32_bf16 v[86:89], v[168:171], v[200:203], v[86:89]
	v_mfma_f32_16x16x32_bf16 v[82:85], v[176:179], v[200:203], v[82:85]
	v_mfma_f32_16x16x32_bf16 v[70:73], v[168:171], v[216:219], v[70:73]
	v_mfma_f32_16x16x32_bf16 v[66:69], v[176:179], v[216:219], v[66:69]
	v_mfma_f32_16x16x32_bf16 v[122:125], v[172:175], v[188:191], v[122:125]
	v_mfma_f32_16x16x32_bf16 v[114:117], v[180:183], v[188:191], v[114:117]
	v_mfma_f32_16x16x32_bf16 v[102:105], v[172:175], v[196:199], v[102:105]
	v_mfma_f32_16x16x32_bf16 v[98:101], v[180:183], v[196:199], v[98:101]
	v_mfma_f32_16x16x32_bf16 v[86:89], v[172:175], v[204:207], v[86:89]
	v_mfma_f32_16x16x32_bf16 v[82:85], v[180:183], v[204:207], v[82:85]
	v_mfma_f32_16x16x32_bf16 v[70:73], v[172:175], v[220:223], v[70:73]
	v_mfma_f32_16x16x32_bf16 v[66:69], v[180:183], v[220:223], v[66:69]
	s_barrier
	s_add_i32 s46, s50, s71
	v_lshl_add_u64 v[164:165], v[164:165], 0, s[56:57]
	s_mov_b32 m0, s46
	s_nop 0
	global_load_lds_dwordx4 v[164:165], off
	s_add_i32 m0, s46, 0x2000
	s_add_u32 s44, s44, 0x100080
	v_lshl_add_u64 v[164:165], v[208:209], 0, s[56:57]
	s_addc_u32 s45, s45, 0
	s_add_i32 s46, s64, s71
	global_load_lds_dwordx4 v[164:165], off
	s_mov_b32 m0, s46
	s_nop 0
	global_load_lds_dwordx4 v126, s[44:45]
	s_add_i32 m0, s46, 0x2000
	s_nop 0
	global_load_lds_dwordx4 v118, s[44:45]
	s_mov_b32 m0, s78
	v_lshl_add_u64 v[164:165], v[224:225], 0, s[56:57]
	global_load_lds_dwordx4 v[164:165], off
	s_mov_b32 m0, s79
	v_lshl_add_u64 v[164:165], v[242:243], 0, s[56:57]
	global_load_lds_dwordx4 v[164:165], off
	ds_read_b128 v[184:187], v147 offset:49152
	ds_read_b128 v[188:191], v147 offset:50176
	ds_read_b128 v[192:195], v147 offset:51200
	ds_read_b128 v[196:199], v147 offset:52224
	ds_read_b128 v[200:203], v147 offset:53248
	ds_read_b128 v[204:207], v147 offset:54272
	ds_read_b128 v[216:219], v147 offset:55296
	ds_read_b128 v[220:223], v147 offset:56320
	s_waitcnt vmcnt(8) lgkmcnt(0)
	s_barrier
	v_mfma_f32_16x16x32_bf16 v[62:65], v[148:151], v[184:187], v[62:65]
	v_mfma_f32_16x16x32_bf16 v[58:61], v[156:159], v[184:187], v[58:61]
	v_mfma_f32_16x16x32_bf16 v[46:49], v[148:151], v[192:195], v[46:49]
	v_mfma_f32_16x16x32_bf16 v[42:45], v[156:159], v[192:195], v[42:45]
	v_mfma_f32_16x16x32_bf16 v[30:33], v[148:151], v[200:203], v[30:33]
	v_mfma_f32_16x16x32_bf16 v[26:29], v[156:159], v[200:203], v[26:29]
	v_mfma_f32_16x16x32_bf16 v[14:17], v[148:151], v[216:219], v[14:17]
	v_mfma_f32_16x16x32_bf16 v[10:13], v[156:159], v[216:219], v[10:13]
	v_mfma_f32_16x16x32_bf16 v[62:65], v[152:155], v[188:191], v[62:65]
	v_mfma_f32_16x16x32_bf16 v[58:61], v[160:163], v[188:191], v[58:61]
	v_mfma_f32_16x16x32_bf16 v[46:49], v[152:155], v[196:199], v[46:49]
	v_mfma_f32_16x16x32_bf16 v[42:45], v[160:163], v[196:199], v[42:45]
	v_mfma_f32_16x16x32_bf16 v[30:33], v[152:155], v[204:207], v[30:33]
	v_mfma_f32_16x16x32_bf16 v[26:29], v[160:163], v[204:207], v[26:29]
	v_mfma_f32_16x16x32_bf16 v[14:17], v[152:155], v[220:223], v[14:17]
	v_mfma_f32_16x16x32_bf16 v[10:13], v[160:163], v[220:223], v[10:13]
	v_mfma_f32_16x16x32_bf16 v[54:57], v[168:171], v[184:187], v[54:57]
	v_mfma_f32_16x16x32_bf16 v[50:53], v[176:179], v[184:187], v[50:53]
	v_mfma_f32_16x16x32_bf16 v[38:41], v[168:171], v[192:195], v[38:41]
	v_mfma_f32_16x16x32_bf16 v[34:37], v[176:179], v[192:195], v[34:37]
	v_mfma_f32_16x16x32_bf16 v[22:25], v[168:171], v[200:203], v[22:25]
	v_mfma_f32_16x16x32_bf16 v[18:21], v[176:179], v[200:203], v[18:21]
	v_mfma_f32_16x16x32_bf16 v[6:9], v[168:171], v[216:219], v[6:9]
	v_mfma_f32_16x16x32_bf16 v[2:5], v[176:179], v[216:219], v[2:5]
	v_mfma_f32_16x16x32_bf16 v[54:57], v[172:175], v[188:191], v[54:57]
	v_mfma_f32_16x16x32_bf16 v[50:53], v[180:183], v[188:191], v[50:53]
	v_mfma_f32_16x16x32_bf16 v[38:41], v[172:175], v[196:199], v[38:41]
	v_mfma_f32_16x16x32_bf16 v[34:37], v[180:183], v[196:199], v[34:37]
	v_mfma_f32_16x16x32_bf16 v[22:25], v[172:175], v[204:207], v[22:25]
	v_mfma_f32_16x16x32_bf16 v[18:21], v[180:183], v[204:207], v[18:21]
	v_mfma_f32_16x16x32_bf16 v[6:9], v[172:175], v[220:223], v[6:9]
	v_mfma_f32_16x16x32_bf16 v[2:5], v[180:183], v[220:223], v[2:5]
	s_barrier
	s_add_i32 s84, s84, 2
	s_add_u32 s36, s36, 0x100
	s_addc_u32 s37, s37, 0
	s_cmp_gt_u32 s84, 61
	s_cbranch_scc0 .LBB0_2796
	s_add_u32 s36, s59, 0xffffff00
	s_addc_u32 s37, s81, -1
	s_andn2_b64 vcc, exec, s[42:43]
	s_cbranch_vccnz .LBB0_2799
	v_mov_b32_e32 v2, 0
	s_mov_b32 s12, s26
	s_mov_b32 s80, s28
	s_mov_b64 s[24:25], s[34:35]
	s_mov_b32 s68, s58
	v_mov_b32_e32 v3, v2
	v_mov_b32_e32 v4, v2
	v_mov_b32_e32 v5, v2
	v_mov_b32_e32 v6, v2
	v_mov_b32_e32 v7, v2
	v_mov_b32_e32 v8, v2
	v_mov_b32_e32 v9, v2
	v_mov_b32_e32 v18, v2
	v_mov_b32_e32 v19, v2
	v_mov_b32_e32 v20, v2
	v_mov_b32_e32 v21, v2
	v_mov_b32_e32 v22, v2
	v_mov_b32_e32 v23, v2
	v_mov_b32_e32 v24, v2
	v_mov_b32_e32 v25, v2
	v_mov_b32_e32 v34, v2
	v_mov_b32_e32 v35, v2
	v_mov_b32_e32 v36, v2
	v_mov_b32_e32 v37, v2
	v_mov_b32_e32 v38, v2
	v_mov_b32_e32 v39, v2
	v_mov_b32_e32 v40, v2
	v_mov_b32_e32 v41, v2
	v_mov_b32_e32 v50, v2
	v_mov_b32_e32 v51, v2
	v_mov_b32_e32 v52, v2
	v_mov_b32_e32 v53, v2
	v_mov_b32_e32 v54, v2
	v_mov_b32_e32 v55, v2
	v_mov_b32_e32 v56, v2
	v_mov_b32_e32 v57, v2
	v_mov_b32_e32 v10, v2
	v_mov_b32_e32 v11, v2
	v_mov_b32_e32 v12, v2
	v_mov_b32_e32 v13, v2
	v_mov_b32_e32 v14, v2
	v_mov_b32_e32 v15, v2
	v_mov_b32_e32 v16, v2
	v_mov_b32_e32 v17, v2
	v_mov_b32_e32 v26, v2
	v_mov_b32_e32 v27, v2
	v_mov_b32_e32 v28, v2
	v_mov_b32_e32 v29, v2
	v_mov_b32_e32 v30, v2
	v_mov_b32_e32 v31, v2
	v_mov_b32_e32 v32, v2
	v_mov_b32_e32 v33, v2
	v_mov_b32_e32 v42, v2
	v_mov_b32_e32 v43, v2
	v_mov_b32_e32 v44, v2
	v_mov_b32_e32 v45, v2
	v_mov_b32_e32 v46, v2
	v_mov_b32_e32 v47, v2
	v_mov_b32_e32 v48, v2
	v_mov_b32_e32 v49, v2
	v_mov_b32_e32 v58, v2
	v_mov_b32_e32 v59, v2
	v_mov_b32_e32 v60, v2
	v_mov_b32_e32 v61, v2
	v_mov_b32_e32 v62, v2
	v_mov_b32_e32 v63, v2
	v_mov_b32_e32 v64, v2
	v_mov_b32_e32 v65, v2
	v_mov_b32_e32 v66, v2
	v_mov_b32_e32 v67, v2
	v_mov_b32_e32 v68, v2
	v_mov_b32_e32 v69, v2
	v_mov_b32_e32 v70, v2
	v_mov_b32_e32 v71, v2
	v_mov_b32_e32 v72, v2
	v_mov_b32_e32 v73, v2
	v_mov_b32_e32 v82, v2
	v_mov_b32_e32 v83, v2
	v_mov_b32_e32 v84, v2
	v_mov_b32_e32 v85, v2
	v_mov_b32_e32 v86, v2
	v_mov_b32_e32 v87, v2
	v_mov_b32_e32 v88, v2
	v_mov_b32_e32 v89, v2
	v_mov_b32_e32 v98, v2
	v_mov_b32_e32 v99, v2
	v_mov_b32_e32 v100, v2
	v_mov_b32_e32 v101, v2
	v_mov_b32_e32 v102, v2
	v_mov_b32_e32 v103, v2
	v_mov_b32_e32 v104, v2
	v_mov_b32_e32 v105, v2
	v_mov_b32_e32 v114, v2
	v_mov_b32_e32 v115, v2
	v_mov_b32_e32 v116, v2
	v_mov_b32_e32 v117, v2
	v_mov_b32_e32 v122, v2
	v_mov_b32_e32 v123, v2
	v_mov_b32_e32 v124, v2
	v_mov_b32_e32 v125, v2
	v_mov_b32_e32 v74, v2
	v_mov_b32_e32 v75, v2
	v_mov_b32_e32 v76, v2
	v_mov_b32_e32 v77, v2
	v_mov_b32_e32 v78, v2
	v_mov_b32_e32 v79, v2
	v_mov_b32_e32 v80, v2
	v_mov_b32_e32 v81, v2
	v_mov_b32_e32 v90, v2
	v_mov_b32_e32 v91, v2
	v_mov_b32_e32 v92, v2
	v_mov_b32_e32 v93, v2
	v_mov_b32_e32 v94, v2
	v_mov_b32_e32 v95, v2
	v_mov_b32_e32 v96, v2
	v_mov_b32_e32 v97, v2
	v_mov_b32_e32 v106, v2
	v_mov_b32_e32 v107, v2
	v_mov_b32_e32 v108, v2
	v_mov_b32_e32 v109, v2
	v_mov_b32_e32 v110, v2
	v_mov_b32_e32 v111, v2
	v_mov_b32_e32 v112, v2
	v_mov_b32_e32 v113, v2
	v_mov_b32_e32 v130, v2
	v_mov_b32_e32 v131, v2
	v_mov_b32_e32 v132, v2
	v_mov_b32_e32 v133, v2
	v_mov_b32_e32 v134, v2
	v_mov_b32_e32 v135, v2
	v_mov_b32_e32 v136, v2
	v_mov_b32_e32 v137, v2
	s_movk_i32 s92, 0x2b20
	s_andn2_b64 vcc, exec, s[40:41]
	s_cbranch_vccnz .LBB0_2800
	s_branch .LBB0_2801

.LBB0_2891:
	s_add_u32 s44, s24, s36
	s_addc_u32 s45, s25, s37
	s_add_u32 s44, s44, 0x100
	s_addc_u32 s45, s45, 0
	s_add_u32 s50, s59, s36
	s_addc_u32 s64, s81, s37
	s_add_i32 s65, 0, 0x10000
	s_cmpk_eq_i32 s36, 0x1f00
	s_cselect_b32 s47, s29, s45
	s_cselect_b32 s46, s82, s44
	s_cselect_b32 s45, s27, s64
	s_cselect_b32 s44, s83, s50
	s_add_i32 s50, 0, 0x14000
	v_lshl_add_u64 v[164:165], v[144:145], 0, s[36:37]
	s_add_i32 m0, s4, 0xc000
	s_nop 0
	global_load_lds_dwordx4 v[164:165], off
	s_add_i32 m0, s4, 0xe000
	v_lshl_add_u64 v[164:165], v[142:143], 0, s[36:37]
	global_load_lds_dwordx4 v[164:165], off
	ds_read_b128 v[148:151], v225
	ds_read_b128 v[152:155], v225 offset:1024
	ds_read_b128 v[156:159], v225 offset:2048
	ds_read_b128 v[160:163], v225 offset:3072
	ds_read_b128 v[168:171], v225 offset:16384
	ds_read_b128 v[172:175], v225 offset:17408
	ds_read_b128 v[176:179], v225 offset:18432
	ds_read_b128 v[180:183], v225 offset:19456
	ds_read_b128 v[184:187], v147
	ds_read_b128 v[188:191], v147 offset:1024
	ds_read_b128 v[192:195], v147 offset:2048
	ds_read_b128 v[196:199], v147 offset:3072
	ds_read_b128 v[200:203], v147 offset:4096
	ds_read_b128 v[204:207], v147 offset:5120
	ds_read_b128 v[216:219], v147 offset:6144
	ds_read_b128 v[220:223], v147 offset:7168
	s_waitcnt vmcnt(8) lgkmcnt(0)
	s_barrier
	v_mfma_f32_16x16x32_bf16 v[134:137], v[148:151], v[184:187], v[134:137]
	v_mfma_f32_16x16x32_bf16 v[130:133], v[156:159], v[184:187], v[130:133]
	v_mfma_f32_16x16x32_bf16 v[110:113], v[148:151], v[192:195], v[110:113]
	v_mfma_f32_16x16x32_bf16 v[106:109], v[156:159], v[192:195], v[106:109]
	v_mfma_f32_16x16x32_bf16 v[94:97], v[148:151], v[200:203], v[94:97]
	v_mfma_f32_16x16x32_bf16 v[90:93], v[156:159], v[200:203], v[90:93]
	v_mfma_f32_16x16x32_bf16 v[78:81], v[148:151], v[216:219], v[78:81]
	v_mfma_f32_16x16x32_bf16 v[74:77], v[156:159], v[216:219], v[74:77]
	v_mfma_f32_16x16x32_bf16 v[134:137], v[152:155], v[188:191], v[134:137]
	v_mfma_f32_16x16x32_bf16 v[130:133], v[160:163], v[188:191], v[130:133]
	v_mfma_f32_16x16x32_bf16 v[110:113], v[152:155], v[196:199], v[110:113]
	v_mfma_f32_16x16x32_bf16 v[106:109], v[160:163], v[196:199], v[106:109]
	v_mfma_f32_16x16x32_bf16 v[94:97], v[152:155], v[204:207], v[94:97]
	v_mfma_f32_16x16x32_bf16 v[90:93], v[160:163], v[204:207], v[90:93]
	v_mfma_f32_16x16x32_bf16 v[78:81], v[152:155], v[220:223], v[78:81]
	v_mfma_f32_16x16x32_bf16 v[74:77], v[160:163], v[220:223], v[74:77]
	v_mfma_f32_16x16x32_bf16 v[118:121], v[168:171], v[184:187], v[118:121]
	v_mfma_f32_16x16x32_bf16 v[114:117], v[176:179], v[184:187], v[114:117]
	v_mfma_f32_16x16x32_bf16 v[102:105], v[168:171], v[192:195], v[102:105]
	v_mfma_f32_16x16x32_bf16 v[98:101], v[176:179], v[192:195], v[98:101]
	v_mfma_f32_16x16x32_bf16 v[86:89], v[168:171], v[200:203], v[86:89]
	v_mfma_f32_16x16x32_bf16 v[82:85], v[176:179], v[200:203], v[82:85]
	v_mfma_f32_16x16x32_bf16 v[70:73], v[168:171], v[216:219], v[70:73]
	v_mfma_f32_16x16x32_bf16 v[66:69], v[176:179], v[216:219], v[66:69]
	v_mfma_f32_16x16x32_bf16 v[118:121], v[172:175], v[188:191], v[118:121]
	v_mfma_f32_16x16x32_bf16 v[114:117], v[180:183], v[188:191], v[114:117]
	v_mfma_f32_16x16x32_bf16 v[102:105], v[172:175], v[196:199], v[102:105]
	v_mfma_f32_16x16x32_bf16 v[98:101], v[180:183], v[196:199], v[98:101]
	v_mfma_f32_16x16x32_bf16 v[86:89], v[172:175], v[204:207], v[86:89]
	v_mfma_f32_16x16x32_bf16 v[82:85], v[180:183], v[204:207], v[82:85]
	v_mfma_f32_16x16x32_bf16 v[70:73], v[172:175], v[220:223], v[70:73]
	v_mfma_f32_16x16x32_bf16 v[66:69], v[180:183], v[220:223], v[66:69]
	s_barrier
	s_add_i32 s64, s65, s76
	v_lshl_add_u64 v[164:165], s[44:45], 0, v[126:127]
	s_mov_b32 m0, s64
	s_nop 0
	global_load_lds_dwordx4 v126, s[44:45]
	s_add_i32 m0, s64, 0x2000
	s_add_u32 s92, s44, 0x100000
	v_lshl_add_u64 v[208:209], s[44:45], 0, v[122:123]
	s_addc_u32 s93, s45, 0
	s_add_i32 s50, s50, s76
	global_load_lds_dwordx4 v122, s[44:45]
	s_mov_b32 m0, s50
	v_lshl_add_u64 v[242:243], s[46:47], 0, v[124:125]
	global_load_lds_dwordx4 v126, s[92:93]
	s_add_i32 m0, s50, 0x2000
	s_nop 0
	global_load_lds_dwordx4 v122, s[92:93]
	s_mov_b32 m0, s4
	v_lshl_add_u64 v[240:241], s[46:47], 0, v[128:129]
	global_load_lds_dwordx4 v128, s[46:47]
	s_mov_b32 m0, s33
	s_nop 0
	global_load_lds_dwordx4 v124, s[46:47]
	ds_read_b128 v[184:187], v147 offset:16384
	ds_read_b128 v[188:191], v147 offset:17408
	ds_read_b128 v[192:195], v147 offset:18432
	ds_read_b128 v[196:199], v147 offset:19456
	ds_read_b128 v[200:203], v147 offset:20480
	ds_read_b128 v[204:207], v147 offset:21504
	ds_read_b128 v[216:219], v147 offset:22528
	ds_read_b128 v[220:223], v147 offset:23552
	s_waitcnt vmcnt(8) lgkmcnt(0)
	s_barrier
	v_mfma_f32_16x16x32_bf16 v[62:65], v[148:151], v[184:187], v[62:65]
	v_mfma_f32_16x16x32_bf16 v[58:61], v[156:159], v[184:187], v[58:61]
	v_mfma_f32_16x16x32_bf16 v[46:49], v[148:151], v[192:195], v[46:49]
	v_mfma_f32_16x16x32_bf16 v[42:45], v[156:159], v[192:195], v[42:45]
	v_mfma_f32_16x16x32_bf16 v[30:33], v[148:151], v[200:203], v[30:33]
	v_mfma_f32_16x16x32_bf16 v[26:29], v[156:159], v[200:203], v[26:29]
	v_mfma_f32_16x16x32_bf16 v[14:17], v[148:151], v[216:219], v[14:17]
	v_mfma_f32_16x16x32_bf16 v[10:13], v[156:159], v[216:219], v[10:13]
	v_mfma_f32_16x16x32_bf16 v[62:65], v[152:155], v[188:191], v[62:65]
	v_mfma_f32_16x16x32_bf16 v[58:61], v[160:163], v[188:191], v[58:61]
	v_mfma_f32_16x16x32_bf16 v[46:49], v[152:155], v[196:199], v[46:49]
	v_mfma_f32_16x16x32_bf16 v[42:45], v[160:163], v[196:199], v[42:45]
	v_mfma_f32_16x16x32_bf16 v[30:33], v[152:155], v[204:207], v[30:33]
	v_mfma_f32_16x16x32_bf16 v[26:29], v[160:163], v[204:207], v[26:29]
	v_mfma_f32_16x16x32_bf16 v[14:17], v[152:155], v[220:223], v[14:17]
	v_mfma_f32_16x16x32_bf16 v[10:13], v[160:163], v[220:223], v[10:13]
	v_mfma_f32_16x16x32_bf16 v[54:57], v[168:171], v[184:187], v[54:57]
	v_mfma_f32_16x16x32_bf16 v[50:53], v[176:179], v[184:187], v[50:53]
	v_mfma_f32_16x16x32_bf16 v[38:41], v[168:171], v[192:195], v[38:41]
	v_mfma_f32_16x16x32_bf16 v[34:37], v[176:179], v[192:195], v[34:37]
	v_mfma_f32_16x16x32_bf16 v[22:25], v[168:171], v[200:203], v[22:25]
	v_mfma_f32_16x16x32_bf16 v[18:21], v[176:179], v[200:203], v[18:21]
	v_mfma_f32_16x16x32_bf16 v[6:9], v[168:171], v[216:219], v[6:9]
	v_mfma_f32_16x16x32_bf16 v[2:5], v[176:179], v[216:219], v[2:5]
	v_mfma_f32_16x16x32_bf16 v[54:57], v[172:175], v[188:191], v[54:57]
	v_mfma_f32_16x16x32_bf16 v[50:53], v[180:183], v[188:191], v[50:53]
	v_mfma_f32_16x16x32_bf16 v[38:41], v[172:175], v[196:199], v[38:41]
	v_mfma_f32_16x16x32_bf16 v[34:37], v[180:183], v[196:199], v[34:37]
	v_mfma_f32_16x16x32_bf16 v[22:25], v[172:175], v[204:207], v[22:25]
	v_mfma_f32_16x16x32_bf16 v[18:21], v[180:183], v[204:207], v[18:21]
	v_mfma_f32_16x16x32_bf16 v[6:9], v[172:175], v[220:223], v[6:9]
	v_mfma_f32_16x16x32_bf16 v[2:5], v[180:183], v[220:223], v[2:5]
	s_barrier
	s_add_i32 s50, 0, 0x18000
	s_add_i32 s64, 0, 0x1c000
	s_add_u32 s46, s46, 0x100000
	s_addc_u32 s47, s47, 0
	s_mov_b32 m0, s77
	s_nop 0
	global_load_lds_dwordx4 v128, s[46:47]
	s_mov_b32 m0, s78
	v_lshl_add_u64 v[244:245], s[46:47], 0, v[124:125]
	global_load_lds_dwordx4 v124, s[46:47]
	ds_read_b128 v[148:151], v225 offset:32768
	ds_read_b128 v[152:155], v225 offset:33792
	ds_read_b128 v[156:159], v225 offset:34816
	ds_read_b128 v[160:163], v225 offset:35840
	ds_read_b128 v[168:171], v225 offset:49152
	ds_read_b128 v[172:175], v225 offset:50176
	ds_read_b128 v[176:179], v225 offset:51200
	ds_read_b128 v[180:183], v225 offset:52224
	ds_read_b128 v[184:187], v147 offset:32768
	ds_read_b128 v[188:191], v147 offset:33792
	ds_read_b128 v[192:195], v147 offset:34816
	ds_read_b128 v[196:199], v147 offset:35840
	ds_read_b128 v[200:203], v147 offset:36864
	ds_read_b128 v[204:207], v147 offset:37888
	ds_read_b128 v[216:219], v147 offset:38912
	ds_read_b128 v[220:223], v147 offset:39936
	s_waitcnt vmcnt(8) lgkmcnt(0)
	s_barrier
	v_mfma_f32_16x16x32_bf16 v[134:137], v[148:151], v[184:187], v[134:137]
	v_mfma_f32_16x16x32_bf16 v[130:133], v[156:159], v[184:187], v[130:133]
	v_mfma_f32_16x16x32_bf16 v[110:113], v[148:151], v[192:195], v[110:113]
	v_mfma_f32_16x16x32_bf16 v[106:109], v[156:159], v[192:195], v[106:109]
	v_mfma_f32_16x16x32_bf16 v[94:97], v[148:151], v[200:203], v[94:97]
	v_mfma_f32_16x16x32_bf16 v[90:93], v[156:159], v[200:203], v[90:93]
	v_mfma_f32_16x16x32_bf16 v[78:81], v[148:151], v[216:219], v[78:81]
	v_mfma_f32_16x16x32_bf16 v[74:77], v[156:159], v[216:219], v[74:77]
	v_mfma_f32_16x16x32_bf16 v[134:137], v[152:155], v[188:191], v[134:137]
	v_mfma_f32_16x16x32_bf16 v[130:133], v[160:163], v[188:191], v[130:133]
	v_mfma_f32_16x16x32_bf16 v[110:113], v[152:155], v[196:199], v[110:113]
	v_mfma_f32_16x16x32_bf16 v[106:109], v[160:163], v[196:199], v[106:109]
	v_mfma_f32_16x16x32_bf16 v[94:97], v[152:155], v[204:207], v[94:97]
	v_mfma_f32_16x16x32_bf16 v[90:93], v[160:163], v[204:207], v[90:93]
	v_mfma_f32_16x16x32_bf16 v[78:81], v[152:155], v[220:223], v[78:81]
	v_mfma_f32_16x16x32_bf16 v[74:77], v[160:163], v[220:223], v[74:77]
	v_mfma_f32_16x16x32_bf16 v[118:121], v[168:171], v[184:187], v[118:121]
	v_mfma_f32_16x16x32_bf16 v[114:117], v[176:179], v[184:187], v[114:117]
	v_mfma_f32_16x16x32_bf16 v[102:105], v[168:171], v[192:195], v[102:105]
	v_mfma_f32_16x16x32_bf16 v[98:101], v[176:179], v[192:195], v[98:101]
	v_mfma_f32_16x16x32_bf16 v[86:89], v[168:171], v[200:203], v[86:89]
	v_mfma_f32_16x16x32_bf16 v[82:85], v[176:179], v[200:203], v[82:85]
	v_mfma_f32_16x16x32_bf16 v[70:73], v[168:171], v[216:219], v[70:73]
	v_mfma_f32_16x16x32_bf16 v[66:69], v[176:179], v[216:219], v[66:69]
	v_mfma_f32_16x16x32_bf16 v[118:121], v[172:175], v[188:191], v[118:121]
	v_mfma_f32_16x16x32_bf16 v[114:117], v[180:183], v[188:191], v[114:117]
	v_mfma_f32_16x16x32_bf16 v[102:105], v[172:175], v[196:199], v[102:105]
	v_mfma_f32_16x16x32_bf16 v[98:101], v[180:183], v[196:199], v[98:101]
	v_mfma_f32_16x16x32_bf16 v[86:89], v[172:175], v[204:207], v[86:89]
	v_mfma_f32_16x16x32_bf16 v[82:85], v[180:183], v[204:207], v[82:85]
	v_mfma_f32_16x16x32_bf16 v[70:73], v[172:175], v[220:223], v[70:73]
	v_mfma_f32_16x16x32_bf16 v[66:69], v[180:183], v[220:223], v[66:69]
	s_barrier
	s_add_i32 s46, s50, s76
	v_lshl_add_u64 v[164:165], v[164:165], 0, s[56:57]
	s_mov_b32 m0, s46
	s_nop 0
	global_load_lds_dwordx4 v[164:165], off
	s_add_i32 m0, s46, 0x2000
	s_add_u32 s44, s44, 0x100080
	v_lshl_add_u64 v[164:165], v[208:209], 0, s[56:57]
	s_addc_u32 s45, s45, 0
	s_add_i32 s46, s64, s76
	global_load_lds_dwordx4 v[164:165], off
	s_mov_b32 m0, s46
	s_nop 0
	global_load_lds_dwordx4 v126, s[44:45]
	s_add_i32 m0, s46, 0x2000
	s_nop 0
	global_load_lds_dwordx4 v122, s[44:45]
	s_mov_b32 m0, s79
	v_lshl_add_u64 v[164:165], v[240:241], 0, s[56:57]
	global_load_lds_dwordx4 v[164:165], off
	s_mov_b32 m0, s80
	v_lshl_add_u64 v[164:165], v[242:243], 0, s[56:57]
	global_load_lds_dwordx4 v[164:165], off
	ds_read_b128 v[184:187], v147 offset:49152
	ds_read_b128 v[188:191], v147 offset:50176
	ds_read_b128 v[192:195], v147 offset:51200
	ds_read_b128 v[196:199], v147 offset:52224
	ds_read_b128 v[200:203], v147 offset:53248
	ds_read_b128 v[204:207], v147 offset:54272
	ds_read_b128 v[216:219], v147 offset:55296
	ds_read_b128 v[220:223], v147 offset:56320
	s_waitcnt vmcnt(8) lgkmcnt(0)
	s_barrier
	v_mfma_f32_16x16x32_bf16 v[62:65], v[148:151], v[184:187], v[62:65]
	v_mfma_f32_16x16x32_bf16 v[58:61], v[156:159], v[184:187], v[58:61]
	v_mfma_f32_16x16x32_bf16 v[46:49], v[148:151], v[192:195], v[46:49]
	v_mfma_f32_16x16x32_bf16 v[42:45], v[156:159], v[192:195], v[42:45]
	v_mfma_f32_16x16x32_bf16 v[30:33], v[148:151], v[200:203], v[30:33]
	v_mfma_f32_16x16x32_bf16 v[26:29], v[156:159], v[200:203], v[26:29]
	v_mfma_f32_16x16x32_bf16 v[14:17], v[148:151], v[216:219], v[14:17]
	v_mfma_f32_16x16x32_bf16 v[10:13], v[156:159], v[216:219], v[10:13]
	v_mfma_f32_16x16x32_bf16 v[62:65], v[152:155], v[188:191], v[62:65]
	v_mfma_f32_16x16x32_bf16 v[58:61], v[160:163], v[188:191], v[58:61]
	v_mfma_f32_16x16x32_bf16 v[46:49], v[152:155], v[196:199], v[46:49]
	v_mfma_f32_16x16x32_bf16 v[42:45], v[160:163], v[196:199], v[42:45]
	v_mfma_f32_16x16x32_bf16 v[30:33], v[152:155], v[204:207], v[30:33]
	v_mfma_f32_16x16x32_bf16 v[26:29], v[160:163], v[204:207], v[26:29]
	v_mfma_f32_16x16x32_bf16 v[14:17], v[152:155], v[220:223], v[14:17]
	v_mfma_f32_16x16x32_bf16 v[10:13], v[160:163], v[220:223], v[10:13]
	v_mfma_f32_16x16x32_bf16 v[54:57], v[168:171], v[184:187], v[54:57]
	v_mfma_f32_16x16x32_bf16 v[50:53], v[176:179], v[184:187], v[50:53]
	v_mfma_f32_16x16x32_bf16 v[38:41], v[168:171], v[192:195], v[38:41]
	v_mfma_f32_16x16x32_bf16 v[34:37], v[176:179], v[192:195], v[34:37]
	v_mfma_f32_16x16x32_bf16 v[22:25], v[168:171], v[200:203], v[22:25]
	v_mfma_f32_16x16x32_bf16 v[18:21], v[176:179], v[200:203], v[18:21]
	v_mfma_f32_16x16x32_bf16 v[6:9], v[168:171], v[216:219], v[6:9]
	v_mfma_f32_16x16x32_bf16 v[2:5], v[176:179], v[216:219], v[2:5]
	v_mfma_f32_16x16x32_bf16 v[54:57], v[172:175], v[188:191], v[54:57]
	v_mfma_f32_16x16x32_bf16 v[50:53], v[180:183], v[188:191], v[50:53]
	v_mfma_f32_16x16x32_bf16 v[38:41], v[172:175], v[196:199], v[38:41]
	v_mfma_f32_16x16x32_bf16 v[34:37], v[180:183], v[196:199], v[34:37]
	v_mfma_f32_16x16x32_bf16 v[22:25], v[172:175], v[204:207], v[22:25]
	v_mfma_f32_16x16x32_bf16 v[18:21], v[180:183], v[204:207], v[18:21]
	v_mfma_f32_16x16x32_bf16 v[6:9], v[172:175], v[220:223], v[6:9]
	v_mfma_f32_16x16x32_bf16 v[2:5], v[180:183], v[220:223], v[2:5]
	s_barrier
	s_add_i32 s84, s84, 2
	s_add_u32 s36, s36, 0x100
	s_addc_u32 s37, s37, 0
	s_cmp_gt_u32 s84, 61
	s_cbranch_scc0 .LBB0_2891
	s_add_u32 s36, s59, 0xffffff00
	s_addc_u32 s37, s81, -1
	s_andn2_b64 vcc, exec, s[42:43]
	s_cbranch_vccnz .LBB0_2894
	v_mov_b32_e32 v2, 0
	s_mov_b32 s20, s26
	s_mov_b32 s52, s28
	s_mov_b64 s[24:25], s[34:35]
	s_mov_b32 s68, s58
	v_mov_b32_e32 v3, v2
	v_mov_b32_e32 v4, v2
	v_mov_b32_e32 v5, v2
	v_mov_b32_e32 v6, v2
	v_mov_b32_e32 v7, v2
	v_mov_b32_e32 v8, v2
	v_mov_b32_e32 v9, v2
	v_mov_b32_e32 v18, v2
	v_mov_b32_e32 v19, v2
	v_mov_b32_e32 v20, v2
	v_mov_b32_e32 v21, v2
	v_mov_b32_e32 v22, v2
	v_mov_b32_e32 v23, v2
	v_mov_b32_e32 v24, v2
	v_mov_b32_e32 v25, v2
	v_mov_b32_e32 v34, v2
	v_mov_b32_e32 v35, v2
	v_mov_b32_e32 v36, v2
	v_mov_b32_e32 v37, v2
	v_mov_b32_e32 v38, v2
	v_mov_b32_e32 v39, v2
	v_mov_b32_e32 v40, v2
	v_mov_b32_e32 v41, v2
	v_mov_b32_e32 v50, v2
	v_mov_b32_e32 v51, v2
	v_mov_b32_e32 v52, v2
	v_mov_b32_e32 v53, v2
	v_mov_b32_e32 v54, v2
	v_mov_b32_e32 v55, v2
	v_mov_b32_e32 v56, v2
	v_mov_b32_e32 v57, v2
	v_mov_b32_e32 v10, v2
	v_mov_b32_e32 v11, v2
	v_mov_b32_e32 v12, v2
	v_mov_b32_e32 v13, v2
	v_mov_b32_e32 v14, v2
	v_mov_b32_e32 v15, v2
	v_mov_b32_e32 v16, v2
	v_mov_b32_e32 v17, v2
	v_mov_b32_e32 v26, v2
	v_mov_b32_e32 v27, v2
	v_mov_b32_e32 v28, v2
	v_mov_b32_e32 v29, v2
	v_mov_b32_e32 v30, v2
	v_mov_b32_e32 v31, v2
	v_mov_b32_e32 v32, v2
	v_mov_b32_e32 v33, v2
	v_mov_b32_e32 v42, v2
	v_mov_b32_e32 v43, v2
	v_mov_b32_e32 v44, v2
	v_mov_b32_e32 v45, v2
	v_mov_b32_e32 v46, v2
	v_mov_b32_e32 v47, v2
	v_mov_b32_e32 v48, v2
	v_mov_b32_e32 v49, v2
	v_mov_b32_e32 v58, v2
	v_mov_b32_e32 v59, v2
	v_mov_b32_e32 v60, v2
	v_mov_b32_e32 v61, v2
	v_mov_b32_e32 v62, v2
	v_mov_b32_e32 v63, v2
	v_mov_b32_e32 v64, v2
	v_mov_b32_e32 v65, v2
	v_mov_b32_e32 v66, v2
	v_mov_b32_e32 v67, v2
	v_mov_b32_e32 v68, v2
	v_mov_b32_e32 v69, v2
	v_mov_b32_e32 v70, v2
	v_mov_b32_e32 v71, v2
	v_mov_b32_e32 v72, v2
	v_mov_b32_e32 v73, v2
	v_mov_b32_e32 v82, v2
	v_mov_b32_e32 v83, v2
	v_mov_b32_e32 v84, v2
	v_mov_b32_e32 v85, v2
	v_mov_b32_e32 v86, v2
	v_mov_b32_e32 v87, v2
	v_mov_b32_e32 v88, v2
	v_mov_b32_e32 v89, v2
	v_mov_b32_e32 v98, v2
	v_mov_b32_e32 v99, v2
	v_mov_b32_e32 v100, v2
	v_mov_b32_e32 v101, v2
	v_mov_b32_e32 v102, v2
	v_mov_b32_e32 v103, v2
	v_mov_b32_e32 v104, v2
	v_mov_b32_e32 v105, v2
	v_mov_b32_e32 v114, v2
	v_mov_b32_e32 v115, v2
	v_mov_b32_e32 v116, v2
	v_mov_b32_e32 v117, v2
	v_mov_b32_e32 v118, v2
	v_mov_b32_e32 v119, v2
	v_mov_b32_e32 v120, v2
	v_mov_b32_e32 v121, v2
	v_mov_b32_e32 v74, v2
	v_mov_b32_e32 v75, v2
	v_mov_b32_e32 v76, v2
	v_mov_b32_e32 v77, v2
	v_mov_b32_e32 v78, v2
	v_mov_b32_e32 v79, v2
	v_mov_b32_e32 v80, v2
	v_mov_b32_e32 v81, v2
	v_mov_b32_e32 v90, v2
	v_mov_b32_e32 v91, v2
	v_mov_b32_e32 v92, v2
	v_mov_b32_e32 v93, v2
	v_mov_b32_e32 v94, v2
	v_mov_b32_e32 v95, v2
	v_mov_b32_e32 v96, v2
	v_mov_b32_e32 v97, v2
	v_mov_b32_e32 v106, v2
	v_mov_b32_e32 v107, v2
	v_mov_b32_e32 v108, v2
	v_mov_b32_e32 v109, v2
	v_mov_b32_e32 v110, v2
	v_mov_b32_e32 v111, v2
	v_mov_b32_e32 v112, v2
	v_mov_b32_e32 v113, v2
	v_mov_b32_e32 v130, v2
	v_mov_b32_e32 v131, v2
	v_mov_b32_e32 v132, v2
	v_mov_b32_e32 v133, v2
	v_mov_b32_e32 v134, v2
	v_mov_b32_e32 v135, v2
	v_mov_b32_e32 v136, v2
	v_mov_b32_e32 v137, v2
	s_movk_i32 s92, 0x2b20
	s_andn2_b64 vcc, exec, s[40:41]
	s_cbranch_vccnz .LBB0_2895
	s_branch .LBB0_2896

.LBB0_2982:
	s_add_u32 s42, s24, s36
	s_addc_u32 s43, s25, s37
	s_add_u32 s42, s42, 0x100
	s_addc_u32 s43, s43, 0
	s_add_u32 s50, s59, s36
	s_addc_u32 s64, s79, s37
	s_add_i32 s65, 0, 0x10000
	s_cmpk_eq_i32 s36, 0x1f00
	s_cselect_b32 s45, s29, s43
	s_cselect_b32 s44, s80, s42
	s_cselect_b32 s43, s27, s64
	s_cselect_b32 s42, s81, s50
	s_add_i32 s50, 0, 0x14000
	v_lshl_add_u64 v[208:209], v[144:145], 0, s[36:37]
	s_add_i32 m0, s4, 0xc000
	s_nop 0
	global_load_lds_dwordx4 v[208:209], off
	s_add_i32 m0, s4, 0xe000
	v_lshl_add_u64 v[208:209], v[142:143], 0, s[36:37]
	global_load_lds_dwordx4 v[208:209], off
	ds_read_b128 v[148:151], v225
	ds_read_b128 v[152:155], v225 offset:1024
	ds_read_b128 v[156:159], v225 offset:2048
	ds_read_b128 v[160:163], v225 offset:3072
	ds_read_b128 v[164:167], v225 offset:16384
	ds_read_b128 v[168:171], v225 offset:17408
	ds_read_b128 v[172:175], v225 offset:18432
	ds_read_b128 v[176:179], v225 offset:19456
	ds_read_b128 v[180:183], v147
	ds_read_b128 v[184:187], v147 offset:1024
	ds_read_b128 v[188:191], v147 offset:2048
	ds_read_b128 v[192:195], v147 offset:3072
	ds_read_b128 v[196:199], v147 offset:4096
	ds_read_b128 v[200:203], v147 offset:5120
	ds_read_b128 v[204:207], v147 offset:6144
	ds_read_b128 v[216:219], v147 offset:7168
	s_waitcnt vmcnt(8) lgkmcnt(0)
	s_barrier
	v_mfma_f32_16x16x32_bf16 v[134:137], v[148:151], v[180:183], v[134:137]
	v_mfma_f32_16x16x32_bf16 v[130:133], v[156:159], v[180:183], v[130:133]
	v_mfma_f32_16x16x32_bf16 v[110:113], v[148:151], v[188:191], v[110:113]
	v_mfma_f32_16x16x32_bf16 v[106:109], v[156:159], v[188:191], v[106:109]
	v_mfma_f32_16x16x32_bf16 v[94:97], v[148:151], v[196:199], v[94:97]
	v_mfma_f32_16x16x32_bf16 v[90:93], v[156:159], v[196:199], v[90:93]
	v_mfma_f32_16x16x32_bf16 v[78:81], v[148:151], v[204:207], v[78:81]
	v_mfma_f32_16x16x32_bf16 v[74:77], v[156:159], v[204:207], v[74:77]
	v_mfma_f32_16x16x32_bf16 v[134:137], v[152:155], v[184:187], v[134:137]
	v_mfma_f32_16x16x32_bf16 v[130:133], v[160:163], v[184:187], v[130:133]
	v_mfma_f32_16x16x32_bf16 v[110:113], v[152:155], v[192:195], v[110:113]
	v_mfma_f32_16x16x32_bf16 v[106:109], v[160:163], v[192:195], v[106:109]
	v_mfma_f32_16x16x32_bf16 v[94:97], v[152:155], v[200:203], v[94:97]
	v_mfma_f32_16x16x32_bf16 v[90:93], v[160:163], v[200:203], v[90:93]
	v_mfma_f32_16x16x32_bf16 v[78:81], v[152:155], v[216:219], v[78:81]
	v_mfma_f32_16x16x32_bf16 v[74:77], v[160:163], v[216:219], v[74:77]
	v_mfma_f32_16x16x32_bf16 v[118:121], v[164:167], v[180:183], v[118:121]
	v_mfma_f32_16x16x32_bf16 v[114:117], v[172:175], v[180:183], v[114:117]
	v_mfma_f32_16x16x32_bf16 v[102:105], v[164:167], v[188:191], v[102:105]
	v_mfma_f32_16x16x32_bf16 v[98:101], v[172:175], v[188:191], v[98:101]
	v_mfma_f32_16x16x32_bf16 v[86:89], v[164:167], v[196:199], v[86:89]
	v_mfma_f32_16x16x32_bf16 v[82:85], v[172:175], v[196:199], v[82:85]
	v_mfma_f32_16x16x32_bf16 v[70:73], v[164:167], v[204:207], v[70:73]
	v_mfma_f32_16x16x32_bf16 v[66:69], v[172:175], v[204:207], v[66:69]
	v_mfma_f32_16x16x32_bf16 v[118:121], v[168:171], v[184:187], v[118:121]
	v_mfma_f32_16x16x32_bf16 v[114:117], v[176:179], v[184:187], v[114:117]
	v_mfma_f32_16x16x32_bf16 v[102:105], v[168:171], v[192:195], v[102:105]
	v_mfma_f32_16x16x32_bf16 v[98:101], v[176:179], v[192:195], v[98:101]
	v_mfma_f32_16x16x32_bf16 v[86:89], v[168:171], v[200:203], v[86:89]
	v_mfma_f32_16x16x32_bf16 v[82:85], v[176:179], v[200:203], v[82:85]
	v_mfma_f32_16x16x32_bf16 v[70:73], v[168:171], v[216:219], v[70:73]
	v_mfma_f32_16x16x32_bf16 v[66:69], v[176:179], v[216:219], v[66:69]
	s_barrier
	s_add_i32 s64, s65, s63
	v_lshl_add_u64 v[208:209], s[42:43], 0, v[126:127]
	s_mov_b32 m0, s64
	s_nop 0
	global_load_lds_dwordx4 v126, s[42:43]
	s_add_i32 m0, s64, 0x2000
	s_add_u32 s84, s42, 0x100000
	v_lshl_add_u64 v[220:221], s[42:43], 0, v[122:123]
	s_addc_u32 s85, s43, 0
	s_add_i32 s50, s50, s63
	global_load_lds_dwordx4 v122, s[42:43]
	s_mov_b32 m0, s50
	v_lshl_add_u64 v[240:241], s[44:45], 0, v[124:125]
	global_load_lds_dwordx4 v126, s[84:85]
	s_add_i32 m0, s50, 0x2000
	s_nop 0
	global_load_lds_dwordx4 v122, s[84:85]
	s_mov_b32 m0, s4
	v_lshl_add_u64 v[222:223], s[44:45], 0, v[128:129]
	global_load_lds_dwordx4 v128, s[44:45]
	s_mov_b32 m0, s33
	s_nop 0
	global_load_lds_dwordx4 v124, s[44:45]
	ds_read_b128 v[180:183], v147 offset:16384
	ds_read_b128 v[184:187], v147 offset:17408
	ds_read_b128 v[188:191], v147 offset:18432
	ds_read_b128 v[192:195], v147 offset:19456
	ds_read_b128 v[196:199], v147 offset:20480
	ds_read_b128 v[200:203], v147 offset:21504
	ds_read_b128 v[204:207], v147 offset:22528
	ds_read_b128 v[216:219], v147 offset:23552
	s_waitcnt vmcnt(8) lgkmcnt(0)
	s_barrier
	v_mfma_f32_16x16x32_bf16 v[62:65], v[148:151], v[180:183], v[62:65]
	v_mfma_f32_16x16x32_bf16 v[58:61], v[156:159], v[180:183], v[58:61]
	v_mfma_f32_16x16x32_bf16 v[46:49], v[148:151], v[188:191], v[46:49]
	v_mfma_f32_16x16x32_bf16 v[42:45], v[156:159], v[188:191], v[42:45]
	v_mfma_f32_16x16x32_bf16 v[30:33], v[148:151], v[196:199], v[30:33]
	v_mfma_f32_16x16x32_bf16 v[26:29], v[156:159], v[196:199], v[26:29]
	v_mfma_f32_16x16x32_bf16 v[14:17], v[148:151], v[204:207], v[14:17]
	v_mfma_f32_16x16x32_bf16 v[10:13], v[156:159], v[204:207], v[10:13]
	v_mfma_f32_16x16x32_bf16 v[62:65], v[152:155], v[184:187], v[62:65]
	v_mfma_f32_16x16x32_bf16 v[58:61], v[160:163], v[184:187], v[58:61]
	v_mfma_f32_16x16x32_bf16 v[46:49], v[152:155], v[192:195], v[46:49]
	v_mfma_f32_16x16x32_bf16 v[42:45], v[160:163], v[192:195], v[42:45]
	v_mfma_f32_16x16x32_bf16 v[30:33], v[152:155], v[200:203], v[30:33]
	v_mfma_f32_16x16x32_bf16 v[26:29], v[160:163], v[200:203], v[26:29]
	v_mfma_f32_16x16x32_bf16 v[14:17], v[152:155], v[216:219], v[14:17]
	v_mfma_f32_16x16x32_bf16 v[10:13], v[160:163], v[216:219], v[10:13]
	v_mfma_f32_16x16x32_bf16 v[54:57], v[164:167], v[180:183], v[54:57]
	v_mfma_f32_16x16x32_bf16 v[50:53], v[172:175], v[180:183], v[50:53]
	v_mfma_f32_16x16x32_bf16 v[38:41], v[164:167], v[188:191], v[38:41]
	v_mfma_f32_16x16x32_bf16 v[34:37], v[172:175], v[188:191], v[34:37]
	v_mfma_f32_16x16x32_bf16 v[22:25], v[164:167], v[196:199], v[22:25]
	v_mfma_f32_16x16x32_bf16 v[18:21], v[172:175], v[196:199], v[18:21]
	v_mfma_f32_16x16x32_bf16 v[6:9], v[164:167], v[204:207], v[6:9]
	v_mfma_f32_16x16x32_bf16 v[2:5], v[172:175], v[204:207], v[2:5]
	v_mfma_f32_16x16x32_bf16 v[54:57], v[168:171], v[184:187], v[54:57]
	v_mfma_f32_16x16x32_bf16 v[50:53], v[176:179], v[184:187], v[50:53]
	v_mfma_f32_16x16x32_bf16 v[38:41], v[168:171], v[192:195], v[38:41]
	v_mfma_f32_16x16x32_bf16 v[34:37], v[176:179], v[192:195], v[34:37]
	v_mfma_f32_16x16x32_bf16 v[22:25], v[168:171], v[200:203], v[22:25]
	v_mfma_f32_16x16x32_bf16 v[18:21], v[176:179], v[200:203], v[18:21]
	v_mfma_f32_16x16x32_bf16 v[6:9], v[168:171], v[216:219], v[6:9]
	v_mfma_f32_16x16x32_bf16 v[2:5], v[176:179], v[216:219], v[2:5]
	s_barrier
	s_add_i32 s50, 0, 0x18000
	s_add_i32 s64, 0, 0x1c000
	s_add_u32 s44, s44, 0x100000
	s_addc_u32 s45, s45, 0
	s_mov_b32 m0, s70
	s_nop 0
	global_load_lds_dwordx4 v128, s[44:45]
	s_mov_b32 m0, s71
	v_lshl_add_u64 v[242:243], s[44:45], 0, v[124:125]
	global_load_lds_dwordx4 v124, s[44:45]
	ds_read_b128 v[148:151], v225 offset:32768
	ds_read_b128 v[152:155], v225 offset:33792
	ds_read_b128 v[156:159], v225 offset:34816
	ds_read_b128 v[160:163], v225 offset:35840
	ds_read_b128 v[164:167], v225 offset:49152
	ds_read_b128 v[168:171], v225 offset:50176
	ds_read_b128 v[172:175], v225 offset:51200
	ds_read_b128 v[176:179], v225 offset:52224
	ds_read_b128 v[180:183], v147 offset:32768
	ds_read_b128 v[184:187], v147 offset:33792
	ds_read_b128 v[188:191], v147 offset:34816
	ds_read_b128 v[192:195], v147 offset:35840
	ds_read_b128 v[196:199], v147 offset:36864
	ds_read_b128 v[200:203], v147 offset:37888
	ds_read_b128 v[204:207], v147 offset:38912
	ds_read_b128 v[216:219], v147 offset:39936
	s_waitcnt vmcnt(8) lgkmcnt(0)
	s_barrier
	v_mfma_f32_16x16x32_bf16 v[134:137], v[148:151], v[180:183], v[134:137]
	v_mfma_f32_16x16x32_bf16 v[130:133], v[156:159], v[180:183], v[130:133]
	v_mfma_f32_16x16x32_bf16 v[110:113], v[148:151], v[188:191], v[110:113]
	v_mfma_f32_16x16x32_bf16 v[106:109], v[156:159], v[188:191], v[106:109]
	v_mfma_f32_16x16x32_bf16 v[94:97], v[148:151], v[196:199], v[94:97]
	v_mfma_f32_16x16x32_bf16 v[90:93], v[156:159], v[196:199], v[90:93]
	v_mfma_f32_16x16x32_bf16 v[78:81], v[148:151], v[204:207], v[78:81]
	v_mfma_f32_16x16x32_bf16 v[74:77], v[156:159], v[204:207], v[74:77]
	v_mfma_f32_16x16x32_bf16 v[134:137], v[152:155], v[184:187], v[134:137]
	v_mfma_f32_16x16x32_bf16 v[130:133], v[160:163], v[184:187], v[130:133]
	v_mfma_f32_16x16x32_bf16 v[110:113], v[152:155], v[192:195], v[110:113]
	v_mfma_f32_16x16x32_bf16 v[106:109], v[160:163], v[192:195], v[106:109]
	v_mfma_f32_16x16x32_bf16 v[94:97], v[152:155], v[200:203], v[94:97]
	v_mfma_f32_16x16x32_bf16 v[90:93], v[160:163], v[200:203], v[90:93]
	v_mfma_f32_16x16x32_bf16 v[78:81], v[152:155], v[216:219], v[78:81]
	v_mfma_f32_16x16x32_bf16 v[74:77], v[160:163], v[216:219], v[74:77]
	v_mfma_f32_16x16x32_bf16 v[118:121], v[164:167], v[180:183], v[118:121]
	v_mfma_f32_16x16x32_bf16 v[114:117], v[172:175], v[180:183], v[114:117]
	v_mfma_f32_16x16x32_bf16 v[102:105], v[164:167], v[188:191], v[102:105]
	v_mfma_f32_16x16x32_bf16 v[98:101], v[172:175], v[188:191], v[98:101]
	v_mfma_f32_16x16x32_bf16 v[86:89], v[164:167], v[196:199], v[86:89]
	v_mfma_f32_16x16x32_bf16 v[82:85], v[172:175], v[196:199], v[82:85]
	v_mfma_f32_16x16x32_bf16 v[70:73], v[164:167], v[204:207], v[70:73]
	v_mfma_f32_16x16x32_bf16 v[66:69], v[172:175], v[204:207], v[66:69]
	v_mfma_f32_16x16x32_bf16 v[118:121], v[168:171], v[184:187], v[118:121]
	v_mfma_f32_16x16x32_bf16 v[114:117], v[176:179], v[184:187], v[114:117]
	v_mfma_f32_16x16x32_bf16 v[102:105], v[168:171], v[192:195], v[102:105]
	v_mfma_f32_16x16x32_bf16 v[98:101], v[176:179], v[192:195], v[98:101]
	v_mfma_f32_16x16x32_bf16 v[86:89], v[168:171], v[200:203], v[86:89]
	v_mfma_f32_16x16x32_bf16 v[82:85], v[176:179], v[200:203], v[82:85]
	v_mfma_f32_16x16x32_bf16 v[70:73], v[168:171], v[216:219], v[70:73]
	v_mfma_f32_16x16x32_bf16 v[66:69], v[176:179], v[216:219], v[66:69]
	s_barrier
	s_add_i32 s44, s50, s63
	v_lshl_add_u64 v[208:209], v[208:209], 0, s[56:57]
	s_mov_b32 m0, s44
	s_nop 0
	global_load_lds_dwordx4 v[208:209], off
	s_add_i32 m0, s44, 0x2000
	s_add_u32 s42, s42, 0x100080
	v_lshl_add_u64 v[208:209], v[220:221], 0, s[56:57]
	s_addc_u32 s43, s43, 0
	s_add_i32 s44, s64, s63
	global_load_lds_dwordx4 v[208:209], off
	s_mov_b32 m0, s44
	s_nop 0
	global_load_lds_dwordx4 v126, s[42:43]
	s_add_i32 m0, s44, 0x2000
	s_nop 0
	global_load_lds_dwordx4 v122, s[42:43]
	s_mov_b32 m0, s76
	v_lshl_add_u64 v[208:209], v[222:223], 0, s[56:57]
	global_load_lds_dwordx4 v[208:209], off
	s_mov_b32 m0, s77
	v_lshl_add_u64 v[208:209], v[240:241], 0, s[56:57]
	global_load_lds_dwordx4 v[208:209], off
	ds_read_b128 v[180:183], v147 offset:49152
	ds_read_b128 v[184:187], v147 offset:50176
	ds_read_b128 v[188:191], v147 offset:51200
	ds_read_b128 v[192:195], v147 offset:52224
	ds_read_b128 v[196:199], v147 offset:53248
	ds_read_b128 v[200:203], v147 offset:54272
	ds_read_b128 v[204:207], v147 offset:55296
	ds_read_b128 v[216:219], v147 offset:56320
	s_waitcnt vmcnt(8) lgkmcnt(0)
	s_barrier
	v_mfma_f32_16x16x32_bf16 v[62:65], v[148:151], v[180:183], v[62:65]
	v_mfma_f32_16x16x32_bf16 v[58:61], v[156:159], v[180:183], v[58:61]
	v_mfma_f32_16x16x32_bf16 v[46:49], v[148:151], v[188:191], v[46:49]
	v_mfma_f32_16x16x32_bf16 v[42:45], v[156:159], v[188:191], v[42:45]
	v_mfma_f32_16x16x32_bf16 v[30:33], v[148:151], v[196:199], v[30:33]
	v_mfma_f32_16x16x32_bf16 v[26:29], v[156:159], v[196:199], v[26:29]
	v_mfma_f32_16x16x32_bf16 v[14:17], v[148:151], v[204:207], v[14:17]
	v_mfma_f32_16x16x32_bf16 v[10:13], v[156:159], v[204:207], v[10:13]
	v_mfma_f32_16x16x32_bf16 v[62:65], v[152:155], v[184:187], v[62:65]
	v_mfma_f32_16x16x32_bf16 v[58:61], v[160:163], v[184:187], v[58:61]
	v_mfma_f32_16x16x32_bf16 v[46:49], v[152:155], v[192:195], v[46:49]
	v_mfma_f32_16x16x32_bf16 v[42:45], v[160:163], v[192:195], v[42:45]
	v_mfma_f32_16x16x32_bf16 v[30:33], v[152:155], v[200:203], v[30:33]
	v_mfma_f32_16x16x32_bf16 v[26:29], v[160:163], v[200:203], v[26:29]
	v_mfma_f32_16x16x32_bf16 v[14:17], v[152:155], v[216:219], v[14:17]
	v_mfma_f32_16x16x32_bf16 v[10:13], v[160:163], v[216:219], v[10:13]
	v_mfma_f32_16x16x32_bf16 v[54:57], v[164:167], v[180:183], v[54:57]
	v_mfma_f32_16x16x32_bf16 v[50:53], v[172:175], v[180:183], v[50:53]
	v_mfma_f32_16x16x32_bf16 v[38:41], v[164:167], v[188:191], v[38:41]
	v_mfma_f32_16x16x32_bf16 v[34:37], v[172:175], v[188:191], v[34:37]
	v_mfma_f32_16x16x32_bf16 v[22:25], v[164:167], v[196:199], v[22:25]
	v_mfma_f32_16x16x32_bf16 v[18:21], v[172:175], v[196:199], v[18:21]
	v_mfma_f32_16x16x32_bf16 v[6:9], v[164:167], v[204:207], v[6:9]
	v_mfma_f32_16x16x32_bf16 v[2:5], v[172:175], v[204:207], v[2:5]
	v_mfma_f32_16x16x32_bf16 v[54:57], v[168:171], v[184:187], v[54:57]
	v_mfma_f32_16x16x32_bf16 v[50:53], v[176:179], v[184:187], v[50:53]
	v_mfma_f32_16x16x32_bf16 v[38:41], v[168:171], v[192:195], v[38:41]
	v_mfma_f32_16x16x32_bf16 v[34:37], v[176:179], v[192:195], v[34:37]
	v_mfma_f32_16x16x32_bf16 v[22:25], v[168:171], v[200:203], v[22:25]
	v_mfma_f32_16x16x32_bf16 v[18:21], v[176:179], v[200:203], v[18:21]
	v_mfma_f32_16x16x32_bf16 v[6:9], v[168:171], v[216:219], v[6:9]
	v_mfma_f32_16x16x32_bf16 v[2:5], v[176:179], v[216:219], v[2:5]
	s_barrier
	s_add_i32 s82, s82, 2
	s_add_u32 s36, s36, 0x100
	s_addc_u32 s37, s37, 0
	s_cmp_gt_u32 s82, 61
	s_cbranch_scc0 .LBB0_2982
	s_add_u32 s36, s59, 0xffffff00
	s_addc_u32 s37, s79, -1
	s_andn2_b64 vcc, exec, s[40:41]
	s_cbranch_vccnz .LBB0_2985
	v_mov_b32_e32 v2, 0
	s_mov_b32 s20, s26
	s_mov_b32 s78, s28
	s_mov_b64 s[24:25], s[34:35]
	s_mov_b32 s68, s58
	v_mov_b32_e32 v3, v2
	v_mov_b32_e32 v4, v2
	v_mov_b32_e32 v5, v2
	v_mov_b32_e32 v6, v2
	v_mov_b32_e32 v7, v2
	v_mov_b32_e32 v8, v2
	v_mov_b32_e32 v9, v2
	v_mov_b32_e32 v18, v2
	v_mov_b32_e32 v19, v2
	v_mov_b32_e32 v20, v2
	v_mov_b32_e32 v21, v2
	v_mov_b32_e32 v22, v2
	v_mov_b32_e32 v23, v2
	v_mov_b32_e32 v24, v2
	v_mov_b32_e32 v25, v2
	v_mov_b32_e32 v34, v2
	v_mov_b32_e32 v35, v2
	v_mov_b32_e32 v36, v2
	v_mov_b32_e32 v37, v2
	v_mov_b32_e32 v38, v2
	v_mov_b32_e32 v39, v2
	v_mov_b32_e32 v40, v2
	v_mov_b32_e32 v41, v2
	v_mov_b32_e32 v50, v2
	v_mov_b32_e32 v51, v2
	v_mov_b32_e32 v52, v2
	v_mov_b32_e32 v53, v2
	v_mov_b32_e32 v54, v2
	v_mov_b32_e32 v55, v2
	v_mov_b32_e32 v56, v2
	v_mov_b32_e32 v57, v2
	v_mov_b32_e32 v10, v2
	v_mov_b32_e32 v11, v2
	v_mov_b32_e32 v12, v2
	v_mov_b32_e32 v13, v2
	v_mov_b32_e32 v14, v2
	v_mov_b32_e32 v15, v2
	v_mov_b32_e32 v16, v2
	v_mov_b32_e32 v17, v2
	v_mov_b32_e32 v26, v2
	v_mov_b32_e32 v27, v2
	v_mov_b32_e32 v28, v2
	v_mov_b32_e32 v29, v2
	v_mov_b32_e32 v30, v2
	v_mov_b32_e32 v31, v2
	v_mov_b32_e32 v32, v2
	v_mov_b32_e32 v33, v2
	v_mov_b32_e32 v42, v2
	v_mov_b32_e32 v43, v2
	v_mov_b32_e32 v44, v2
	v_mov_b32_e32 v45, v2
	v_mov_b32_e32 v46, v2
	v_mov_b32_e32 v47, v2
	v_mov_b32_e32 v48, v2
	v_mov_b32_e32 v49, v2
	v_mov_b32_e32 v58, v2
	v_mov_b32_e32 v59, v2
	v_mov_b32_e32 v60, v2
	v_mov_b32_e32 v61, v2
	v_mov_b32_e32 v62, v2
	v_mov_b32_e32 v63, v2
	v_mov_b32_e32 v64, v2
	v_mov_b32_e32 v65, v2
	v_mov_b32_e32 v66, v2
	v_mov_b32_e32 v67, v2
	v_mov_b32_e32 v68, v2
	v_mov_b32_e32 v69, v2
	v_mov_b32_e32 v70, v2
	v_mov_b32_e32 v71, v2
	v_mov_b32_e32 v72, v2
	v_mov_b32_e32 v73, v2
	v_mov_b32_e32 v82, v2
	v_mov_b32_e32 v83, v2
	v_mov_b32_e32 v84, v2
	v_mov_b32_e32 v85, v2
	v_mov_b32_e32 v86, v2
	v_mov_b32_e32 v87, v2
	v_mov_b32_e32 v88, v2
	v_mov_b32_e32 v89, v2
	v_mov_b32_e32 v98, v2
	v_mov_b32_e32 v99, v2
	v_mov_b32_e32 v100, v2
	v_mov_b32_e32 v101, v2
	v_mov_b32_e32 v102, v2
	v_mov_b32_e32 v103, v2
	v_mov_b32_e32 v104, v2
	v_mov_b32_e32 v105, v2
	v_mov_b32_e32 v114, v2
	v_mov_b32_e32 v115, v2
	v_mov_b32_e32 v116, v2
	v_mov_b32_e32 v117, v2
	v_mov_b32_e32 v118, v2
	v_mov_b32_e32 v119, v2
	v_mov_b32_e32 v120, v2
	v_mov_b32_e32 v121, v2
	v_mov_b32_e32 v74, v2
	v_mov_b32_e32 v75, v2
	v_mov_b32_e32 v76, v2
	v_mov_b32_e32 v77, v2
	v_mov_b32_e32 v78, v2
	v_mov_b32_e32 v79, v2
	v_mov_b32_e32 v80, v2
	v_mov_b32_e32 v81, v2
	v_mov_b32_e32 v90, v2
	v_mov_b32_e32 v91, v2
	v_mov_b32_e32 v92, v2
	v_mov_b32_e32 v93, v2
	v_mov_b32_e32 v94, v2
	v_mov_b32_e32 v95, v2
	v_mov_b32_e32 v96, v2
	v_mov_b32_e32 v97, v2
	v_mov_b32_e32 v106, v2
	v_mov_b32_e32 v107, v2
	v_mov_b32_e32 v108, v2
	v_mov_b32_e32 v109, v2
	v_mov_b32_e32 v110, v2
	v_mov_b32_e32 v111, v2
	v_mov_b32_e32 v112, v2
	v_mov_b32_e32 v113, v2
	v_mov_b32_e32 v130, v2
	v_mov_b32_e32 v131, v2
	v_mov_b32_e32 v132, v2
	v_mov_b32_e32 v133, v2
	v_mov_b32_e32 v134, v2
	v_mov_b32_e32 v135, v2
	v_mov_b32_e32 v136, v2
	v_mov_b32_e32 v137, v2
	s_andn2_b64 vcc, exec, s[38:39]
	s_cbranch_vccnz .LBB0_2986
	s_branch .LBB0_2987
